# hand-written DSA indexer phase: pipelined score tiles, VALU-counted top-256 search
# speedup vs baseline: 1.0109x; 1.0109x over previous
.LBB0_939:
	s_getreg_b32 s0, hwreg(HW_REG_HW_ID, 0, 6)
	s_and_b32 s0, s0, 63
	s_lshl_b32 s0, s0, 2
	s_or_b32 s0, s0, 0x20400
	v_mov_b32_e32 v0, s0
	ds_read_b32 v2, v0
	v_mbcnt_lo_u32_b32 v0, -1, 0
	v_mbcnt_hi_u32_b32 v0, -1, v0
	s_waitcnt lgkmcnt(0)
	v_readfirstlane_b32 s0, v2
	s_nop 1
	v_lshl_or_b32 v2, s0, 6, v0
	s_nop 0
	v_readfirstlane_b32 s0, v2
	s_ashr_i32 s0, s0, 6
	s_add_i32 s81, s0, s4
	s_movk_i32 s0, 0xb0
	s_cmpk_gt_i32 s81, 0xfff
	s_cbranch_scc1 .LBB0_938
	v_writelane_b32 v255, s3, 45
	v_readlane_b32 s2, v254, 0
	v_readlane_b32 s3, v254, 1
	s_load_dwordx2 s[0:1], s[2:3], s0 offset:0x0
	v_and_b32_e32 v50, 31, v0
	v_lshrrev_b32_e32 v51, 5, v0
	v_bfe_u32 v52, v0, 2, 1
	v_and_b32_e32 v53, 3, v0
	v_lshrrev_b32_e32 v54, 1, v0
	v_and_or_b32 v53, v54, 12, v53
	v_mov_b32_e32 v54, 0x2200
	v_mul_u32_u24_e32 v55, v52, v54
	v_lshl_add_u32 v55, v53, 7, v55
	v_lshl_add_u32 v55, v51, 4, v55
	v_add_u32_e32 v55, 0x1800, v55
	v_mul_u32_u24_e32 v56, v51, v54
	v_add_u32_e32 v56, 0x2080, v56
	v_lshlrev_b32_e32 v57, 4, v0
	v_lshlrev_b32_e32 v58, 2, v0
	v_mov_b32_e32 v61, 0xff800000
	s_waitcnt lgkmcnt(0)
	s_add_u32 s4, s0, 0x3a600000
	s_addc_u32 s5, s1, 0
	s_add_u32 s6, s0, 0x4e100000
	s_addc_u32 s7, s1, 0
	s_add_u32 s8, s0, 0x4be00000
	s_addc_u32 s9, s1, 0
	s_mov_b32 s10, 0
.Lidx_id:
	s_and_b32 s11, s81, 0x3ff
	s_lshr_b32 s12, s81, 10
	s_sub_i32 s13, 0x3ff, s11
	s_bitcmp1_b32 s10, 0
	s_cselect_b32 s11, s13, s11
	s_lshl_b32 s13, s11, 1
	s_lshl_b32 s14, s12, 11
	s_or_b32 s14, s14, s13
	s_add_i32 s15, s13, 1
	s_lshr_b32 s15, s15, 5
	s_add_i32 s15, s15, 1
	s_add_i32 s16, s15, 7
	s_lshr_b32 s16, s16, 3
	s_mul_i32 s17, s14, 0x2200
	s_mul_hi_u32 s25, s14, 0x2200
	s_add_u32 s18, s4, s17
	s_addc_u32 s19, s5, s25
	s_lshl_b32 s17, s12, 18
	s_add_u32 s20, s6, s17
	s_addc_u32 s21, s7, 0
	s_lshl_b32 s17, s14, 8
	s_add_u32 s22, s8, s17
	s_addc_u32 s23, s9, 0
	global_load_dwordx4 v[128:131], v55, s[18:19]
	global_load_dwordx4 v[132:135], v55, s[18:19] offset:32
	global_load_dwordx4 v[136:139], v55, s[18:19] offset:64
	global_load_dwordx4 v[140:143], v55, s[18:19] offset:96
	global_load_dwordx4 v[192:195], v56, s[18:19]
	global_load_dwordx4 v[196:199], v56, s[18:19] offset:16
	global_load_dwordx4 v[2:5], v57, s[20:21]
	global_load_dwordx4 v[6:9], v57, s[20:21] offset:1024
	global_load_dwordx4 v[10:13], v57, s[20:21] offset:2048
	global_load_dwordx4 v[14:17], v57, s[20:21] offset:3072
	s_add_u32 s20, s20, 0x1000
	s_addc_u32 s21, s21, 0
	global_load_dwordx4 v[18:21], v57, s[20:21]
	global_load_dwordx4 v[22:25], v57, s[20:21] offset:1024
	global_load_dwordx4 v[26:29], v57, s[20:21] offset:2048
	global_load_dwordx4 v[30:33], v57, s[20:21] offset:3072
	s_add_u32 s20, s20, 0x1000
	s_addc_u32 s21, s21, 0
	v_sub_u32_e32 v59, v51, v50
	v_add_u32_e32 v59, s13, v59
	v_mov_b32_e32 v60, 0x7fffff
	v_mov_b32_e32 v64, v60
	v_mov_b32_e32 v65, v60
	v_mov_b32_e32 v66, v60
	v_mov_b32_e32 v67, v60
	v_mov_b32_e32 v68, v60
	v_mov_b32_e32 v69, v60
	v_mov_b32_e32 v70, v60
	v_mov_b32_e32 v71, v60
	v_mov_b32_e32 v72, v60
	v_mov_b32_e32 v73, v60
	v_mov_b32_e32 v74, v60
	v_mov_b32_e32 v75, v60
	v_mov_b32_e32 v76, v60
	v_mov_b32_e32 v77, v60
	v_mov_b32_e32 v78, v60
	v_mov_b32_e32 v79, v60
	v_mov_b32_e32 v80, v60
	v_mov_b32_e32 v81, v60
	v_mov_b32_e32 v82, v60
	v_mov_b32_e32 v83, v60
	v_mov_b32_e32 v84, v60
	v_mov_b32_e32 v85, v60
	v_mov_b32_e32 v86, v60
	v_mov_b32_e32 v87, v60
	v_mov_b32_e32 v88, v60
	v_mov_b32_e32 v89, v60
	v_mov_b32_e32 v90, v60
	v_mov_b32_e32 v91, v60
	v_mov_b32_e32 v92, v60
	v_mov_b32_e32 v93, v60
	v_mov_b32_e32 v94, v60
	v_mov_b32_e32 v95, v60
	v_mov_b32_e32 v96, v60
	v_mov_b32_e32 v97, v60
	v_mov_b32_e32 v98, v60
	v_mov_b32_e32 v99, v60
	v_mov_b32_e32 v100, v60
	v_mov_b32_e32 v101, v60
	v_mov_b32_e32 v102, v60
	v_mov_b32_e32 v103, v60
	v_mov_b32_e32 v104, v60
	v_mov_b32_e32 v105, v60
	v_mov_b32_e32 v106, v60
	v_mov_b32_e32 v107, v60
	v_mov_b32_e32 v108, v60
	v_mov_b32_e32 v109, v60
	v_mov_b32_e32 v110, v60
	v_mov_b32_e32 v111, v60
	v_mov_b32_e32 v112, v60
	v_mov_b32_e32 v113, v60
	v_mov_b32_e32 v114, v60
	v_mov_b32_e32 v115, v60
	v_mov_b32_e32 v116, v60
	v_mov_b32_e32 v117, v60
	v_mov_b32_e32 v118, v60
	v_mov_b32_e32 v119, v60
	v_mov_b32_e32 v120, v60
	v_mov_b32_e32 v121, v60
	v_mov_b32_e32 v122, v60
	v_mov_b32_e32 v123, v60
	v_mov_b32_e32 v124, v60
	v_mov_b32_e32 v125, v60
	v_mov_b32_e32 v126, v60
	v_mov_b32_e32 v127, v60
	s_waitcnt vmcnt(8)
	v_lshlrev_b32_e32 v204, 16, v192
	v_and_b32_e32 v208, 0xffff0000, v192
	v_mul_f32_e32 v144, 0x3d000000, v204
	v_mul_f32_e32 v145, 0x3d000000, v208
	v_lshlrev_b32_e32 v204, 16, v193
	v_and_b32_e32 v208, 0xffff0000, v193
	v_mul_f32_e32 v146, 0x3d000000, v204
	v_mul_f32_e32 v147, 0x3d000000, v208
	v_lshlrev_b32_e32 v204, 16, v194
	v_and_b32_e32 v208, 0xffff0000, v194
	v_mul_f32_e32 v148, 0x3d000000, v204
	v_mul_f32_e32 v149, 0x3d000000, v208
	v_lshlrev_b32_e32 v204, 16, v195
	v_and_b32_e32 v208, 0xffff0000, v195
	v_mul_f32_e32 v150, 0x3d000000, v204
	v_mul_f32_e32 v151, 0x3d000000, v208
	v_lshlrev_b32_e32 v204, 16, v196
	v_and_b32_e32 v208, 0xffff0000, v196
	v_mul_f32_e32 v152, 0x3d000000, v204
	v_mul_f32_e32 v153, 0x3d000000, v208
	v_lshlrev_b32_e32 v204, 16, v197
	v_and_b32_e32 v208, 0xffff0000, v197
	v_mul_f32_e32 v154, 0x3d000000, v204
	v_mul_f32_e32 v155, 0x3d000000, v208
	v_lshlrev_b32_e32 v204, 16, v198
	v_and_b32_e32 v208, 0xffff0000, v198
	v_mul_f32_e32 v156, 0x3d000000, v204
	v_mul_f32_e32 v157, 0x3d000000, v208
	v_lshlrev_b32_e32 v204, 16, v199
	v_and_b32_e32 v208, 0xffff0000, v199
	v_mul_f32_e32 v158, 0x3d000000, v204
	v_mul_f32_e32 v159, 0x3d000000, v208
	s_cmp_le_u32 s15, 0
	global_load_dwordx4 v[34:37], v57, s[20:21]
	global_load_dwordx4 v[38:41], v57, s[20:21] offset:1024
	global_load_dwordx4 v[42:45], v57, s[20:21] offset:2048
	global_load_dwordx4 v[46:49], v57, s[20:21] offset:3072
	s_add_u32 s20, s20, 0x1000
	s_addc_u32 s21, s21, 0
	s_waitcnt vmcnt(8)
	v_mfma_f32_32x32x16_bf16 v[160:175], v[128:131], v[2:5], 0
	v_mfma_f32_32x32x16_bf16 v[160:175], v[132:135], v[6:9], v[160:175]
	v_mfma_f32_32x32x16_bf16 v[160:175], v[136:139], v[10:13], v[160:175]
	v_mfma_f32_32x32x16_bf16 v[160:175], v[140:143], v[14:17], v[160:175]
	s_cmp_le_u32 s15, 1
	s_cbranch_scc0 .Lidx_go1
	s_nop 15
	s_branch .Lidx_p1
.Lidx_go1:
	global_load_dwordx4 v[2:5], v57, s[20:21]
	global_load_dwordx4 v[6:9], v57, s[20:21] offset:1024
	global_load_dwordx4 v[10:13], v57, s[20:21] offset:2048
	global_load_dwordx4 v[14:17], v57, s[20:21] offset:3072
	s_add_u32 s20, s20, 0x1000
	s_addc_u32 s21, s21, 0
	s_waitcnt vmcnt(8)
	v_mfma_f32_32x32x16_bf16 v[176:191], v[128:131], v[18:21], 0
	v_mfma_f32_32x32x16_bf16 v[176:191], v[132:135], v[22:25], v[176:191]
	v_mfma_f32_32x32x16_bf16 v[176:191], v[136:139], v[26:29], v[176:191]
	v_mfma_f32_32x32x16_bf16 v[176:191], v[140:143], v[30:33], v[176:191]
.Lidx_p1:
	v_cmp_le_i32_e32 vcc, 0, v59
	v_max_f32_e32 v204, 0, v160
	v_max_f32_e32 v208, 0, v161
	v_fma_f32 v201, v144, v204, 0
	v_max_f32_e32 v204, 0, v162
	v_fmac_f32_e32 v201, v145, v208
	v_max_f32_e32 v208, 0, v163
	v_fmac_f32_e32 v201, v146, v204
	v_max_f32_e32 v204, 0, v164
	v_fmac_f32_e32 v201, v147, v208
	v_max_f32_e32 v208, 0, v165
	v_fmac_f32_e32 v201, v148, v204
	v_max_f32_e32 v204, 0, v166
	v_fmac_f32_e32 v201, v149, v208
	v_max_f32_e32 v208, 0, v167
	v_fmac_f32_e32 v201, v150, v204
	v_max_f32_e32 v204, 0, v168
	v_fmac_f32_e32 v201, v151, v208
	v_max_f32_e32 v208, 0, v169
	v_fmac_f32_e32 v201, v152, v204
	v_max_f32_e32 v204, 0, v170
	v_fmac_f32_e32 v201, v153, v208
	v_max_f32_e32 v208, 0, v171
	v_fmac_f32_e32 v201, v154, v204
	v_max_f32_e32 v204, 0, v172
	v_fmac_f32_e32 v201, v155, v208
	v_max_f32_e32 v208, 0, v173
	v_fmac_f32_e32 v201, v156, v204
	v_max_f32_e32 v204, 0, v174
	v_fmac_f32_e32 v201, v157, v208
	v_max_f32_e32 v208, 0, v175
	v_fmac_f32_e32 v201, v158, v204
	v_fmac_f32_e32 v201, v159, v208
	v_cndmask_b32_e32 v201, v61, v201, vcc
	v_ashrrev_i32_e32 v207, 31, v201
	v_or_b32_e32 v207, 0x80000000, v207
	v_xor_b32_e32 v64, v201, v207
	s_cmp_le_u32 s15, 1
	s_cbranch_scc1 .Lidx_search
	s_cmp_le_u32 s15, 2
	s_cbranch_scc1 .Lidx_p2
	global_load_dwordx4 v[18:21], v57, s[20:21]
	global_load_dwordx4 v[22:25], v57, s[20:21] offset:1024
	global_load_dwordx4 v[26:29], v57, s[20:21] offset:2048
	global_load_dwordx4 v[30:33], v57, s[20:21] offset:3072
	s_add_u32 s20, s20, 0x1000
	s_addc_u32 s21, s21, 0
	s_waitcnt vmcnt(8)
	v_mfma_f32_32x32x16_bf16 v[160:175], v[128:131], v[34:37], 0
	v_mfma_f32_32x32x16_bf16 v[160:175], v[132:135], v[38:41], v[160:175]
	v_mfma_f32_32x32x16_bf16 v[160:175], v[136:139], v[42:45], v[160:175]
	v_mfma_f32_32x32x16_bf16 v[160:175], v[140:143], v[46:49], v[160:175]
.Lidx_p2:
	v_cmp_le_i32_e32 vcc, 32, v59
	v_max_f32_e32 v204, 0, v176
	v_max_f32_e32 v208, 0, v177
	v_fma_f32 v201, v144, v204, 0
	v_max_f32_e32 v204, 0, v178
	v_fmac_f32_e32 v201, v145, v208
	v_max_f32_e32 v208, 0, v179
	v_fmac_f32_e32 v201, v146, v204
	v_max_f32_e32 v204, 0, v180
	v_fmac_f32_e32 v201, v147, v208
	v_max_f32_e32 v208, 0, v181
	v_fmac_f32_e32 v201, v148, v204
	v_max_f32_e32 v204, 0, v182
	v_fmac_f32_e32 v201, v149, v208
	v_max_f32_e32 v208, 0, v183
	v_fmac_f32_e32 v201, v150, v204
	v_max_f32_e32 v204, 0, v184
	v_fmac_f32_e32 v201, v151, v208
	v_max_f32_e32 v208, 0, v185
	v_fmac_f32_e32 v201, v152, v204
	v_max_f32_e32 v204, 0, v186
	v_fmac_f32_e32 v201, v153, v208
	v_max_f32_e32 v208, 0, v187
	v_fmac_f32_e32 v201, v154, v204
	v_max_f32_e32 v204, 0, v188
	v_fmac_f32_e32 v201, v155, v208
	v_max_f32_e32 v208, 0, v189
	v_fmac_f32_e32 v201, v156, v204
	v_max_f32_e32 v204, 0, v190
	v_fmac_f32_e32 v201, v157, v208
	v_max_f32_e32 v208, 0, v191
	v_fmac_f32_e32 v201, v158, v204
	v_fmac_f32_e32 v201, v159, v208
	v_cndmask_b32_e32 v201, v61, v201, vcc
	v_ashrrev_i32_e32 v207, 31, v201
	v_or_b32_e32 v207, 0x80000000, v207
	v_xor_b32_e32 v65, v201, v207
	s_cmp_le_u32 s15, 2
	s_cbranch_scc1 .Lidx_search
	s_cmp_le_u32 s15, 3
	s_cbranch_scc1 .Lidx_p3
	global_load_dwordx4 v[34:37], v57, s[20:21]
	global_load_dwordx4 v[38:41], v57, s[20:21] offset:1024
	global_load_dwordx4 v[42:45], v57, s[20:21] offset:2048
	global_load_dwordx4 v[46:49], v57, s[20:21] offset:3072
	s_add_u32 s20, s20, 0x1000
	s_addc_u32 s21, s21, 0
	s_waitcnt vmcnt(8)
	v_mfma_f32_32x32x16_bf16 v[176:191], v[128:131], v[2:5], 0
	v_mfma_f32_32x32x16_bf16 v[176:191], v[132:135], v[6:9], v[176:191]
	v_mfma_f32_32x32x16_bf16 v[176:191], v[136:139], v[10:13], v[176:191]
	v_mfma_f32_32x32x16_bf16 v[176:191], v[140:143], v[14:17], v[176:191]
.Lidx_p3:
	v_cmp_le_i32_e32 vcc, 64, v59
	v_max_f32_e32 v204, 0, v160
	v_max_f32_e32 v208, 0, v161
	v_fma_f32 v201, v144, v204, 0
	v_max_f32_e32 v204, 0, v162
	v_fmac_f32_e32 v201, v145, v208
	v_max_f32_e32 v208, 0, v163
	v_fmac_f32_e32 v201, v146, v204
	v_max_f32_e32 v204, 0, v164
	v_fmac_f32_e32 v201, v147, v208
	v_max_f32_e32 v208, 0, v165
	v_fmac_f32_e32 v201, v148, v204
	v_max_f32_e32 v204, 0, v166
	v_fmac_f32_e32 v201, v149, v208
	v_max_f32_e32 v208, 0, v167
	v_fmac_f32_e32 v201, v150, v204
	v_max_f32_e32 v204, 0, v168
	v_fmac_f32_e32 v201, v151, v208
	v_max_f32_e32 v208, 0, v169
	v_fmac_f32_e32 v201, v152, v204
	v_max_f32_e32 v204, 0, v170
	v_fmac_f32_e32 v201, v153, v208
	v_max_f32_e32 v208, 0, v171
	v_fmac_f32_e32 v201, v154, v204
	v_max_f32_e32 v204, 0, v172
	v_fmac_f32_e32 v201, v155, v208
	v_max_f32_e32 v208, 0, v173
	v_fmac_f32_e32 v201, v156, v204
	v_max_f32_e32 v204, 0, v174
	v_fmac_f32_e32 v201, v157, v208
	v_max_f32_e32 v208, 0, v175
	v_fmac_f32_e32 v201, v158, v204
	v_fmac_f32_e32 v201, v159, v208
	v_cndmask_b32_e32 v201, v61, v201, vcc
	v_ashrrev_i32_e32 v207, 31, v201
	v_or_b32_e32 v207, 0x80000000, v207
	v_xor_b32_e32 v66, v201, v207
	s_cmp_le_u32 s15, 3
	s_cbranch_scc1 .Lidx_search
	s_cmp_le_u32 s15, 4
	s_cbranch_scc1 .Lidx_p4
	global_load_dwordx4 v[2:5], v57, s[20:21]
	global_load_dwordx4 v[6:9], v57, s[20:21] offset:1024
	global_load_dwordx4 v[10:13], v57, s[20:21] offset:2048
	global_load_dwordx4 v[14:17], v57, s[20:21] offset:3072
	s_add_u32 s20, s20, 0x1000
	s_addc_u32 s21, s21, 0
	s_waitcnt vmcnt(8)
	v_mfma_f32_32x32x16_bf16 v[160:175], v[128:131], v[18:21], 0
	v_mfma_f32_32x32x16_bf16 v[160:175], v[132:135], v[22:25], v[160:175]
	v_mfma_f32_32x32x16_bf16 v[160:175], v[136:139], v[26:29], v[160:175]
	v_mfma_f32_32x32x16_bf16 v[160:175], v[140:143], v[30:33], v[160:175]
.Lidx_p4:
	v_cmp_le_i32_e32 vcc, 0x60, v59
	v_max_f32_e32 v204, 0, v176
	v_max_f32_e32 v208, 0, v177
	v_fma_f32 v201, v144, v204, 0
	v_max_f32_e32 v204, 0, v178
	v_fmac_f32_e32 v201, v145, v208
	v_max_f32_e32 v208, 0, v179
	v_fmac_f32_e32 v201, v146, v204
	v_max_f32_e32 v204, 0, v180
	v_fmac_f32_e32 v201, v147, v208
	v_max_f32_e32 v208, 0, v181
	v_fmac_f32_e32 v201, v148, v204
	v_max_f32_e32 v204, 0, v182
	v_fmac_f32_e32 v201, v149, v208
	v_max_f32_e32 v208, 0, v183
	v_fmac_f32_e32 v201, v150, v204
	v_max_f32_e32 v204, 0, v184
	v_fmac_f32_e32 v201, v151, v208
	v_max_f32_e32 v208, 0, v185
	v_fmac_f32_e32 v201, v152, v204
	v_max_f32_e32 v204, 0, v186
	v_fmac_f32_e32 v201, v153, v208
	v_max_f32_e32 v208, 0, v187
	v_fmac_f32_e32 v201, v154, v204
	v_max_f32_e32 v204, 0, v188
	v_fmac_f32_e32 v201, v155, v208
	v_max_f32_e32 v208, 0, v189
	v_fmac_f32_e32 v201, v156, v204
	v_max_f32_e32 v204, 0, v190
	v_fmac_f32_e32 v201, v157, v208
	v_max_f32_e32 v208, 0, v191
	v_fmac_f32_e32 v201, v158, v204
	v_fmac_f32_e32 v201, v159, v208
	v_cndmask_b32_e32 v201, v61, v201, vcc
	v_ashrrev_i32_e32 v207, 31, v201
	v_or_b32_e32 v207, 0x80000000, v207
	v_xor_b32_e32 v67, v201, v207
	s_cmp_le_u32 s15, 4
	s_cbranch_scc1 .Lidx_search
	s_cmp_le_u32 s15, 5
	s_cbranch_scc1 .Lidx_p5
	global_load_dwordx4 v[18:21], v57, s[20:21]
	global_load_dwordx4 v[22:25], v57, s[20:21] offset:1024
	global_load_dwordx4 v[26:29], v57, s[20:21] offset:2048
	global_load_dwordx4 v[30:33], v57, s[20:21] offset:3072
	s_add_u32 s20, s20, 0x1000
	s_addc_u32 s21, s21, 0
	s_waitcnt vmcnt(8)
	v_mfma_f32_32x32x16_bf16 v[176:191], v[128:131], v[34:37], 0
	v_mfma_f32_32x32x16_bf16 v[176:191], v[132:135], v[38:41], v[176:191]
	v_mfma_f32_32x32x16_bf16 v[176:191], v[136:139], v[42:45], v[176:191]
	v_mfma_f32_32x32x16_bf16 v[176:191], v[140:143], v[46:49], v[176:191]
.Lidx_p5:
	v_cmp_le_i32_e32 vcc, 0x80, v59
	v_max_f32_e32 v204, 0, v160
	v_max_f32_e32 v208, 0, v161
	v_fma_f32 v201, v144, v204, 0
	v_max_f32_e32 v204, 0, v162
	v_fmac_f32_e32 v201, v145, v208
	v_max_f32_e32 v208, 0, v163
	v_fmac_f32_e32 v201, v146, v204
	v_max_f32_e32 v204, 0, v164
	v_fmac_f32_e32 v201, v147, v208
	v_max_f32_e32 v208, 0, v165
	v_fmac_f32_e32 v201, v148, v204
	v_max_f32_e32 v204, 0, v166
	v_fmac_f32_e32 v201, v149, v208
	v_max_f32_e32 v208, 0, v167
	v_fmac_f32_e32 v201, v150, v204
	v_max_f32_e32 v204, 0, v168
	v_fmac_f32_e32 v201, v151, v208
	v_max_f32_e32 v208, 0, v169
	v_fmac_f32_e32 v201, v152, v204
	v_max_f32_e32 v204, 0, v170
	v_fmac_f32_e32 v201, v153, v208
	v_max_f32_e32 v208, 0, v171
	v_fmac_f32_e32 v201, v154, v204
	v_max_f32_e32 v204, 0, v172
	v_fmac_f32_e32 v201, v155, v208
	v_max_f32_e32 v208, 0, v173
	v_fmac_f32_e32 v201, v156, v204
	v_max_f32_e32 v204, 0, v174
	v_fmac_f32_e32 v201, v157, v208
	v_max_f32_e32 v208, 0, v175
	v_fmac_f32_e32 v201, v158, v204
	v_fmac_f32_e32 v201, v159, v208
	v_cndmask_b32_e32 v201, v61, v201, vcc
	v_ashrrev_i32_e32 v207, 31, v201
	v_or_b32_e32 v207, 0x80000000, v207
	v_xor_b32_e32 v68, v201, v207
	s_cmp_le_u32 s15, 5
	s_cbranch_scc1 .Lidx_search
	s_cmp_le_u32 s15, 6
	s_cbranch_scc1 .Lidx_p6
	global_load_dwordx4 v[34:37], v57, s[20:21]
	global_load_dwordx4 v[38:41], v57, s[20:21] offset:1024
	global_load_dwordx4 v[42:45], v57, s[20:21] offset:2048
	global_load_dwordx4 v[46:49], v57, s[20:21] offset:3072
	s_add_u32 s20, s20, 0x1000
	s_addc_u32 s21, s21, 0
	s_waitcnt vmcnt(8)
	v_mfma_f32_32x32x16_bf16 v[160:175], v[128:131], v[2:5], 0
	v_mfma_f32_32x32x16_bf16 v[160:175], v[132:135], v[6:9], v[160:175]
	v_mfma_f32_32x32x16_bf16 v[160:175], v[136:139], v[10:13], v[160:175]
	v_mfma_f32_32x32x16_bf16 v[160:175], v[140:143], v[14:17], v[160:175]
.Lidx_p6:
	v_cmp_le_i32_e32 vcc, 0xa0, v59
	v_max_f32_e32 v204, 0, v176
	v_max_f32_e32 v208, 0, v177
	v_fma_f32 v201, v144, v204, 0
	v_max_f32_e32 v204, 0, v178
	v_fmac_f32_e32 v201, v145, v208
	v_max_f32_e32 v208, 0, v179
	v_fmac_f32_e32 v201, v146, v204
	v_max_f32_e32 v204, 0, v180
	v_fmac_f32_e32 v201, v147, v208
	v_max_f32_e32 v208, 0, v181
	v_fmac_f32_e32 v201, v148, v204
	v_max_f32_e32 v204, 0, v182
	v_fmac_f32_e32 v201, v149, v208
	v_max_f32_e32 v208, 0, v183
	v_fmac_f32_e32 v201, v150, v204
	v_max_f32_e32 v204, 0, v184
	v_fmac_f32_e32 v201, v151, v208
	v_max_f32_e32 v208, 0, v185
	v_fmac_f32_e32 v201, v152, v204
	v_max_f32_e32 v204, 0, v186
	v_fmac_f32_e32 v201, v153, v208
	v_max_f32_e32 v208, 0, v187
	v_fmac_f32_e32 v201, v154, v204
	v_max_f32_e32 v204, 0, v188
	v_fmac_f32_e32 v201, v155, v208
	v_max_f32_e32 v208, 0, v189
	v_fmac_f32_e32 v201, v156, v204
	v_max_f32_e32 v204, 0, v190
	v_fmac_f32_e32 v201, v157, v208
	v_max_f32_e32 v208, 0, v191
	v_fmac_f32_e32 v201, v158, v204
	v_fmac_f32_e32 v201, v159, v208
	v_cndmask_b32_e32 v201, v61, v201, vcc
	v_ashrrev_i32_e32 v207, 31, v201
	v_or_b32_e32 v207, 0x80000000, v207
	v_xor_b32_e32 v69, v201, v207
	s_cmp_le_u32 s15, 6
	s_cbranch_scc1 .Lidx_search
	s_cmp_le_u32 s15, 7
	s_cbranch_scc1 .Lidx_p7
	global_load_dwordx4 v[2:5], v57, s[20:21]
	global_load_dwordx4 v[6:9], v57, s[20:21] offset:1024
	global_load_dwordx4 v[10:13], v57, s[20:21] offset:2048
	global_load_dwordx4 v[14:17], v57, s[20:21] offset:3072
	s_add_u32 s20, s20, 0x1000
	s_addc_u32 s21, s21, 0
	s_waitcnt vmcnt(8)
	v_mfma_f32_32x32x16_bf16 v[176:191], v[128:131], v[18:21], 0
	v_mfma_f32_32x32x16_bf16 v[176:191], v[132:135], v[22:25], v[176:191]
	v_mfma_f32_32x32x16_bf16 v[176:191], v[136:139], v[26:29], v[176:191]
	v_mfma_f32_32x32x16_bf16 v[176:191], v[140:143], v[30:33], v[176:191]
.Lidx_p7:
	v_cmp_le_i32_e32 vcc, 0xc0, v59
	v_max_f32_e32 v204, 0, v160
	v_max_f32_e32 v208, 0, v161
	v_fma_f32 v201, v144, v204, 0
	v_max_f32_e32 v204, 0, v162
	v_fmac_f32_e32 v201, v145, v208
	v_max_f32_e32 v208, 0, v163
	v_fmac_f32_e32 v201, v146, v204
	v_max_f32_e32 v204, 0, v164
	v_fmac_f32_e32 v201, v147, v208
	v_max_f32_e32 v208, 0, v165
	v_fmac_f32_e32 v201, v148, v204
	v_max_f32_e32 v204, 0, v166
	v_fmac_f32_e32 v201, v149, v208
	v_max_f32_e32 v208, 0, v167
	v_fmac_f32_e32 v201, v150, v204
	v_max_f32_e32 v204, 0, v168
	v_fmac_f32_e32 v201, v151, v208
	v_max_f32_e32 v208, 0, v169
	v_fmac_f32_e32 v201, v152, v204
	v_max_f32_e32 v204, 0, v170
	v_fmac_f32_e32 v201, v153, v208
	v_max_f32_e32 v208, 0, v171
	v_fmac_f32_e32 v201, v154, v204
	v_max_f32_e32 v204, 0, v172
	v_fmac_f32_e32 v201, v155, v208
	v_max_f32_e32 v208, 0, v173
	v_fmac_f32_e32 v201, v156, v204
	v_max_f32_e32 v204, 0, v174
	v_fmac_f32_e32 v201, v157, v208
	v_max_f32_e32 v208, 0, v175
	v_fmac_f32_e32 v201, v158, v204
	v_fmac_f32_e32 v201, v159, v208
	v_cndmask_b32_e32 v201, v61, v201, vcc
	v_ashrrev_i32_e32 v207, 31, v201
	v_or_b32_e32 v207, 0x80000000, v207
	v_xor_b32_e32 v70, v201, v207
	s_cmp_le_u32 s15, 7
	s_cbranch_scc1 .Lidx_search
	s_cmp_le_u32 s15, 8
	s_cbranch_scc1 .Lidx_p8
	global_load_dwordx4 v[18:21], v57, s[20:21]
	global_load_dwordx4 v[22:25], v57, s[20:21] offset:1024
	global_load_dwordx4 v[26:29], v57, s[20:21] offset:2048
	global_load_dwordx4 v[30:33], v57, s[20:21] offset:3072
	s_add_u32 s20, s20, 0x1000
	s_addc_u32 s21, s21, 0
	s_waitcnt vmcnt(8)
	v_mfma_f32_32x32x16_bf16 v[160:175], v[128:131], v[34:37], 0
	v_mfma_f32_32x32x16_bf16 v[160:175], v[132:135], v[38:41], v[160:175]
	v_mfma_f32_32x32x16_bf16 v[160:175], v[136:139], v[42:45], v[160:175]
	v_mfma_f32_32x32x16_bf16 v[160:175], v[140:143], v[46:49], v[160:175]
.Lidx_p8:
	v_cmp_le_i32_e32 vcc, 0xe0, v59
	v_max_f32_e32 v204, 0, v176
	v_max_f32_e32 v208, 0, v177
	v_fma_f32 v201, v144, v204, 0
	v_max_f32_e32 v204, 0, v178
	v_fmac_f32_e32 v201, v145, v208
	v_max_f32_e32 v208, 0, v179
	v_fmac_f32_e32 v201, v146, v204
	v_max_f32_e32 v204, 0, v180
	v_fmac_f32_e32 v201, v147, v208
	v_max_f32_e32 v208, 0, v181
	v_fmac_f32_e32 v201, v148, v204
	v_max_f32_e32 v204, 0, v182
	v_fmac_f32_e32 v201, v149, v208
	v_max_f32_e32 v208, 0, v183
	v_fmac_f32_e32 v201, v150, v204
	v_max_f32_e32 v204, 0, v184
	v_fmac_f32_e32 v201, v151, v208
	v_max_f32_e32 v208, 0, v185
	v_fmac_f32_e32 v201, v152, v204
	v_max_f32_e32 v204, 0, v186
	v_fmac_f32_e32 v201, v153, v208
	v_max_f32_e32 v208, 0, v187
	v_fmac_f32_e32 v201, v154, v204
	v_max_f32_e32 v204, 0, v188
	v_fmac_f32_e32 v201, v155, v208
	v_max_f32_e32 v208, 0, v189
	v_fmac_f32_e32 v201, v156, v204
	v_max_f32_e32 v204, 0, v190
	v_fmac_f32_e32 v201, v157, v208
	v_max_f32_e32 v208, 0, v191
	v_fmac_f32_e32 v201, v158, v204
	v_fmac_f32_e32 v201, v159, v208
	v_cndmask_b32_e32 v201, v61, v201, vcc
	v_ashrrev_i32_e32 v207, 31, v201
	v_or_b32_e32 v207, 0x80000000, v207
	v_xor_b32_e32 v71, v201, v207
	s_cmp_le_u32 s15, 8
	s_cbranch_scc1 .Lidx_search
	s_cmp_le_u32 s15, 9
	s_cbranch_scc1 .Lidx_p9
	global_load_dwordx4 v[34:37], v57, s[20:21]
	global_load_dwordx4 v[38:41], v57, s[20:21] offset:1024
	global_load_dwordx4 v[42:45], v57, s[20:21] offset:2048
	global_load_dwordx4 v[46:49], v57, s[20:21] offset:3072
	s_add_u32 s20, s20, 0x1000
	s_addc_u32 s21, s21, 0
	s_waitcnt vmcnt(8)
	v_mfma_f32_32x32x16_bf16 v[176:191], v[128:131], v[2:5], 0
	v_mfma_f32_32x32x16_bf16 v[176:191], v[132:135], v[6:9], v[176:191]
	v_mfma_f32_32x32x16_bf16 v[176:191], v[136:139], v[10:13], v[176:191]
	v_mfma_f32_32x32x16_bf16 v[176:191], v[140:143], v[14:17], v[176:191]
.Lidx_p9:
	v_cmp_le_i32_e32 vcc, 0x100, v59
	v_max_f32_e32 v204, 0, v160
	v_max_f32_e32 v208, 0, v161
	v_fma_f32 v201, v144, v204, 0
	v_max_f32_e32 v204, 0, v162
	v_fmac_f32_e32 v201, v145, v208
	v_max_f32_e32 v208, 0, v163
	v_fmac_f32_e32 v201, v146, v204
	v_max_f32_e32 v204, 0, v164
	v_fmac_f32_e32 v201, v147, v208
	v_max_f32_e32 v208, 0, v165
	v_fmac_f32_e32 v201, v148, v204
	v_max_f32_e32 v204, 0, v166
	v_fmac_f32_e32 v201, v149, v208
	v_max_f32_e32 v208, 0, v167
	v_fmac_f32_e32 v201, v150, v204
	v_max_f32_e32 v204, 0, v168
	v_fmac_f32_e32 v201, v151, v208
	v_max_f32_e32 v208, 0, v169
	v_fmac_f32_e32 v201, v152, v204
	v_max_f32_e32 v204, 0, v170
	v_fmac_f32_e32 v201, v153, v208
	v_max_f32_e32 v208, 0, v171
	v_fmac_f32_e32 v201, v154, v204
	v_max_f32_e32 v204, 0, v172
	v_fmac_f32_e32 v201, v155, v208
	v_max_f32_e32 v208, 0, v173
	v_fmac_f32_e32 v201, v156, v204
	v_max_f32_e32 v204, 0, v174
	v_fmac_f32_e32 v201, v157, v208
	v_max_f32_e32 v208, 0, v175
	v_fmac_f32_e32 v201, v158, v204
	v_fmac_f32_e32 v201, v159, v208
	v_cndmask_b32_e32 v201, v61, v201, vcc
	v_ashrrev_i32_e32 v207, 31, v201
	v_or_b32_e32 v207, 0x80000000, v207
	v_xor_b32_e32 v72, v201, v207
	s_cmp_le_u32 s15, 9
	s_cbranch_scc1 .Lidx_search
	s_cmp_le_u32 s15, 10
	s_cbranch_scc1 .Lidx_p10
	global_load_dwordx4 v[2:5], v57, s[20:21]
	global_load_dwordx4 v[6:9], v57, s[20:21] offset:1024
	global_load_dwordx4 v[10:13], v57, s[20:21] offset:2048
	global_load_dwordx4 v[14:17], v57, s[20:21] offset:3072
	s_add_u32 s20, s20, 0x1000
	s_addc_u32 s21, s21, 0
	s_waitcnt vmcnt(8)
	v_mfma_f32_32x32x16_bf16 v[160:175], v[128:131], v[18:21], 0
	v_mfma_f32_32x32x16_bf16 v[160:175], v[132:135], v[22:25], v[160:175]
	v_mfma_f32_32x32x16_bf16 v[160:175], v[136:139], v[26:29], v[160:175]
	v_mfma_f32_32x32x16_bf16 v[160:175], v[140:143], v[30:33], v[160:175]
.Lidx_p10:
	v_cmp_le_i32_e32 vcc, 0x120, v59
	v_max_f32_e32 v204, 0, v176
	v_max_f32_e32 v208, 0, v177
	v_fma_f32 v201, v144, v204, 0
	v_max_f32_e32 v204, 0, v178
	v_fmac_f32_e32 v201, v145, v208
	v_max_f32_e32 v208, 0, v179
	v_fmac_f32_e32 v201, v146, v204
	v_max_f32_e32 v204, 0, v180
	v_fmac_f32_e32 v201, v147, v208
	v_max_f32_e32 v208, 0, v181
	v_fmac_f32_e32 v201, v148, v204
	v_max_f32_e32 v204, 0, v182
	v_fmac_f32_e32 v201, v149, v208
	v_max_f32_e32 v208, 0, v183
	v_fmac_f32_e32 v201, v150, v204
	v_max_f32_e32 v204, 0, v184
	v_fmac_f32_e32 v201, v151, v208
	v_max_f32_e32 v208, 0, v185
	v_fmac_f32_e32 v201, v152, v204
	v_max_f32_e32 v204, 0, v186
	v_fmac_f32_e32 v201, v153, v208
	v_max_f32_e32 v208, 0, v187
	v_fmac_f32_e32 v201, v154, v204
	v_max_f32_e32 v204, 0, v188
	v_fmac_f32_e32 v201, v155, v208
	v_max_f32_e32 v208, 0, v189
	v_fmac_f32_e32 v201, v156, v204
	v_max_f32_e32 v204, 0, v190
	v_fmac_f32_e32 v201, v157, v208
	v_max_f32_e32 v208, 0, v191
	v_fmac_f32_e32 v201, v158, v204
	v_fmac_f32_e32 v201, v159, v208
	v_cndmask_b32_e32 v201, v61, v201, vcc
	v_ashrrev_i32_e32 v207, 31, v201
	v_or_b32_e32 v207, 0x80000000, v207
	v_xor_b32_e32 v73, v201, v207
	s_cmp_le_u32 s15, 10
	s_cbranch_scc1 .Lidx_search
	s_cmp_le_u32 s15, 11
	s_cbranch_scc1 .Lidx_p11
	global_load_dwordx4 v[18:21], v57, s[20:21]
	global_load_dwordx4 v[22:25], v57, s[20:21] offset:1024
	global_load_dwordx4 v[26:29], v57, s[20:21] offset:2048
	global_load_dwordx4 v[30:33], v57, s[20:21] offset:3072
	s_add_u32 s20, s20, 0x1000
	s_addc_u32 s21, s21, 0
	s_waitcnt vmcnt(8)
	v_mfma_f32_32x32x16_bf16 v[176:191], v[128:131], v[34:37], 0
	v_mfma_f32_32x32x16_bf16 v[176:191], v[132:135], v[38:41], v[176:191]
	v_mfma_f32_32x32x16_bf16 v[176:191], v[136:139], v[42:45], v[176:191]
	v_mfma_f32_32x32x16_bf16 v[176:191], v[140:143], v[46:49], v[176:191]
.Lidx_p11:
	v_cmp_le_i32_e32 vcc, 0x140, v59
	v_max_f32_e32 v204, 0, v160
	v_max_f32_e32 v208, 0, v161
	v_fma_f32 v201, v144, v204, 0
	v_max_f32_e32 v204, 0, v162
	v_fmac_f32_e32 v201, v145, v208
	v_max_f32_e32 v208, 0, v163
	v_fmac_f32_e32 v201, v146, v204
	v_max_f32_e32 v204, 0, v164
	v_fmac_f32_e32 v201, v147, v208
	v_max_f32_e32 v208, 0, v165
	v_fmac_f32_e32 v201, v148, v204
	v_max_f32_e32 v204, 0, v166
	v_fmac_f32_e32 v201, v149, v208
	v_max_f32_e32 v208, 0, v167
	v_fmac_f32_e32 v201, v150, v204
	v_max_f32_e32 v204, 0, v168
	v_fmac_f32_e32 v201, v151, v208
	v_max_f32_e32 v208, 0, v169
	v_fmac_f32_e32 v201, v152, v204
	v_max_f32_e32 v204, 0, v170
	v_fmac_f32_e32 v201, v153, v208
	v_max_f32_e32 v208, 0, v171
	v_fmac_f32_e32 v201, v154, v204
	v_max_f32_e32 v204, 0, v172
	v_fmac_f32_e32 v201, v155, v208
	v_max_f32_e32 v208, 0, v173
	v_fmac_f32_e32 v201, v156, v204
	v_max_f32_e32 v204, 0, v174
	v_fmac_f32_e32 v201, v157, v208
	v_max_f32_e32 v208, 0, v175
	v_fmac_f32_e32 v201, v158, v204
	v_fmac_f32_e32 v201, v159, v208
	v_cndmask_b32_e32 v201, v61, v201, vcc
	v_ashrrev_i32_e32 v207, 31, v201
	v_or_b32_e32 v207, 0x80000000, v207
	v_xor_b32_e32 v74, v201, v207
	s_cmp_le_u32 s15, 11
	s_cbranch_scc1 .Lidx_search
	s_cmp_le_u32 s15, 12
	s_cbranch_scc1 .Lidx_p12
	global_load_dwordx4 v[34:37], v57, s[20:21]
	global_load_dwordx4 v[38:41], v57, s[20:21] offset:1024
	global_load_dwordx4 v[42:45], v57, s[20:21] offset:2048
	global_load_dwordx4 v[46:49], v57, s[20:21] offset:3072
	s_add_u32 s20, s20, 0x1000
	s_addc_u32 s21, s21, 0
	s_waitcnt vmcnt(8)
	v_mfma_f32_32x32x16_bf16 v[160:175], v[128:131], v[2:5], 0
	v_mfma_f32_32x32x16_bf16 v[160:175], v[132:135], v[6:9], v[160:175]
	v_mfma_f32_32x32x16_bf16 v[160:175], v[136:139], v[10:13], v[160:175]
	v_mfma_f32_32x32x16_bf16 v[160:175], v[140:143], v[14:17], v[160:175]
.Lidx_p12:
	v_cmp_le_i32_e32 vcc, 0x160, v59
	v_max_f32_e32 v204, 0, v176
	v_max_f32_e32 v208, 0, v177
	v_fma_f32 v201, v144, v204, 0
	v_max_f32_e32 v204, 0, v178
	v_fmac_f32_e32 v201, v145, v208
	v_max_f32_e32 v208, 0, v179
	v_fmac_f32_e32 v201, v146, v204
	v_max_f32_e32 v204, 0, v180
	v_fmac_f32_e32 v201, v147, v208
	v_max_f32_e32 v208, 0, v181
	v_fmac_f32_e32 v201, v148, v204
	v_max_f32_e32 v204, 0, v182
	v_fmac_f32_e32 v201, v149, v208
	v_max_f32_e32 v208, 0, v183
	v_fmac_f32_e32 v201, v150, v204
	v_max_f32_e32 v204, 0, v184
	v_fmac_f32_e32 v201, v151, v208
	v_max_f32_e32 v208, 0, v185
	v_fmac_f32_e32 v201, v152, v204
	v_max_f32_e32 v204, 0, v186
	v_fmac_f32_e32 v201, v153, v208
	v_max_f32_e32 v208, 0, v187
	v_fmac_f32_e32 v201, v154, v204
	v_max_f32_e32 v204, 0, v188
	v_fmac_f32_e32 v201, v155, v208
	v_max_f32_e32 v208, 0, v189
	v_fmac_f32_e32 v201, v156, v204
	v_max_f32_e32 v204, 0, v190
	v_fmac_f32_e32 v201, v157, v208
	v_max_f32_e32 v208, 0, v191
	v_fmac_f32_e32 v201, v158, v204
	v_fmac_f32_e32 v201, v159, v208
	v_cndmask_b32_e32 v201, v61, v201, vcc
	v_ashrrev_i32_e32 v207, 31, v201
	v_or_b32_e32 v207, 0x80000000, v207
	v_xor_b32_e32 v75, v201, v207
	s_cmp_le_u32 s15, 12
	s_cbranch_scc1 .Lidx_search
	s_cmp_le_u32 s15, 13
	s_cbranch_scc1 .Lidx_p13
	global_load_dwordx4 v[2:5], v57, s[20:21]
	global_load_dwordx4 v[6:9], v57, s[20:21] offset:1024
	global_load_dwordx4 v[10:13], v57, s[20:21] offset:2048
	global_load_dwordx4 v[14:17], v57, s[20:21] offset:3072
	s_add_u32 s20, s20, 0x1000
	s_addc_u32 s21, s21, 0
	s_waitcnt vmcnt(8)
	v_mfma_f32_32x32x16_bf16 v[176:191], v[128:131], v[18:21], 0
	v_mfma_f32_32x32x16_bf16 v[176:191], v[132:135], v[22:25], v[176:191]
	v_mfma_f32_32x32x16_bf16 v[176:191], v[136:139], v[26:29], v[176:191]
	v_mfma_f32_32x32x16_bf16 v[176:191], v[140:143], v[30:33], v[176:191]
.Lidx_p13:
	v_cmp_le_i32_e32 vcc, 0x180, v59
	v_max_f32_e32 v204, 0, v160
	v_max_f32_e32 v208, 0, v161
	v_fma_f32 v201, v144, v204, 0
	v_max_f32_e32 v204, 0, v162
	v_fmac_f32_e32 v201, v145, v208
	v_max_f32_e32 v208, 0, v163
	v_fmac_f32_e32 v201, v146, v204
	v_max_f32_e32 v204, 0, v164
	v_fmac_f32_e32 v201, v147, v208
	v_max_f32_e32 v208, 0, v165
	v_fmac_f32_e32 v201, v148, v204
	v_max_f32_e32 v204, 0, v166
	v_fmac_f32_e32 v201, v149, v208
	v_max_f32_e32 v208, 0, v167
	v_fmac_f32_e32 v201, v150, v204
	v_max_f32_e32 v204, 0, v168
	v_fmac_f32_e32 v201, v151, v208
	v_max_f32_e32 v208, 0, v169
	v_fmac_f32_e32 v201, v152, v204
	v_max_f32_e32 v204, 0, v170
	v_fmac_f32_e32 v201, v153, v208
	v_max_f32_e32 v208, 0, v171
	v_fmac_f32_e32 v201, v154, v204
	v_max_f32_e32 v204, 0, v172
	v_fmac_f32_e32 v201, v155, v208
	v_max_f32_e32 v208, 0, v173
	v_fmac_f32_e32 v201, v156, v204
	v_max_f32_e32 v204, 0, v174
	v_fmac_f32_e32 v201, v157, v208
	v_max_f32_e32 v208, 0, v175
	v_fmac_f32_e32 v201, v158, v204
	v_fmac_f32_e32 v201, v159, v208
	v_cndmask_b32_e32 v201, v61, v201, vcc
	v_ashrrev_i32_e32 v207, 31, v201
	v_or_b32_e32 v207, 0x80000000, v207
	v_xor_b32_e32 v76, v201, v207
	s_cmp_le_u32 s15, 13
	s_cbranch_scc1 .Lidx_search
	s_cmp_le_u32 s15, 14
	s_cbranch_scc1 .Lidx_p14
	global_load_dwordx4 v[18:21], v57, s[20:21]
	global_load_dwordx4 v[22:25], v57, s[20:21] offset:1024
	global_load_dwordx4 v[26:29], v57, s[20:21] offset:2048
	global_load_dwordx4 v[30:33], v57, s[20:21] offset:3072
	s_add_u32 s20, s20, 0x1000
	s_addc_u32 s21, s21, 0
	s_waitcnt vmcnt(8)
	v_mfma_f32_32x32x16_bf16 v[160:175], v[128:131], v[34:37], 0
	v_mfma_f32_32x32x16_bf16 v[160:175], v[132:135], v[38:41], v[160:175]
	v_mfma_f32_32x32x16_bf16 v[160:175], v[136:139], v[42:45], v[160:175]
	v_mfma_f32_32x32x16_bf16 v[160:175], v[140:143], v[46:49], v[160:175]
.Lidx_p14:
	v_cmp_le_i32_e32 vcc, 0x1a0, v59
	v_max_f32_e32 v204, 0, v176
	v_max_f32_e32 v208, 0, v177
	v_fma_f32 v201, v144, v204, 0
	v_max_f32_e32 v204, 0, v178
	v_fmac_f32_e32 v201, v145, v208
	v_max_f32_e32 v208, 0, v179
	v_fmac_f32_e32 v201, v146, v204
	v_max_f32_e32 v204, 0, v180
	v_fmac_f32_e32 v201, v147, v208
	v_max_f32_e32 v208, 0, v181
	v_fmac_f32_e32 v201, v148, v204
	v_max_f32_e32 v204, 0, v182
	v_fmac_f32_e32 v201, v149, v208
	v_max_f32_e32 v208, 0, v183
	v_fmac_f32_e32 v201, v150, v204
	v_max_f32_e32 v204, 0, v184
	v_fmac_f32_e32 v201, v151, v208
	v_max_f32_e32 v208, 0, v185
	v_fmac_f32_e32 v201, v152, v204
	v_max_f32_e32 v204, 0, v186
	v_fmac_f32_e32 v201, v153, v208
	v_max_f32_e32 v208, 0, v187
	v_fmac_f32_e32 v201, v154, v204
	v_max_f32_e32 v204, 0, v188
	v_fmac_f32_e32 v201, v155, v208
	v_max_f32_e32 v208, 0, v189
	v_fmac_f32_e32 v201, v156, v204
	v_max_f32_e32 v204, 0, v190
	v_fmac_f32_e32 v201, v157, v208
	v_max_f32_e32 v208, 0, v191
	v_fmac_f32_e32 v201, v158, v204
	v_fmac_f32_e32 v201, v159, v208
	v_cndmask_b32_e32 v201, v61, v201, vcc
	v_ashrrev_i32_e32 v207, 31, v201
	v_or_b32_e32 v207, 0x80000000, v207
	v_xor_b32_e32 v77, v201, v207
	s_cmp_le_u32 s15, 14
	s_cbranch_scc1 .Lidx_search
	s_cmp_le_u32 s15, 15
	s_cbranch_scc1 .Lidx_p15
	global_load_dwordx4 v[34:37], v57, s[20:21]
	global_load_dwordx4 v[38:41], v57, s[20:21] offset:1024
	global_load_dwordx4 v[42:45], v57, s[20:21] offset:2048
	global_load_dwordx4 v[46:49], v57, s[20:21] offset:3072
	s_add_u32 s20, s20, 0x1000
	s_addc_u32 s21, s21, 0
	s_waitcnt vmcnt(8)
	v_mfma_f32_32x32x16_bf16 v[176:191], v[128:131], v[2:5], 0
	v_mfma_f32_32x32x16_bf16 v[176:191], v[132:135], v[6:9], v[176:191]
	v_mfma_f32_32x32x16_bf16 v[176:191], v[136:139], v[10:13], v[176:191]
	v_mfma_f32_32x32x16_bf16 v[176:191], v[140:143], v[14:17], v[176:191]
.Lidx_p15:
	v_cmp_le_i32_e32 vcc, 0x1c0, v59
	v_max_f32_e32 v204, 0, v160
	v_max_f32_e32 v208, 0, v161
	v_fma_f32 v201, v144, v204, 0
	v_max_f32_e32 v204, 0, v162
	v_fmac_f32_e32 v201, v145, v208
	v_max_f32_e32 v208, 0, v163
	v_fmac_f32_e32 v201, v146, v204
	v_max_f32_e32 v204, 0, v164
	v_fmac_f32_e32 v201, v147, v208
	v_max_f32_e32 v208, 0, v165
	v_fmac_f32_e32 v201, v148, v204
	v_max_f32_e32 v204, 0, v166
	v_fmac_f32_e32 v201, v149, v208
	v_max_f32_e32 v208, 0, v167
	v_fmac_f32_e32 v201, v150, v204
	v_max_f32_e32 v204, 0, v168
	v_fmac_f32_e32 v201, v151, v208
	v_max_f32_e32 v208, 0, v169
	v_fmac_f32_e32 v201, v152, v204
	v_max_f32_e32 v204, 0, v170
	v_fmac_f32_e32 v201, v153, v208
	v_max_f32_e32 v208, 0, v171
	v_fmac_f32_e32 v201, v154, v204
	v_max_f32_e32 v204, 0, v172
	v_fmac_f32_e32 v201, v155, v208
	v_max_f32_e32 v208, 0, v173
	v_fmac_f32_e32 v201, v156, v204
	v_max_f32_e32 v204, 0, v174
	v_fmac_f32_e32 v201, v157, v208
	v_max_f32_e32 v208, 0, v175
	v_fmac_f32_e32 v201, v158, v204
	v_fmac_f32_e32 v201, v159, v208
	v_cndmask_b32_e32 v201, v61, v201, vcc
	v_ashrrev_i32_e32 v207, 31, v201
	v_or_b32_e32 v207, 0x80000000, v207
	v_xor_b32_e32 v78, v201, v207
	s_cmp_le_u32 s15, 15
	s_cbranch_scc1 .Lidx_search
	s_cmp_le_u32 s15, 16
	s_cbranch_scc1 .Lidx_p16
	global_load_dwordx4 v[2:5], v57, s[20:21]
	global_load_dwordx4 v[6:9], v57, s[20:21] offset:1024
	global_load_dwordx4 v[10:13], v57, s[20:21] offset:2048
	global_load_dwordx4 v[14:17], v57, s[20:21] offset:3072
	s_add_u32 s20, s20, 0x1000
	s_addc_u32 s21, s21, 0
	s_waitcnt vmcnt(8)
	v_mfma_f32_32x32x16_bf16 v[160:175], v[128:131], v[18:21], 0
	v_mfma_f32_32x32x16_bf16 v[160:175], v[132:135], v[22:25], v[160:175]
	v_mfma_f32_32x32x16_bf16 v[160:175], v[136:139], v[26:29], v[160:175]
	v_mfma_f32_32x32x16_bf16 v[160:175], v[140:143], v[30:33], v[160:175]
.Lidx_p16:
	v_cmp_le_i32_e32 vcc, 0x1e0, v59
	v_max_f32_e32 v204, 0, v176
	v_max_f32_e32 v208, 0, v177
	v_fma_f32 v201, v144, v204, 0
	v_max_f32_e32 v204, 0, v178
	v_fmac_f32_e32 v201, v145, v208
	v_max_f32_e32 v208, 0, v179
	v_fmac_f32_e32 v201, v146, v204
	v_max_f32_e32 v204, 0, v180
	v_fmac_f32_e32 v201, v147, v208
	v_max_f32_e32 v208, 0, v181
	v_fmac_f32_e32 v201, v148, v204
	v_max_f32_e32 v204, 0, v182
	v_fmac_f32_e32 v201, v149, v208
	v_max_f32_e32 v208, 0, v183
	v_fmac_f32_e32 v201, v150, v204
	v_max_f32_e32 v204, 0, v184
	v_fmac_f32_e32 v201, v151, v208
	v_max_f32_e32 v208, 0, v185
	v_fmac_f32_e32 v201, v152, v204
	v_max_f32_e32 v204, 0, v186
	v_fmac_f32_e32 v201, v153, v208
	v_max_f32_e32 v208, 0, v187
	v_fmac_f32_e32 v201, v154, v204
	v_max_f32_e32 v204, 0, v188
	v_fmac_f32_e32 v201, v155, v208
	v_max_f32_e32 v208, 0, v189
	v_fmac_f32_e32 v201, v156, v204
	v_max_f32_e32 v204, 0, v190
	v_fmac_f32_e32 v201, v157, v208
	v_max_f32_e32 v208, 0, v191
	v_fmac_f32_e32 v201, v158, v204
	v_fmac_f32_e32 v201, v159, v208
	v_cndmask_b32_e32 v201, v61, v201, vcc
	v_ashrrev_i32_e32 v207, 31, v201
	v_or_b32_e32 v207, 0x80000000, v207
	v_xor_b32_e32 v79, v201, v207
	s_cmp_le_u32 s15, 16
	s_cbranch_scc1 .Lidx_search
	s_cmp_le_u32 s15, 17
	s_cbranch_scc1 .Lidx_p17
	global_load_dwordx4 v[18:21], v57, s[20:21]
	global_load_dwordx4 v[22:25], v57, s[20:21] offset:1024
	global_load_dwordx4 v[26:29], v57, s[20:21] offset:2048
	global_load_dwordx4 v[30:33], v57, s[20:21] offset:3072
	s_add_u32 s20, s20, 0x1000
	s_addc_u32 s21, s21, 0
	s_waitcnt vmcnt(8)
	v_mfma_f32_32x32x16_bf16 v[176:191], v[128:131], v[34:37], 0
	v_mfma_f32_32x32x16_bf16 v[176:191], v[132:135], v[38:41], v[176:191]
	v_mfma_f32_32x32x16_bf16 v[176:191], v[136:139], v[42:45], v[176:191]
	v_mfma_f32_32x32x16_bf16 v[176:191], v[140:143], v[46:49], v[176:191]
.Lidx_p17:
	v_cmp_le_i32_e32 vcc, 0x200, v59
	v_max_f32_e32 v204, 0, v160
	v_max_f32_e32 v208, 0, v161
	v_fma_f32 v201, v144, v204, 0
	v_max_f32_e32 v204, 0, v162
	v_fmac_f32_e32 v201, v145, v208
	v_max_f32_e32 v208, 0, v163
	v_fmac_f32_e32 v201, v146, v204
	v_max_f32_e32 v204, 0, v164
	v_fmac_f32_e32 v201, v147, v208
	v_max_f32_e32 v208, 0, v165
	v_fmac_f32_e32 v201, v148, v204
	v_max_f32_e32 v204, 0, v166
	v_fmac_f32_e32 v201, v149, v208
	v_max_f32_e32 v208, 0, v167
	v_fmac_f32_e32 v201, v150, v204
	v_max_f32_e32 v204, 0, v168
	v_fmac_f32_e32 v201, v151, v208
	v_max_f32_e32 v208, 0, v169
	v_fmac_f32_e32 v201, v152, v204
	v_max_f32_e32 v204, 0, v170
	v_fmac_f32_e32 v201, v153, v208
	v_max_f32_e32 v208, 0, v171
	v_fmac_f32_e32 v201, v154, v204
	v_max_f32_e32 v204, 0, v172
	v_fmac_f32_e32 v201, v155, v208
	v_max_f32_e32 v208, 0, v173
	v_fmac_f32_e32 v201, v156, v204
	v_max_f32_e32 v204, 0, v174
	v_fmac_f32_e32 v201, v157, v208
	v_max_f32_e32 v208, 0, v175
	v_fmac_f32_e32 v201, v158, v204
	v_fmac_f32_e32 v201, v159, v208
	v_cndmask_b32_e32 v201, v61, v201, vcc
	v_ashrrev_i32_e32 v207, 31, v201
	v_or_b32_e32 v207, 0x80000000, v207
	v_xor_b32_e32 v80, v201, v207
	s_cmp_le_u32 s15, 17
	s_cbranch_scc1 .Lidx_search
	s_cmp_le_u32 s15, 18
	s_cbranch_scc1 .Lidx_p18
	global_load_dwordx4 v[34:37], v57, s[20:21]
	global_load_dwordx4 v[38:41], v57, s[20:21] offset:1024
	global_load_dwordx4 v[42:45], v57, s[20:21] offset:2048
	global_load_dwordx4 v[46:49], v57, s[20:21] offset:3072
	s_add_u32 s20, s20, 0x1000
	s_addc_u32 s21, s21, 0
	s_waitcnt vmcnt(8)
	v_mfma_f32_32x32x16_bf16 v[160:175], v[128:131], v[2:5], 0
	v_mfma_f32_32x32x16_bf16 v[160:175], v[132:135], v[6:9], v[160:175]
	v_mfma_f32_32x32x16_bf16 v[160:175], v[136:139], v[10:13], v[160:175]
	v_mfma_f32_32x32x16_bf16 v[160:175], v[140:143], v[14:17], v[160:175]
.Lidx_p18:
	v_cmp_le_i32_e32 vcc, 0x220, v59
	v_max_f32_e32 v204, 0, v176
	v_max_f32_e32 v208, 0, v177
	v_fma_f32 v201, v144, v204, 0
	v_max_f32_e32 v204, 0, v178
	v_fmac_f32_e32 v201, v145, v208
	v_max_f32_e32 v208, 0, v179
	v_fmac_f32_e32 v201, v146, v204
	v_max_f32_e32 v204, 0, v180
	v_fmac_f32_e32 v201, v147, v208
	v_max_f32_e32 v208, 0, v181
	v_fmac_f32_e32 v201, v148, v204
	v_max_f32_e32 v204, 0, v182
	v_fmac_f32_e32 v201, v149, v208
	v_max_f32_e32 v208, 0, v183
	v_fmac_f32_e32 v201, v150, v204
	v_max_f32_e32 v204, 0, v184
	v_fmac_f32_e32 v201, v151, v208
	v_max_f32_e32 v208, 0, v185
	v_fmac_f32_e32 v201, v152, v204
	v_max_f32_e32 v204, 0, v186
	v_fmac_f32_e32 v201, v153, v208
	v_max_f32_e32 v208, 0, v187
	v_fmac_f32_e32 v201, v154, v204
	v_max_f32_e32 v204, 0, v188
	v_fmac_f32_e32 v201, v155, v208
	v_max_f32_e32 v208, 0, v189
	v_fmac_f32_e32 v201, v156, v204
	v_max_f32_e32 v204, 0, v190
	v_fmac_f32_e32 v201, v157, v208
	v_max_f32_e32 v208, 0, v191
	v_fmac_f32_e32 v201, v158, v204
	v_fmac_f32_e32 v201, v159, v208
	v_cndmask_b32_e32 v201, v61, v201, vcc
	v_ashrrev_i32_e32 v207, 31, v201
	v_or_b32_e32 v207, 0x80000000, v207
	v_xor_b32_e32 v81, v201, v207
	s_cmp_le_u32 s15, 18
	s_cbranch_scc1 .Lidx_search
	s_cmp_le_u32 s15, 19
	s_cbranch_scc1 .Lidx_p19
	global_load_dwordx4 v[2:5], v57, s[20:21]
	global_load_dwordx4 v[6:9], v57, s[20:21] offset:1024
	global_load_dwordx4 v[10:13], v57, s[20:21] offset:2048
	global_load_dwordx4 v[14:17], v57, s[20:21] offset:3072
	s_add_u32 s20, s20, 0x1000
	s_addc_u32 s21, s21, 0
	s_waitcnt vmcnt(8)
	v_mfma_f32_32x32x16_bf16 v[176:191], v[128:131], v[18:21], 0
	v_mfma_f32_32x32x16_bf16 v[176:191], v[132:135], v[22:25], v[176:191]
	v_mfma_f32_32x32x16_bf16 v[176:191], v[136:139], v[26:29], v[176:191]
	v_mfma_f32_32x32x16_bf16 v[176:191], v[140:143], v[30:33], v[176:191]
.Lidx_p19:
	v_cmp_le_i32_e32 vcc, 0x240, v59
	v_max_f32_e32 v204, 0, v160
	v_max_f32_e32 v208, 0, v161
	v_fma_f32 v201, v144, v204, 0
	v_max_f32_e32 v204, 0, v162
	v_fmac_f32_e32 v201, v145, v208
	v_max_f32_e32 v208, 0, v163
	v_fmac_f32_e32 v201, v146, v204
	v_max_f32_e32 v204, 0, v164
	v_fmac_f32_e32 v201, v147, v208
	v_max_f32_e32 v208, 0, v165
	v_fmac_f32_e32 v201, v148, v204
	v_max_f32_e32 v204, 0, v166
	v_fmac_f32_e32 v201, v149, v208
	v_max_f32_e32 v208, 0, v167
	v_fmac_f32_e32 v201, v150, v204
	v_max_f32_e32 v204, 0, v168
	v_fmac_f32_e32 v201, v151, v208
	v_max_f32_e32 v208, 0, v169
	v_fmac_f32_e32 v201, v152, v204
	v_max_f32_e32 v204, 0, v170
	v_fmac_f32_e32 v201, v153, v208
	v_max_f32_e32 v208, 0, v171
	v_fmac_f32_e32 v201, v154, v204
	v_max_f32_e32 v204, 0, v172
	v_fmac_f32_e32 v201, v155, v208
	v_max_f32_e32 v208, 0, v173
	v_fmac_f32_e32 v201, v156, v204
	v_max_f32_e32 v204, 0, v174
	v_fmac_f32_e32 v201, v157, v208
	v_max_f32_e32 v208, 0, v175
	v_fmac_f32_e32 v201, v158, v204
	v_fmac_f32_e32 v201, v159, v208
	v_cndmask_b32_e32 v201, v61, v201, vcc
	v_ashrrev_i32_e32 v207, 31, v201
	v_or_b32_e32 v207, 0x80000000, v207
	v_xor_b32_e32 v82, v201, v207
	s_cmp_le_u32 s15, 19
	s_cbranch_scc1 .Lidx_search
	s_cmp_le_u32 s15, 20
	s_cbranch_scc1 .Lidx_p20
	global_load_dwordx4 v[18:21], v57, s[20:21]
	global_load_dwordx4 v[22:25], v57, s[20:21] offset:1024
	global_load_dwordx4 v[26:29], v57, s[20:21] offset:2048
	global_load_dwordx4 v[30:33], v57, s[20:21] offset:3072
	s_add_u32 s20, s20, 0x1000
	s_addc_u32 s21, s21, 0
	s_waitcnt vmcnt(8)
	v_mfma_f32_32x32x16_bf16 v[160:175], v[128:131], v[34:37], 0
	v_mfma_f32_32x32x16_bf16 v[160:175], v[132:135], v[38:41], v[160:175]
	v_mfma_f32_32x32x16_bf16 v[160:175], v[136:139], v[42:45], v[160:175]
	v_mfma_f32_32x32x16_bf16 v[160:175], v[140:143], v[46:49], v[160:175]
.Lidx_p20:
	v_cmp_le_i32_e32 vcc, 0x260, v59
	v_max_f32_e32 v204, 0, v176
	v_max_f32_e32 v208, 0, v177
	v_fma_f32 v201, v144, v204, 0
	v_max_f32_e32 v204, 0, v178
	v_fmac_f32_e32 v201, v145, v208
	v_max_f32_e32 v208, 0, v179
	v_fmac_f32_e32 v201, v146, v204
	v_max_f32_e32 v204, 0, v180
	v_fmac_f32_e32 v201, v147, v208
	v_max_f32_e32 v208, 0, v181
	v_fmac_f32_e32 v201, v148, v204
	v_max_f32_e32 v204, 0, v182
	v_fmac_f32_e32 v201, v149, v208
	v_max_f32_e32 v208, 0, v183
	v_fmac_f32_e32 v201, v150, v204
	v_max_f32_e32 v204, 0, v184
	v_fmac_f32_e32 v201, v151, v208
	v_max_f32_e32 v208, 0, v185
	v_fmac_f32_e32 v201, v152, v204
	v_max_f32_e32 v204, 0, v186
	v_fmac_f32_e32 v201, v153, v208
	v_max_f32_e32 v208, 0, v187
	v_fmac_f32_e32 v201, v154, v204
	v_max_f32_e32 v204, 0, v188
	v_fmac_f32_e32 v201, v155, v208
	v_max_f32_e32 v208, 0, v189
	v_fmac_f32_e32 v201, v156, v204
	v_max_f32_e32 v204, 0, v190
	v_fmac_f32_e32 v201, v157, v208
	v_max_f32_e32 v208, 0, v191
	v_fmac_f32_e32 v201, v158, v204
	v_fmac_f32_e32 v201, v159, v208
	v_cndmask_b32_e32 v201, v61, v201, vcc
	v_ashrrev_i32_e32 v207, 31, v201
	v_or_b32_e32 v207, 0x80000000, v207
	v_xor_b32_e32 v83, v201, v207
	s_cmp_le_u32 s15, 20
	s_cbranch_scc1 .Lidx_search
	s_cmp_le_u32 s15, 21
	s_cbranch_scc1 .Lidx_p21
	global_load_dwordx4 v[34:37], v57, s[20:21]
	global_load_dwordx4 v[38:41], v57, s[20:21] offset:1024
	global_load_dwordx4 v[42:45], v57, s[20:21] offset:2048
	global_load_dwordx4 v[46:49], v57, s[20:21] offset:3072
	s_add_u32 s20, s20, 0x1000
	s_addc_u32 s21, s21, 0
	s_waitcnt vmcnt(8)
	v_mfma_f32_32x32x16_bf16 v[176:191], v[128:131], v[2:5], 0
	v_mfma_f32_32x32x16_bf16 v[176:191], v[132:135], v[6:9], v[176:191]
	v_mfma_f32_32x32x16_bf16 v[176:191], v[136:139], v[10:13], v[176:191]
	v_mfma_f32_32x32x16_bf16 v[176:191], v[140:143], v[14:17], v[176:191]
.Lidx_p21:
	v_cmp_le_i32_e32 vcc, 0x280, v59
	v_max_f32_e32 v204, 0, v160
	v_max_f32_e32 v208, 0, v161
	v_fma_f32 v201, v144, v204, 0
	v_max_f32_e32 v204, 0, v162
	v_fmac_f32_e32 v201, v145, v208
	v_max_f32_e32 v208, 0, v163
	v_fmac_f32_e32 v201, v146, v204
	v_max_f32_e32 v204, 0, v164
	v_fmac_f32_e32 v201, v147, v208
	v_max_f32_e32 v208, 0, v165
	v_fmac_f32_e32 v201, v148, v204
	v_max_f32_e32 v204, 0, v166
	v_fmac_f32_e32 v201, v149, v208
	v_max_f32_e32 v208, 0, v167
	v_fmac_f32_e32 v201, v150, v204
	v_max_f32_e32 v204, 0, v168
	v_fmac_f32_e32 v201, v151, v208
	v_max_f32_e32 v208, 0, v169
	v_fmac_f32_e32 v201, v152, v204
	v_max_f32_e32 v204, 0, v170
	v_fmac_f32_e32 v201, v153, v208
	v_max_f32_e32 v208, 0, v171
	v_fmac_f32_e32 v201, v154, v204
	v_max_f32_e32 v204, 0, v172
	v_fmac_f32_e32 v201, v155, v208
	v_max_f32_e32 v208, 0, v173
	v_fmac_f32_e32 v201, v156, v204
	v_max_f32_e32 v204, 0, v174
	v_fmac_f32_e32 v201, v157, v208
	v_max_f32_e32 v208, 0, v175
	v_fmac_f32_e32 v201, v158, v204
	v_fmac_f32_e32 v201, v159, v208
	v_cndmask_b32_e32 v201, v61, v201, vcc
	v_ashrrev_i32_e32 v207, 31, v201
	v_or_b32_e32 v207, 0x80000000, v207
	v_xor_b32_e32 v84, v201, v207
	s_cmp_le_u32 s15, 21
	s_cbranch_scc1 .Lidx_search
	s_cmp_le_u32 s15, 22
	s_cbranch_scc1 .Lidx_p22
	global_load_dwordx4 v[2:5], v57, s[20:21]
	global_load_dwordx4 v[6:9], v57, s[20:21] offset:1024
	global_load_dwordx4 v[10:13], v57, s[20:21] offset:2048
	global_load_dwordx4 v[14:17], v57, s[20:21] offset:3072
	s_add_u32 s20, s20, 0x1000
	s_addc_u32 s21, s21, 0
	s_waitcnt vmcnt(8)
	v_mfma_f32_32x32x16_bf16 v[160:175], v[128:131], v[18:21], 0
	v_mfma_f32_32x32x16_bf16 v[160:175], v[132:135], v[22:25], v[160:175]
	v_mfma_f32_32x32x16_bf16 v[160:175], v[136:139], v[26:29], v[160:175]
	v_mfma_f32_32x32x16_bf16 v[160:175], v[140:143], v[30:33], v[160:175]
.Lidx_p22:
	v_cmp_le_i32_e32 vcc, 0x2a0, v59
	v_max_f32_e32 v204, 0, v176
	v_max_f32_e32 v208, 0, v177
	v_fma_f32 v201, v144, v204, 0
	v_max_f32_e32 v204, 0, v178
	v_fmac_f32_e32 v201, v145, v208
	v_max_f32_e32 v208, 0, v179
	v_fmac_f32_e32 v201, v146, v204
	v_max_f32_e32 v204, 0, v180
	v_fmac_f32_e32 v201, v147, v208
	v_max_f32_e32 v208, 0, v181
	v_fmac_f32_e32 v201, v148, v204
	v_max_f32_e32 v204, 0, v182
	v_fmac_f32_e32 v201, v149, v208
	v_max_f32_e32 v208, 0, v183
	v_fmac_f32_e32 v201, v150, v204
	v_max_f32_e32 v204, 0, v184
	v_fmac_f32_e32 v201, v151, v208
	v_max_f32_e32 v208, 0, v185
	v_fmac_f32_e32 v201, v152, v204
	v_max_f32_e32 v204, 0, v186
	v_fmac_f32_e32 v201, v153, v208
	v_max_f32_e32 v208, 0, v187
	v_fmac_f32_e32 v201, v154, v204
	v_max_f32_e32 v204, 0, v188
	v_fmac_f32_e32 v201, v155, v208
	v_max_f32_e32 v208, 0, v189
	v_fmac_f32_e32 v201, v156, v204
	v_max_f32_e32 v204, 0, v190
	v_fmac_f32_e32 v201, v157, v208
	v_max_f32_e32 v208, 0, v191
	v_fmac_f32_e32 v201, v158, v204
	v_fmac_f32_e32 v201, v159, v208
	v_cndmask_b32_e32 v201, v61, v201, vcc
	v_ashrrev_i32_e32 v207, 31, v201
	v_or_b32_e32 v207, 0x80000000, v207
	v_xor_b32_e32 v85, v201, v207
	s_cmp_le_u32 s15, 22
	s_cbranch_scc1 .Lidx_search
	s_cmp_le_u32 s15, 23
	s_cbranch_scc1 .Lidx_p23
	global_load_dwordx4 v[18:21], v57, s[20:21]
	global_load_dwordx4 v[22:25], v57, s[20:21] offset:1024
	global_load_dwordx4 v[26:29], v57, s[20:21] offset:2048
	global_load_dwordx4 v[30:33], v57, s[20:21] offset:3072
	s_add_u32 s20, s20, 0x1000
	s_addc_u32 s21, s21, 0
	s_waitcnt vmcnt(8)
	v_mfma_f32_32x32x16_bf16 v[176:191], v[128:131], v[34:37], 0
	v_mfma_f32_32x32x16_bf16 v[176:191], v[132:135], v[38:41], v[176:191]
	v_mfma_f32_32x32x16_bf16 v[176:191], v[136:139], v[42:45], v[176:191]
	v_mfma_f32_32x32x16_bf16 v[176:191], v[140:143], v[46:49], v[176:191]
.Lidx_p23:
	v_cmp_le_i32_e32 vcc, 0x2c0, v59
	v_max_f32_e32 v204, 0, v160
	v_max_f32_e32 v208, 0, v161
	v_fma_f32 v201, v144, v204, 0
	v_max_f32_e32 v204, 0, v162
	v_fmac_f32_e32 v201, v145, v208
	v_max_f32_e32 v208, 0, v163
	v_fmac_f32_e32 v201, v146, v204
	v_max_f32_e32 v204, 0, v164
	v_fmac_f32_e32 v201, v147, v208
	v_max_f32_e32 v208, 0, v165
	v_fmac_f32_e32 v201, v148, v204
	v_max_f32_e32 v204, 0, v166
	v_fmac_f32_e32 v201, v149, v208
	v_max_f32_e32 v208, 0, v167
	v_fmac_f32_e32 v201, v150, v204
	v_max_f32_e32 v204, 0, v168
	v_fmac_f32_e32 v201, v151, v208
	v_max_f32_e32 v208, 0, v169
	v_fmac_f32_e32 v201, v152, v204
	v_max_f32_e32 v204, 0, v170
	v_fmac_f32_e32 v201, v153, v208
	v_max_f32_e32 v208, 0, v171
	v_fmac_f32_e32 v201, v154, v204
	v_max_f32_e32 v204, 0, v172
	v_fmac_f32_e32 v201, v155, v208
	v_max_f32_e32 v208, 0, v173
	v_fmac_f32_e32 v201, v156, v204
	v_max_f32_e32 v204, 0, v174
	v_fmac_f32_e32 v201, v157, v208
	v_max_f32_e32 v208, 0, v175
	v_fmac_f32_e32 v201, v158, v204
	v_fmac_f32_e32 v201, v159, v208
	v_cndmask_b32_e32 v201, v61, v201, vcc
	v_ashrrev_i32_e32 v207, 31, v201
	v_or_b32_e32 v207, 0x80000000, v207
	v_xor_b32_e32 v86, v201, v207
	s_cmp_le_u32 s15, 23
	s_cbranch_scc1 .Lidx_search
	s_cmp_le_u32 s15, 24
	s_cbranch_scc1 .Lidx_p24
	global_load_dwordx4 v[34:37], v57, s[20:21]
	global_load_dwordx4 v[38:41], v57, s[20:21] offset:1024
	global_load_dwordx4 v[42:45], v57, s[20:21] offset:2048
	global_load_dwordx4 v[46:49], v57, s[20:21] offset:3072
	s_add_u32 s20, s20, 0x1000
	s_addc_u32 s21, s21, 0
	s_waitcnt vmcnt(8)
	v_mfma_f32_32x32x16_bf16 v[160:175], v[128:131], v[2:5], 0
	v_mfma_f32_32x32x16_bf16 v[160:175], v[132:135], v[6:9], v[160:175]
	v_mfma_f32_32x32x16_bf16 v[160:175], v[136:139], v[10:13], v[160:175]
	v_mfma_f32_32x32x16_bf16 v[160:175], v[140:143], v[14:17], v[160:175]
.Lidx_p24:
	v_cmp_le_i32_e32 vcc, 0x2e0, v59
	v_max_f32_e32 v204, 0, v176
	v_max_f32_e32 v208, 0, v177
	v_fma_f32 v201, v144, v204, 0
	v_max_f32_e32 v204, 0, v178
	v_fmac_f32_e32 v201, v145, v208
	v_max_f32_e32 v208, 0, v179
	v_fmac_f32_e32 v201, v146, v204
	v_max_f32_e32 v204, 0, v180
	v_fmac_f32_e32 v201, v147, v208
	v_max_f32_e32 v208, 0, v181
	v_fmac_f32_e32 v201, v148, v204
	v_max_f32_e32 v204, 0, v182
	v_fmac_f32_e32 v201, v149, v208
	v_max_f32_e32 v208, 0, v183
	v_fmac_f32_e32 v201, v150, v204
	v_max_f32_e32 v204, 0, v184
	v_fmac_f32_e32 v201, v151, v208
	v_max_f32_e32 v208, 0, v185
	v_fmac_f32_e32 v201, v152, v204
	v_max_f32_e32 v204, 0, v186
	v_fmac_f32_e32 v201, v153, v208
	v_max_f32_e32 v208, 0, v187
	v_fmac_f32_e32 v201, v154, v204
	v_max_f32_e32 v204, 0, v188
	v_fmac_f32_e32 v201, v155, v208
	v_max_f32_e32 v208, 0, v189
	v_fmac_f32_e32 v201, v156, v204
	v_max_f32_e32 v204, 0, v190
	v_fmac_f32_e32 v201, v157, v208
	v_max_f32_e32 v208, 0, v191
	v_fmac_f32_e32 v201, v158, v204
	v_fmac_f32_e32 v201, v159, v208
	v_cndmask_b32_e32 v201, v61, v201, vcc
	v_ashrrev_i32_e32 v207, 31, v201
	v_or_b32_e32 v207, 0x80000000, v207
	v_xor_b32_e32 v87, v201, v207
	s_cmp_le_u32 s15, 24
	s_cbranch_scc1 .Lidx_search
	s_cmp_le_u32 s15, 25
	s_cbranch_scc1 .Lidx_p25
	global_load_dwordx4 v[2:5], v57, s[20:21]
	global_load_dwordx4 v[6:9], v57, s[20:21] offset:1024
	global_load_dwordx4 v[10:13], v57, s[20:21] offset:2048
	global_load_dwordx4 v[14:17], v57, s[20:21] offset:3072
	s_add_u32 s20, s20, 0x1000
	s_addc_u32 s21, s21, 0
	s_waitcnt vmcnt(8)
	v_mfma_f32_32x32x16_bf16 v[176:191], v[128:131], v[18:21], 0
	v_mfma_f32_32x32x16_bf16 v[176:191], v[132:135], v[22:25], v[176:191]
	v_mfma_f32_32x32x16_bf16 v[176:191], v[136:139], v[26:29], v[176:191]
	v_mfma_f32_32x32x16_bf16 v[176:191], v[140:143], v[30:33], v[176:191]
.Lidx_p25:
	v_cmp_le_i32_e32 vcc, 0x300, v59
	v_max_f32_e32 v204, 0, v160
	v_max_f32_e32 v208, 0, v161
	v_fma_f32 v201, v144, v204, 0
	v_max_f32_e32 v204, 0, v162
	v_fmac_f32_e32 v201, v145, v208
	v_max_f32_e32 v208, 0, v163
	v_fmac_f32_e32 v201, v146, v204
	v_max_f32_e32 v204, 0, v164
	v_fmac_f32_e32 v201, v147, v208
	v_max_f32_e32 v208, 0, v165
	v_fmac_f32_e32 v201, v148, v204
	v_max_f32_e32 v204, 0, v166
	v_fmac_f32_e32 v201, v149, v208
	v_max_f32_e32 v208, 0, v167
	v_fmac_f32_e32 v201, v150, v204
	v_max_f32_e32 v204, 0, v168
	v_fmac_f32_e32 v201, v151, v208
	v_max_f32_e32 v208, 0, v169
	v_fmac_f32_e32 v201, v152, v204
	v_max_f32_e32 v204, 0, v170
	v_fmac_f32_e32 v201, v153, v208
	v_max_f32_e32 v208, 0, v171
	v_fmac_f32_e32 v201, v154, v204
	v_max_f32_e32 v204, 0, v172
	v_fmac_f32_e32 v201, v155, v208
	v_max_f32_e32 v208, 0, v173
	v_fmac_f32_e32 v201, v156, v204
	v_max_f32_e32 v204, 0, v174
	v_fmac_f32_e32 v201, v157, v208
	v_max_f32_e32 v208, 0, v175
	v_fmac_f32_e32 v201, v158, v204
	v_fmac_f32_e32 v201, v159, v208
	v_cndmask_b32_e32 v201, v61, v201, vcc
	v_ashrrev_i32_e32 v207, 31, v201
	v_or_b32_e32 v207, 0x80000000, v207
	v_xor_b32_e32 v88, v201, v207
	s_cmp_le_u32 s15, 25
	s_cbranch_scc1 .Lidx_search
	s_cmp_le_u32 s15, 26
	s_cbranch_scc1 .Lidx_p26
	global_load_dwordx4 v[18:21], v57, s[20:21]
	global_load_dwordx4 v[22:25], v57, s[20:21] offset:1024
	global_load_dwordx4 v[26:29], v57, s[20:21] offset:2048
	global_load_dwordx4 v[30:33], v57, s[20:21] offset:3072
	s_add_u32 s20, s20, 0x1000
	s_addc_u32 s21, s21, 0
	s_waitcnt vmcnt(8)
	v_mfma_f32_32x32x16_bf16 v[160:175], v[128:131], v[34:37], 0
	v_mfma_f32_32x32x16_bf16 v[160:175], v[132:135], v[38:41], v[160:175]
	v_mfma_f32_32x32x16_bf16 v[160:175], v[136:139], v[42:45], v[160:175]
	v_mfma_f32_32x32x16_bf16 v[160:175], v[140:143], v[46:49], v[160:175]
.Lidx_p26:
	v_cmp_le_i32_e32 vcc, 0x320, v59
	v_max_f32_e32 v204, 0, v176
	v_max_f32_e32 v208, 0, v177
	v_fma_f32 v201, v144, v204, 0
	v_max_f32_e32 v204, 0, v178
	v_fmac_f32_e32 v201, v145, v208
	v_max_f32_e32 v208, 0, v179
	v_fmac_f32_e32 v201, v146, v204
	v_max_f32_e32 v204, 0, v180
	v_fmac_f32_e32 v201, v147, v208
	v_max_f32_e32 v208, 0, v181
	v_fmac_f32_e32 v201, v148, v204
	v_max_f32_e32 v204, 0, v182
	v_fmac_f32_e32 v201, v149, v208
	v_max_f32_e32 v208, 0, v183
	v_fmac_f32_e32 v201, v150, v204
	v_max_f32_e32 v204, 0, v184
	v_fmac_f32_e32 v201, v151, v208
	v_max_f32_e32 v208, 0, v185
	v_fmac_f32_e32 v201, v152, v204
	v_max_f32_e32 v204, 0, v186
	v_fmac_f32_e32 v201, v153, v208
	v_max_f32_e32 v208, 0, v187
	v_fmac_f32_e32 v201, v154, v204
	v_max_f32_e32 v204, 0, v188
	v_fmac_f32_e32 v201, v155, v208
	v_max_f32_e32 v208, 0, v189
	v_fmac_f32_e32 v201, v156, v204
	v_max_f32_e32 v204, 0, v190
	v_fmac_f32_e32 v201, v157, v208
	v_max_f32_e32 v208, 0, v191
	v_fmac_f32_e32 v201, v158, v204
	v_fmac_f32_e32 v201, v159, v208
	v_cndmask_b32_e32 v201, v61, v201, vcc
	v_ashrrev_i32_e32 v207, 31, v201
	v_or_b32_e32 v207, 0x80000000, v207
	v_xor_b32_e32 v89, v201, v207
	s_cmp_le_u32 s15, 26
	s_cbranch_scc1 .Lidx_search
	s_cmp_le_u32 s15, 27
	s_cbranch_scc1 .Lidx_p27
	global_load_dwordx4 v[34:37], v57, s[20:21]
	global_load_dwordx4 v[38:41], v57, s[20:21] offset:1024
	global_load_dwordx4 v[42:45], v57, s[20:21] offset:2048
	global_load_dwordx4 v[46:49], v57, s[20:21] offset:3072
	s_add_u32 s20, s20, 0x1000
	s_addc_u32 s21, s21, 0
	s_waitcnt vmcnt(8)
	v_mfma_f32_32x32x16_bf16 v[176:191], v[128:131], v[2:5], 0
	v_mfma_f32_32x32x16_bf16 v[176:191], v[132:135], v[6:9], v[176:191]
	v_mfma_f32_32x32x16_bf16 v[176:191], v[136:139], v[10:13], v[176:191]
	v_mfma_f32_32x32x16_bf16 v[176:191], v[140:143], v[14:17], v[176:191]
.Lidx_p27:
	v_cmp_le_i32_e32 vcc, 0x340, v59
	v_max_f32_e32 v204, 0, v160
	v_max_f32_e32 v208, 0, v161
	v_fma_f32 v201, v144, v204, 0
	v_max_f32_e32 v204, 0, v162
	v_fmac_f32_e32 v201, v145, v208
	v_max_f32_e32 v208, 0, v163
	v_fmac_f32_e32 v201, v146, v204
	v_max_f32_e32 v204, 0, v164
	v_fmac_f32_e32 v201, v147, v208
	v_max_f32_e32 v208, 0, v165
	v_fmac_f32_e32 v201, v148, v204
	v_max_f32_e32 v204, 0, v166
	v_fmac_f32_e32 v201, v149, v208
	v_max_f32_e32 v208, 0, v167
	v_fmac_f32_e32 v201, v150, v204
	v_max_f32_e32 v204, 0, v168
	v_fmac_f32_e32 v201, v151, v208
	v_max_f32_e32 v208, 0, v169
	v_fmac_f32_e32 v201, v152, v204
	v_max_f32_e32 v204, 0, v170
	v_fmac_f32_e32 v201, v153, v208
	v_max_f32_e32 v208, 0, v171
	v_fmac_f32_e32 v201, v154, v204
	v_max_f32_e32 v204, 0, v172
	v_fmac_f32_e32 v201, v155, v208
	v_max_f32_e32 v208, 0, v173
	v_fmac_f32_e32 v201, v156, v204
	v_max_f32_e32 v204, 0, v174
	v_fmac_f32_e32 v201, v157, v208
	v_max_f32_e32 v208, 0, v175
	v_fmac_f32_e32 v201, v158, v204
	v_fmac_f32_e32 v201, v159, v208
	v_cndmask_b32_e32 v201, v61, v201, vcc
	v_ashrrev_i32_e32 v207, 31, v201
	v_or_b32_e32 v207, 0x80000000, v207
	v_xor_b32_e32 v90, v201, v207
	s_cmp_le_u32 s15, 27
	s_cbranch_scc1 .Lidx_search
	s_cmp_le_u32 s15, 28
	s_cbranch_scc1 .Lidx_p28
	global_load_dwordx4 v[2:5], v57, s[20:21]
	global_load_dwordx4 v[6:9], v57, s[20:21] offset:1024
	global_load_dwordx4 v[10:13], v57, s[20:21] offset:2048
	global_load_dwordx4 v[14:17], v57, s[20:21] offset:3072
	s_add_u32 s20, s20, 0x1000
	s_addc_u32 s21, s21, 0
	s_waitcnt vmcnt(8)
	v_mfma_f32_32x32x16_bf16 v[160:175], v[128:131], v[18:21], 0
	v_mfma_f32_32x32x16_bf16 v[160:175], v[132:135], v[22:25], v[160:175]
	v_mfma_f32_32x32x16_bf16 v[160:175], v[136:139], v[26:29], v[160:175]
	v_mfma_f32_32x32x16_bf16 v[160:175], v[140:143], v[30:33], v[160:175]
.Lidx_p28:
	v_cmp_le_i32_e32 vcc, 0x360, v59
	v_max_f32_e32 v204, 0, v176
	v_max_f32_e32 v208, 0, v177
	v_fma_f32 v201, v144, v204, 0
	v_max_f32_e32 v204, 0, v178
	v_fmac_f32_e32 v201, v145, v208
	v_max_f32_e32 v208, 0, v179
	v_fmac_f32_e32 v201, v146, v204
	v_max_f32_e32 v204, 0, v180
	v_fmac_f32_e32 v201, v147, v208
	v_max_f32_e32 v208, 0, v181
	v_fmac_f32_e32 v201, v148, v204
	v_max_f32_e32 v204, 0, v182
	v_fmac_f32_e32 v201, v149, v208
	v_max_f32_e32 v208, 0, v183
	v_fmac_f32_e32 v201, v150, v204
	v_max_f32_e32 v204, 0, v184
	v_fmac_f32_e32 v201, v151, v208
	v_max_f32_e32 v208, 0, v185
	v_fmac_f32_e32 v201, v152, v204
	v_max_f32_e32 v204, 0, v186
	v_fmac_f32_e32 v201, v153, v208
	v_max_f32_e32 v208, 0, v187
	v_fmac_f32_e32 v201, v154, v204
	v_max_f32_e32 v204, 0, v188
	v_fmac_f32_e32 v201, v155, v208
	v_max_f32_e32 v208, 0, v189
	v_fmac_f32_e32 v201, v156, v204
	v_max_f32_e32 v204, 0, v190
	v_fmac_f32_e32 v201, v157, v208
	v_max_f32_e32 v208, 0, v191
	v_fmac_f32_e32 v201, v158, v204
	v_fmac_f32_e32 v201, v159, v208
	v_cndmask_b32_e32 v201, v61, v201, vcc
	v_ashrrev_i32_e32 v207, 31, v201
	v_or_b32_e32 v207, 0x80000000, v207
	v_xor_b32_e32 v91, v201, v207
	s_cmp_le_u32 s15, 28
	s_cbranch_scc1 .Lidx_search
	s_cmp_le_u32 s15, 29
	s_cbranch_scc1 .Lidx_p29
	global_load_dwordx4 v[18:21], v57, s[20:21]
	global_load_dwordx4 v[22:25], v57, s[20:21] offset:1024
	global_load_dwordx4 v[26:29], v57, s[20:21] offset:2048
	global_load_dwordx4 v[30:33], v57, s[20:21] offset:3072
	s_add_u32 s20, s20, 0x1000
	s_addc_u32 s21, s21, 0
	s_waitcnt vmcnt(8)
	v_mfma_f32_32x32x16_bf16 v[176:191], v[128:131], v[34:37], 0
	v_mfma_f32_32x32x16_bf16 v[176:191], v[132:135], v[38:41], v[176:191]
	v_mfma_f32_32x32x16_bf16 v[176:191], v[136:139], v[42:45], v[176:191]
	v_mfma_f32_32x32x16_bf16 v[176:191], v[140:143], v[46:49], v[176:191]
.Lidx_p29:
	v_cmp_le_i32_e32 vcc, 0x380, v59
	v_max_f32_e32 v204, 0, v160
	v_max_f32_e32 v208, 0, v161
	v_fma_f32 v201, v144, v204, 0
	v_max_f32_e32 v204, 0, v162
	v_fmac_f32_e32 v201, v145, v208
	v_max_f32_e32 v208, 0, v163
	v_fmac_f32_e32 v201, v146, v204
	v_max_f32_e32 v204, 0, v164
	v_fmac_f32_e32 v201, v147, v208
	v_max_f32_e32 v208, 0, v165
	v_fmac_f32_e32 v201, v148, v204
	v_max_f32_e32 v204, 0, v166
	v_fmac_f32_e32 v201, v149, v208
	v_max_f32_e32 v208, 0, v167
	v_fmac_f32_e32 v201, v150, v204
	v_max_f32_e32 v204, 0, v168
	v_fmac_f32_e32 v201, v151, v208
	v_max_f32_e32 v208, 0, v169
	v_fmac_f32_e32 v201, v152, v204
	v_max_f32_e32 v204, 0, v170
	v_fmac_f32_e32 v201, v153, v208
	v_max_f32_e32 v208, 0, v171
	v_fmac_f32_e32 v201, v154, v204
	v_max_f32_e32 v204, 0, v172
	v_fmac_f32_e32 v201, v155, v208
	v_max_f32_e32 v208, 0, v173
	v_fmac_f32_e32 v201, v156, v204
	v_max_f32_e32 v204, 0, v174
	v_fmac_f32_e32 v201, v157, v208
	v_max_f32_e32 v208, 0, v175
	v_fmac_f32_e32 v201, v158, v204
	v_fmac_f32_e32 v201, v159, v208
	v_cndmask_b32_e32 v201, v61, v201, vcc
	v_ashrrev_i32_e32 v207, 31, v201
	v_or_b32_e32 v207, 0x80000000, v207
	v_xor_b32_e32 v92, v201, v207
	s_cmp_le_u32 s15, 29
	s_cbranch_scc1 .Lidx_search
	s_cmp_le_u32 s15, 30
	s_cbranch_scc1 .Lidx_p30
	global_load_dwordx4 v[34:37], v57, s[20:21]
	global_load_dwordx4 v[38:41], v57, s[20:21] offset:1024
	global_load_dwordx4 v[42:45], v57, s[20:21] offset:2048
	global_load_dwordx4 v[46:49], v57, s[20:21] offset:3072
	s_add_u32 s20, s20, 0x1000
	s_addc_u32 s21, s21, 0
	s_waitcnt vmcnt(8)
	v_mfma_f32_32x32x16_bf16 v[160:175], v[128:131], v[2:5], 0
	v_mfma_f32_32x32x16_bf16 v[160:175], v[132:135], v[6:9], v[160:175]
	v_mfma_f32_32x32x16_bf16 v[160:175], v[136:139], v[10:13], v[160:175]
	v_mfma_f32_32x32x16_bf16 v[160:175], v[140:143], v[14:17], v[160:175]
.Lidx_p30:
	v_cmp_le_i32_e32 vcc, 0x3a0, v59
	v_max_f32_e32 v204, 0, v176
	v_max_f32_e32 v208, 0, v177
	v_fma_f32 v201, v144, v204, 0
	v_max_f32_e32 v204, 0, v178
	v_fmac_f32_e32 v201, v145, v208
	v_max_f32_e32 v208, 0, v179
	v_fmac_f32_e32 v201, v146, v204
	v_max_f32_e32 v204, 0, v180
	v_fmac_f32_e32 v201, v147, v208
	v_max_f32_e32 v208, 0, v181
	v_fmac_f32_e32 v201, v148, v204
	v_max_f32_e32 v204, 0, v182
	v_fmac_f32_e32 v201, v149, v208
	v_max_f32_e32 v208, 0, v183
	v_fmac_f32_e32 v201, v150, v204
	v_max_f32_e32 v204, 0, v184
	v_fmac_f32_e32 v201, v151, v208
	v_max_f32_e32 v208, 0, v185
	v_fmac_f32_e32 v201, v152, v204
	v_max_f32_e32 v204, 0, v186
	v_fmac_f32_e32 v201, v153, v208
	v_max_f32_e32 v208, 0, v187
	v_fmac_f32_e32 v201, v154, v204
	v_max_f32_e32 v204, 0, v188
	v_fmac_f32_e32 v201, v155, v208
	v_max_f32_e32 v208, 0, v189
	v_fmac_f32_e32 v201, v156, v204
	v_max_f32_e32 v204, 0, v190
	v_fmac_f32_e32 v201, v157, v208
	v_max_f32_e32 v208, 0, v191
	v_fmac_f32_e32 v201, v158, v204
	v_fmac_f32_e32 v201, v159, v208
	v_cndmask_b32_e32 v201, v61, v201, vcc
	v_ashrrev_i32_e32 v207, 31, v201
	v_or_b32_e32 v207, 0x80000000, v207
	v_xor_b32_e32 v93, v201, v207
	s_cmp_le_u32 s15, 30
	s_cbranch_scc1 .Lidx_search
	s_cmp_le_u32 s15, 31
	s_cbranch_scc1 .Lidx_p31
	global_load_dwordx4 v[2:5], v57, s[20:21]
	global_load_dwordx4 v[6:9], v57, s[20:21] offset:1024
	global_load_dwordx4 v[10:13], v57, s[20:21] offset:2048
	global_load_dwordx4 v[14:17], v57, s[20:21] offset:3072
	s_add_u32 s20, s20, 0x1000
	s_addc_u32 s21, s21, 0
	s_waitcnt vmcnt(8)
	v_mfma_f32_32x32x16_bf16 v[176:191], v[128:131], v[18:21], 0
	v_mfma_f32_32x32x16_bf16 v[176:191], v[132:135], v[22:25], v[176:191]
	v_mfma_f32_32x32x16_bf16 v[176:191], v[136:139], v[26:29], v[176:191]
	v_mfma_f32_32x32x16_bf16 v[176:191], v[140:143], v[30:33], v[176:191]
.Lidx_p31:
	v_cmp_le_i32_e32 vcc, 0x3c0, v59
	v_max_f32_e32 v204, 0, v160
	v_max_f32_e32 v208, 0, v161
	v_fma_f32 v201, v144, v204, 0
	v_max_f32_e32 v204, 0, v162
	v_fmac_f32_e32 v201, v145, v208
	v_max_f32_e32 v208, 0, v163
	v_fmac_f32_e32 v201, v146, v204
	v_max_f32_e32 v204, 0, v164
	v_fmac_f32_e32 v201, v147, v208
	v_max_f32_e32 v208, 0, v165
	v_fmac_f32_e32 v201, v148, v204
	v_max_f32_e32 v204, 0, v166
	v_fmac_f32_e32 v201, v149, v208
	v_max_f32_e32 v208, 0, v167
	v_fmac_f32_e32 v201, v150, v204
	v_max_f32_e32 v204, 0, v168
	v_fmac_f32_e32 v201, v151, v208
	v_max_f32_e32 v208, 0, v169
	v_fmac_f32_e32 v201, v152, v204
	v_max_f32_e32 v204, 0, v170
	v_fmac_f32_e32 v201, v153, v208
	v_max_f32_e32 v208, 0, v171
	v_fmac_f32_e32 v201, v154, v204
	v_max_f32_e32 v204, 0, v172
	v_fmac_f32_e32 v201, v155, v208
	v_max_f32_e32 v208, 0, v173
	v_fmac_f32_e32 v201, v156, v204
	v_max_f32_e32 v204, 0, v174
	v_fmac_f32_e32 v201, v157, v208
	v_max_f32_e32 v208, 0, v175
	v_fmac_f32_e32 v201, v158, v204
	v_fmac_f32_e32 v201, v159, v208
	v_cndmask_b32_e32 v201, v61, v201, vcc
	v_ashrrev_i32_e32 v207, 31, v201
	v_or_b32_e32 v207, 0x80000000, v207
	v_xor_b32_e32 v94, v201, v207
	s_cmp_le_u32 s15, 31
	s_cbranch_scc1 .Lidx_search
	s_cmp_le_u32 s15, 32
	s_cbranch_scc1 .Lidx_p32
	global_load_dwordx4 v[18:21], v57, s[20:21]
	global_load_dwordx4 v[22:25], v57, s[20:21] offset:1024
	global_load_dwordx4 v[26:29], v57, s[20:21] offset:2048
	global_load_dwordx4 v[30:33], v57, s[20:21] offset:3072
	s_add_u32 s20, s20, 0x1000
	s_addc_u32 s21, s21, 0
	s_waitcnt vmcnt(8)
	v_mfma_f32_32x32x16_bf16 v[160:175], v[128:131], v[34:37], 0
	v_mfma_f32_32x32x16_bf16 v[160:175], v[132:135], v[38:41], v[160:175]
	v_mfma_f32_32x32x16_bf16 v[160:175], v[136:139], v[42:45], v[160:175]
	v_mfma_f32_32x32x16_bf16 v[160:175], v[140:143], v[46:49], v[160:175]
.Lidx_p32:
	v_cmp_le_i32_e32 vcc, 0x3e0, v59
	v_max_f32_e32 v204, 0, v176
	v_max_f32_e32 v208, 0, v177
	v_fma_f32 v201, v144, v204, 0
	v_max_f32_e32 v204, 0, v178
	v_fmac_f32_e32 v201, v145, v208
	v_max_f32_e32 v208, 0, v179
	v_fmac_f32_e32 v201, v146, v204
	v_max_f32_e32 v204, 0, v180
	v_fmac_f32_e32 v201, v147, v208
	v_max_f32_e32 v208, 0, v181
	v_fmac_f32_e32 v201, v148, v204
	v_max_f32_e32 v204, 0, v182
	v_fmac_f32_e32 v201, v149, v208
	v_max_f32_e32 v208, 0, v183
	v_fmac_f32_e32 v201, v150, v204
	v_max_f32_e32 v204, 0, v184
	v_fmac_f32_e32 v201, v151, v208
	v_max_f32_e32 v208, 0, v185
	v_fmac_f32_e32 v201, v152, v204
	v_max_f32_e32 v204, 0, v186
	v_fmac_f32_e32 v201, v153, v208
	v_max_f32_e32 v208, 0, v187
	v_fmac_f32_e32 v201, v154, v204
	v_max_f32_e32 v204, 0, v188
	v_fmac_f32_e32 v201, v155, v208
	v_max_f32_e32 v208, 0, v189
	v_fmac_f32_e32 v201, v156, v204
	v_max_f32_e32 v204, 0, v190
	v_fmac_f32_e32 v201, v157, v208
	v_max_f32_e32 v208, 0, v191
	v_fmac_f32_e32 v201, v158, v204
	v_fmac_f32_e32 v201, v159, v208
	v_cndmask_b32_e32 v201, v61, v201, vcc
	v_ashrrev_i32_e32 v207, 31, v201
	v_or_b32_e32 v207, 0x80000000, v207
	v_xor_b32_e32 v95, v201, v207
	s_cmp_le_u32 s15, 32
	s_cbranch_scc1 .Lidx_search
	s_cmp_le_u32 s15, 33
	s_cbranch_scc1 .Lidx_p33
	global_load_dwordx4 v[34:37], v57, s[20:21]
	global_load_dwordx4 v[38:41], v57, s[20:21] offset:1024
	global_load_dwordx4 v[42:45], v57, s[20:21] offset:2048
	global_load_dwordx4 v[46:49], v57, s[20:21] offset:3072
	s_add_u32 s20, s20, 0x1000
	s_addc_u32 s21, s21, 0
	s_waitcnt vmcnt(8)
	v_mfma_f32_32x32x16_bf16 v[176:191], v[128:131], v[2:5], 0
	v_mfma_f32_32x32x16_bf16 v[176:191], v[132:135], v[6:9], v[176:191]
	v_mfma_f32_32x32x16_bf16 v[176:191], v[136:139], v[10:13], v[176:191]
	v_mfma_f32_32x32x16_bf16 v[176:191], v[140:143], v[14:17], v[176:191]
.Lidx_p33:
	v_cmp_le_i32_e32 vcc, 0x400, v59
	v_max_f32_e32 v204, 0, v160
	v_max_f32_e32 v208, 0, v161
	v_fma_f32 v201, v144, v204, 0
	v_max_f32_e32 v204, 0, v162
	v_fmac_f32_e32 v201, v145, v208
	v_max_f32_e32 v208, 0, v163
	v_fmac_f32_e32 v201, v146, v204
	v_max_f32_e32 v204, 0, v164
	v_fmac_f32_e32 v201, v147, v208
	v_max_f32_e32 v208, 0, v165
	v_fmac_f32_e32 v201, v148, v204
	v_max_f32_e32 v204, 0, v166
	v_fmac_f32_e32 v201, v149, v208
	v_max_f32_e32 v208, 0, v167
	v_fmac_f32_e32 v201, v150, v204
	v_max_f32_e32 v204, 0, v168
	v_fmac_f32_e32 v201, v151, v208
	v_max_f32_e32 v208, 0, v169
	v_fmac_f32_e32 v201, v152, v204
	v_max_f32_e32 v204, 0, v170
	v_fmac_f32_e32 v201, v153, v208
	v_max_f32_e32 v208, 0, v171
	v_fmac_f32_e32 v201, v154, v204
	v_max_f32_e32 v204, 0, v172
	v_fmac_f32_e32 v201, v155, v208
	v_max_f32_e32 v208, 0, v173
	v_fmac_f32_e32 v201, v156, v204
	v_max_f32_e32 v204, 0, v174
	v_fmac_f32_e32 v201, v157, v208
	v_max_f32_e32 v208, 0, v175
	v_fmac_f32_e32 v201, v158, v204
	v_fmac_f32_e32 v201, v159, v208
	v_cndmask_b32_e32 v201, v61, v201, vcc
	v_ashrrev_i32_e32 v207, 31, v201
	v_or_b32_e32 v207, 0x80000000, v207
	v_xor_b32_e32 v96, v201, v207
	s_cmp_le_u32 s15, 33
	s_cbranch_scc1 .Lidx_search
	s_cmp_le_u32 s15, 34
	s_cbranch_scc1 .Lidx_p34
	global_load_dwordx4 v[2:5], v57, s[20:21]
	global_load_dwordx4 v[6:9], v57, s[20:21] offset:1024
	global_load_dwordx4 v[10:13], v57, s[20:21] offset:2048
	global_load_dwordx4 v[14:17], v57, s[20:21] offset:3072
	s_add_u32 s20, s20, 0x1000
	s_addc_u32 s21, s21, 0
	s_waitcnt vmcnt(8)
	v_mfma_f32_32x32x16_bf16 v[160:175], v[128:131], v[18:21], 0
	v_mfma_f32_32x32x16_bf16 v[160:175], v[132:135], v[22:25], v[160:175]
	v_mfma_f32_32x32x16_bf16 v[160:175], v[136:139], v[26:29], v[160:175]
	v_mfma_f32_32x32x16_bf16 v[160:175], v[140:143], v[30:33], v[160:175]
.Lidx_p34:
	v_cmp_le_i32_e32 vcc, 0x420, v59
	v_max_f32_e32 v204, 0, v176
	v_max_f32_e32 v208, 0, v177
	v_fma_f32 v201, v144, v204, 0
	v_max_f32_e32 v204, 0, v178
	v_fmac_f32_e32 v201, v145, v208
	v_max_f32_e32 v208, 0, v179
	v_fmac_f32_e32 v201, v146, v204
	v_max_f32_e32 v204, 0, v180
	v_fmac_f32_e32 v201, v147, v208
	v_max_f32_e32 v208, 0, v181
	v_fmac_f32_e32 v201, v148, v204
	v_max_f32_e32 v204, 0, v182
	v_fmac_f32_e32 v201, v149, v208
	v_max_f32_e32 v208, 0, v183
	v_fmac_f32_e32 v201, v150, v204
	v_max_f32_e32 v204, 0, v184
	v_fmac_f32_e32 v201, v151, v208
	v_max_f32_e32 v208, 0, v185
	v_fmac_f32_e32 v201, v152, v204
	v_max_f32_e32 v204, 0, v186
	v_fmac_f32_e32 v201, v153, v208
	v_max_f32_e32 v208, 0, v187
	v_fmac_f32_e32 v201, v154, v204
	v_max_f32_e32 v204, 0, v188
	v_fmac_f32_e32 v201, v155, v208
	v_max_f32_e32 v208, 0, v189
	v_fmac_f32_e32 v201, v156, v204
	v_max_f32_e32 v204, 0, v190
	v_fmac_f32_e32 v201, v157, v208
	v_max_f32_e32 v208, 0, v191
	v_fmac_f32_e32 v201, v158, v204
	v_fmac_f32_e32 v201, v159, v208
	v_cndmask_b32_e32 v201, v61, v201, vcc
	v_ashrrev_i32_e32 v207, 31, v201
	v_or_b32_e32 v207, 0x80000000, v207
	v_xor_b32_e32 v97, v201, v207
	s_cmp_le_u32 s15, 34
	s_cbranch_scc1 .Lidx_search
	s_cmp_le_u32 s15, 35
	s_cbranch_scc1 .Lidx_p35
	global_load_dwordx4 v[18:21], v57, s[20:21]
	global_load_dwordx4 v[22:25], v57, s[20:21] offset:1024
	global_load_dwordx4 v[26:29], v57, s[20:21] offset:2048
	global_load_dwordx4 v[30:33], v57, s[20:21] offset:3072
	s_add_u32 s20, s20, 0x1000
	s_addc_u32 s21, s21, 0
	s_waitcnt vmcnt(8)
	v_mfma_f32_32x32x16_bf16 v[176:191], v[128:131], v[34:37], 0
	v_mfma_f32_32x32x16_bf16 v[176:191], v[132:135], v[38:41], v[176:191]
	v_mfma_f32_32x32x16_bf16 v[176:191], v[136:139], v[42:45], v[176:191]
	v_mfma_f32_32x32x16_bf16 v[176:191], v[140:143], v[46:49], v[176:191]
.Lidx_p35:
	v_cmp_le_i32_e32 vcc, 0x440, v59
	v_max_f32_e32 v204, 0, v160
	v_max_f32_e32 v208, 0, v161
	v_fma_f32 v201, v144, v204, 0
	v_max_f32_e32 v204, 0, v162
	v_fmac_f32_e32 v201, v145, v208
	v_max_f32_e32 v208, 0, v163
	v_fmac_f32_e32 v201, v146, v204
	v_max_f32_e32 v204, 0, v164
	v_fmac_f32_e32 v201, v147, v208
	v_max_f32_e32 v208, 0, v165
	v_fmac_f32_e32 v201, v148, v204
	v_max_f32_e32 v204, 0, v166
	v_fmac_f32_e32 v201, v149, v208
	v_max_f32_e32 v208, 0, v167
	v_fmac_f32_e32 v201, v150, v204
	v_max_f32_e32 v204, 0, v168
	v_fmac_f32_e32 v201, v151, v208
	v_max_f32_e32 v208, 0, v169
	v_fmac_f32_e32 v201, v152, v204
	v_max_f32_e32 v204, 0, v170
	v_fmac_f32_e32 v201, v153, v208
	v_max_f32_e32 v208, 0, v171
	v_fmac_f32_e32 v201, v154, v204
	v_max_f32_e32 v204, 0, v172
	v_fmac_f32_e32 v201, v155, v208
	v_max_f32_e32 v208, 0, v173
	v_fmac_f32_e32 v201, v156, v204
	v_max_f32_e32 v204, 0, v174
	v_fmac_f32_e32 v201, v157, v208
	v_max_f32_e32 v208, 0, v175
	v_fmac_f32_e32 v201, v158, v204
	v_fmac_f32_e32 v201, v159, v208
	v_cndmask_b32_e32 v201, v61, v201, vcc
	v_ashrrev_i32_e32 v207, 31, v201
	v_or_b32_e32 v207, 0x80000000, v207
	v_xor_b32_e32 v98, v201, v207
	s_cmp_le_u32 s15, 35
	s_cbranch_scc1 .Lidx_search
	s_cmp_le_u32 s15, 36
	s_cbranch_scc1 .Lidx_p36
	global_load_dwordx4 v[34:37], v57, s[20:21]
	global_load_dwordx4 v[38:41], v57, s[20:21] offset:1024
	global_load_dwordx4 v[42:45], v57, s[20:21] offset:2048
	global_load_dwordx4 v[46:49], v57, s[20:21] offset:3072
	s_add_u32 s20, s20, 0x1000
	s_addc_u32 s21, s21, 0
	s_waitcnt vmcnt(8)
	v_mfma_f32_32x32x16_bf16 v[160:175], v[128:131], v[2:5], 0
	v_mfma_f32_32x32x16_bf16 v[160:175], v[132:135], v[6:9], v[160:175]
	v_mfma_f32_32x32x16_bf16 v[160:175], v[136:139], v[10:13], v[160:175]
	v_mfma_f32_32x32x16_bf16 v[160:175], v[140:143], v[14:17], v[160:175]
.Lidx_p36:
	v_cmp_le_i32_e32 vcc, 0x460, v59
	v_max_f32_e32 v204, 0, v176
	v_max_f32_e32 v208, 0, v177
	v_fma_f32 v201, v144, v204, 0
	v_max_f32_e32 v204, 0, v178
	v_fmac_f32_e32 v201, v145, v208
	v_max_f32_e32 v208, 0, v179
	v_fmac_f32_e32 v201, v146, v204
	v_max_f32_e32 v204, 0, v180
	v_fmac_f32_e32 v201, v147, v208
	v_max_f32_e32 v208, 0, v181
	v_fmac_f32_e32 v201, v148, v204
	v_max_f32_e32 v204, 0, v182
	v_fmac_f32_e32 v201, v149, v208
	v_max_f32_e32 v208, 0, v183
	v_fmac_f32_e32 v201, v150, v204
	v_max_f32_e32 v204, 0, v184
	v_fmac_f32_e32 v201, v151, v208
	v_max_f32_e32 v208, 0, v185
	v_fmac_f32_e32 v201, v152, v204
	v_max_f32_e32 v204, 0, v186
	v_fmac_f32_e32 v201, v153, v208
	v_max_f32_e32 v208, 0, v187
	v_fmac_f32_e32 v201, v154, v204
	v_max_f32_e32 v204, 0, v188
	v_fmac_f32_e32 v201, v155, v208
	v_max_f32_e32 v208, 0, v189
	v_fmac_f32_e32 v201, v156, v204
	v_max_f32_e32 v204, 0, v190
	v_fmac_f32_e32 v201, v157, v208
	v_max_f32_e32 v208, 0, v191
	v_fmac_f32_e32 v201, v158, v204
	v_fmac_f32_e32 v201, v159, v208
	v_cndmask_b32_e32 v201, v61, v201, vcc
	v_ashrrev_i32_e32 v207, 31, v201
	v_or_b32_e32 v207, 0x80000000, v207
	v_xor_b32_e32 v99, v201, v207
	s_cmp_le_u32 s15, 36
	s_cbranch_scc1 .Lidx_search
	s_cmp_le_u32 s15, 37
	s_cbranch_scc1 .Lidx_p37
	global_load_dwordx4 v[2:5], v57, s[20:21]
	global_load_dwordx4 v[6:9], v57, s[20:21] offset:1024
	global_load_dwordx4 v[10:13], v57, s[20:21] offset:2048
	global_load_dwordx4 v[14:17], v57, s[20:21] offset:3072
	s_add_u32 s20, s20, 0x1000
	s_addc_u32 s21, s21, 0
	s_waitcnt vmcnt(8)
	v_mfma_f32_32x32x16_bf16 v[176:191], v[128:131], v[18:21], 0
	v_mfma_f32_32x32x16_bf16 v[176:191], v[132:135], v[22:25], v[176:191]
	v_mfma_f32_32x32x16_bf16 v[176:191], v[136:139], v[26:29], v[176:191]
	v_mfma_f32_32x32x16_bf16 v[176:191], v[140:143], v[30:33], v[176:191]
.Lidx_p37:
	v_cmp_le_i32_e32 vcc, 0x480, v59
	v_max_f32_e32 v204, 0, v160
	v_max_f32_e32 v208, 0, v161
	v_fma_f32 v201, v144, v204, 0
	v_max_f32_e32 v204, 0, v162
	v_fmac_f32_e32 v201, v145, v208
	v_max_f32_e32 v208, 0, v163
	v_fmac_f32_e32 v201, v146, v204
	v_max_f32_e32 v204, 0, v164
	v_fmac_f32_e32 v201, v147, v208
	v_max_f32_e32 v208, 0, v165
	v_fmac_f32_e32 v201, v148, v204
	v_max_f32_e32 v204, 0, v166
	v_fmac_f32_e32 v201, v149, v208
	v_max_f32_e32 v208, 0, v167
	v_fmac_f32_e32 v201, v150, v204
	v_max_f32_e32 v204, 0, v168
	v_fmac_f32_e32 v201, v151, v208
	v_max_f32_e32 v208, 0, v169
	v_fmac_f32_e32 v201, v152, v204
	v_max_f32_e32 v204, 0, v170
	v_fmac_f32_e32 v201, v153, v208
	v_max_f32_e32 v208, 0, v171
	v_fmac_f32_e32 v201, v154, v204
	v_max_f32_e32 v204, 0, v172
	v_fmac_f32_e32 v201, v155, v208
	v_max_f32_e32 v208, 0, v173
	v_fmac_f32_e32 v201, v156, v204
	v_max_f32_e32 v204, 0, v174
	v_fmac_f32_e32 v201, v157, v208
	v_max_f32_e32 v208, 0, v175
	v_fmac_f32_e32 v201, v158, v204
	v_fmac_f32_e32 v201, v159, v208
	v_cndmask_b32_e32 v201, v61, v201, vcc
	v_ashrrev_i32_e32 v207, 31, v201
	v_or_b32_e32 v207, 0x80000000, v207
	v_xor_b32_e32 v100, v201, v207
	s_cmp_le_u32 s15, 37
	s_cbranch_scc1 .Lidx_search
	s_cmp_le_u32 s15, 38
	s_cbranch_scc1 .Lidx_p38
	global_load_dwordx4 v[18:21], v57, s[20:21]
	global_load_dwordx4 v[22:25], v57, s[20:21] offset:1024
	global_load_dwordx4 v[26:29], v57, s[20:21] offset:2048
	global_load_dwordx4 v[30:33], v57, s[20:21] offset:3072
	s_add_u32 s20, s20, 0x1000
	s_addc_u32 s21, s21, 0
	s_waitcnt vmcnt(8)
	v_mfma_f32_32x32x16_bf16 v[160:175], v[128:131], v[34:37], 0
	v_mfma_f32_32x32x16_bf16 v[160:175], v[132:135], v[38:41], v[160:175]
	v_mfma_f32_32x32x16_bf16 v[160:175], v[136:139], v[42:45], v[160:175]
	v_mfma_f32_32x32x16_bf16 v[160:175], v[140:143], v[46:49], v[160:175]
.Lidx_p38:
	v_cmp_le_i32_e32 vcc, 0x4a0, v59
	v_max_f32_e32 v204, 0, v176
	v_max_f32_e32 v208, 0, v177
	v_fma_f32 v201, v144, v204, 0
	v_max_f32_e32 v204, 0, v178
	v_fmac_f32_e32 v201, v145, v208
	v_max_f32_e32 v208, 0, v179
	v_fmac_f32_e32 v201, v146, v204
	v_max_f32_e32 v204, 0, v180
	v_fmac_f32_e32 v201, v147, v208
	v_max_f32_e32 v208, 0, v181
	v_fmac_f32_e32 v201, v148, v204
	v_max_f32_e32 v204, 0, v182
	v_fmac_f32_e32 v201, v149, v208
	v_max_f32_e32 v208, 0, v183
	v_fmac_f32_e32 v201, v150, v204
	v_max_f32_e32 v204, 0, v184
	v_fmac_f32_e32 v201, v151, v208
	v_max_f32_e32 v208, 0, v185
	v_fmac_f32_e32 v201, v152, v204
	v_max_f32_e32 v204, 0, v186
	v_fmac_f32_e32 v201, v153, v208
	v_max_f32_e32 v208, 0, v187
	v_fmac_f32_e32 v201, v154, v204
	v_max_f32_e32 v204, 0, v188
	v_fmac_f32_e32 v201, v155, v208
	v_max_f32_e32 v208, 0, v189
	v_fmac_f32_e32 v201, v156, v204
	v_max_f32_e32 v204, 0, v190
	v_fmac_f32_e32 v201, v157, v208
	v_max_f32_e32 v208, 0, v191
	v_fmac_f32_e32 v201, v158, v204
	v_fmac_f32_e32 v201, v159, v208
	v_cndmask_b32_e32 v201, v61, v201, vcc
	v_ashrrev_i32_e32 v207, 31, v201
	v_or_b32_e32 v207, 0x80000000, v207
	v_xor_b32_e32 v101, v201, v207
	s_cmp_le_u32 s15, 38
	s_cbranch_scc1 .Lidx_search
	s_cmp_le_u32 s15, 39
	s_cbranch_scc1 .Lidx_p39
	global_load_dwordx4 v[34:37], v57, s[20:21]
	global_load_dwordx4 v[38:41], v57, s[20:21] offset:1024
	global_load_dwordx4 v[42:45], v57, s[20:21] offset:2048
	global_load_dwordx4 v[46:49], v57, s[20:21] offset:3072
	s_add_u32 s20, s20, 0x1000
	s_addc_u32 s21, s21, 0
	s_waitcnt vmcnt(8)
	v_mfma_f32_32x32x16_bf16 v[176:191], v[128:131], v[2:5], 0
	v_mfma_f32_32x32x16_bf16 v[176:191], v[132:135], v[6:9], v[176:191]
	v_mfma_f32_32x32x16_bf16 v[176:191], v[136:139], v[10:13], v[176:191]
	v_mfma_f32_32x32x16_bf16 v[176:191], v[140:143], v[14:17], v[176:191]
.Lidx_p39:
	v_cmp_le_i32_e32 vcc, 0x4c0, v59
	v_max_f32_e32 v204, 0, v160
	v_max_f32_e32 v208, 0, v161
	v_fma_f32 v201, v144, v204, 0
	v_max_f32_e32 v204, 0, v162
	v_fmac_f32_e32 v201, v145, v208
	v_max_f32_e32 v208, 0, v163
	v_fmac_f32_e32 v201, v146, v204
	v_max_f32_e32 v204, 0, v164
	v_fmac_f32_e32 v201, v147, v208
	v_max_f32_e32 v208, 0, v165
	v_fmac_f32_e32 v201, v148, v204
	v_max_f32_e32 v204, 0, v166
	v_fmac_f32_e32 v201, v149, v208
	v_max_f32_e32 v208, 0, v167
	v_fmac_f32_e32 v201, v150, v204
	v_max_f32_e32 v204, 0, v168
	v_fmac_f32_e32 v201, v151, v208
	v_max_f32_e32 v208, 0, v169
	v_fmac_f32_e32 v201, v152, v204
	v_max_f32_e32 v204, 0, v170
	v_fmac_f32_e32 v201, v153, v208
	v_max_f32_e32 v208, 0, v171
	v_fmac_f32_e32 v201, v154, v204
	v_max_f32_e32 v204, 0, v172
	v_fmac_f32_e32 v201, v155, v208
	v_max_f32_e32 v208, 0, v173
	v_fmac_f32_e32 v201, v156, v204
	v_max_f32_e32 v204, 0, v174
	v_fmac_f32_e32 v201, v157, v208
	v_max_f32_e32 v208, 0, v175
	v_fmac_f32_e32 v201, v158, v204
	v_fmac_f32_e32 v201, v159, v208
	v_cndmask_b32_e32 v201, v61, v201, vcc
	v_ashrrev_i32_e32 v207, 31, v201
	v_or_b32_e32 v207, 0x80000000, v207
	v_xor_b32_e32 v102, v201, v207
	s_cmp_le_u32 s15, 39
	s_cbranch_scc1 .Lidx_search
	s_cmp_le_u32 s15, 40
	s_cbranch_scc1 .Lidx_p40
	global_load_dwordx4 v[2:5], v57, s[20:21]
	global_load_dwordx4 v[6:9], v57, s[20:21] offset:1024
	global_load_dwordx4 v[10:13], v57, s[20:21] offset:2048
	global_load_dwordx4 v[14:17], v57, s[20:21] offset:3072
	s_add_u32 s20, s20, 0x1000
	s_addc_u32 s21, s21, 0
	s_waitcnt vmcnt(8)
	v_mfma_f32_32x32x16_bf16 v[160:175], v[128:131], v[18:21], 0
	v_mfma_f32_32x32x16_bf16 v[160:175], v[132:135], v[22:25], v[160:175]
	v_mfma_f32_32x32x16_bf16 v[160:175], v[136:139], v[26:29], v[160:175]
	v_mfma_f32_32x32x16_bf16 v[160:175], v[140:143], v[30:33], v[160:175]
.Lidx_p40:
	v_cmp_le_i32_e32 vcc, 0x4e0, v59
	v_max_f32_e32 v204, 0, v176
	v_max_f32_e32 v208, 0, v177
	v_fma_f32 v201, v144, v204, 0
	v_max_f32_e32 v204, 0, v178
	v_fmac_f32_e32 v201, v145, v208
	v_max_f32_e32 v208, 0, v179
	v_fmac_f32_e32 v201, v146, v204
	v_max_f32_e32 v204, 0, v180
	v_fmac_f32_e32 v201, v147, v208
	v_max_f32_e32 v208, 0, v181
	v_fmac_f32_e32 v201, v148, v204
	v_max_f32_e32 v204, 0, v182
	v_fmac_f32_e32 v201, v149, v208
	v_max_f32_e32 v208, 0, v183
	v_fmac_f32_e32 v201, v150, v204
	v_max_f32_e32 v204, 0, v184
	v_fmac_f32_e32 v201, v151, v208
	v_max_f32_e32 v208, 0, v185
	v_fmac_f32_e32 v201, v152, v204
	v_max_f32_e32 v204, 0, v186
	v_fmac_f32_e32 v201, v153, v208
	v_max_f32_e32 v208, 0, v187
	v_fmac_f32_e32 v201, v154, v204
	v_max_f32_e32 v204, 0, v188
	v_fmac_f32_e32 v201, v155, v208
	v_max_f32_e32 v208, 0, v189
	v_fmac_f32_e32 v201, v156, v204
	v_max_f32_e32 v204, 0, v190
	v_fmac_f32_e32 v201, v157, v208
	v_max_f32_e32 v208, 0, v191
	v_fmac_f32_e32 v201, v158, v204
	v_fmac_f32_e32 v201, v159, v208
	v_cndmask_b32_e32 v201, v61, v201, vcc
	v_ashrrev_i32_e32 v207, 31, v201
	v_or_b32_e32 v207, 0x80000000, v207
	v_xor_b32_e32 v103, v201, v207
	s_cmp_le_u32 s15, 40
	s_cbranch_scc1 .Lidx_search
	s_cmp_le_u32 s15, 41
	s_cbranch_scc1 .Lidx_p41
	global_load_dwordx4 v[18:21], v57, s[20:21]
	global_load_dwordx4 v[22:25], v57, s[20:21] offset:1024
	global_load_dwordx4 v[26:29], v57, s[20:21] offset:2048
	global_load_dwordx4 v[30:33], v57, s[20:21] offset:3072
	s_add_u32 s20, s20, 0x1000
	s_addc_u32 s21, s21, 0
	s_waitcnt vmcnt(8)
	v_mfma_f32_32x32x16_bf16 v[176:191], v[128:131], v[34:37], 0
	v_mfma_f32_32x32x16_bf16 v[176:191], v[132:135], v[38:41], v[176:191]
	v_mfma_f32_32x32x16_bf16 v[176:191], v[136:139], v[42:45], v[176:191]
	v_mfma_f32_32x32x16_bf16 v[176:191], v[140:143], v[46:49], v[176:191]
.Lidx_p41:
	v_cmp_le_i32_e32 vcc, 0x500, v59
	v_max_f32_e32 v204, 0, v160
	v_max_f32_e32 v208, 0, v161
	v_fma_f32 v201, v144, v204, 0
	v_max_f32_e32 v204, 0, v162
	v_fmac_f32_e32 v201, v145, v208
	v_max_f32_e32 v208, 0, v163
	v_fmac_f32_e32 v201, v146, v204
	v_max_f32_e32 v204, 0, v164
	v_fmac_f32_e32 v201, v147, v208
	v_max_f32_e32 v208, 0, v165
	v_fmac_f32_e32 v201, v148, v204
	v_max_f32_e32 v204, 0, v166
	v_fmac_f32_e32 v201, v149, v208
	v_max_f32_e32 v208, 0, v167
	v_fmac_f32_e32 v201, v150, v204
	v_max_f32_e32 v204, 0, v168
	v_fmac_f32_e32 v201, v151, v208
	v_max_f32_e32 v208, 0, v169
	v_fmac_f32_e32 v201, v152, v204
	v_max_f32_e32 v204, 0, v170
	v_fmac_f32_e32 v201, v153, v208
	v_max_f32_e32 v208, 0, v171
	v_fmac_f32_e32 v201, v154, v204
	v_max_f32_e32 v204, 0, v172
	v_fmac_f32_e32 v201, v155, v208
	v_max_f32_e32 v208, 0, v173
	v_fmac_f32_e32 v201, v156, v204
	v_max_f32_e32 v204, 0, v174
	v_fmac_f32_e32 v201, v157, v208
	v_max_f32_e32 v208, 0, v175
	v_fmac_f32_e32 v201, v158, v204
	v_fmac_f32_e32 v201, v159, v208
	v_cndmask_b32_e32 v201, v61, v201, vcc
	v_ashrrev_i32_e32 v207, 31, v201
	v_or_b32_e32 v207, 0x80000000, v207
	v_xor_b32_e32 v104, v201, v207
	s_cmp_le_u32 s15, 41
	s_cbranch_scc1 .Lidx_search
	s_cmp_le_u32 s15, 42
	s_cbranch_scc1 .Lidx_p42
	global_load_dwordx4 v[34:37], v57, s[20:21]
	global_load_dwordx4 v[38:41], v57, s[20:21] offset:1024
	global_load_dwordx4 v[42:45], v57, s[20:21] offset:2048
	global_load_dwordx4 v[46:49], v57, s[20:21] offset:3072
	s_add_u32 s20, s20, 0x1000
	s_addc_u32 s21, s21, 0
	s_waitcnt vmcnt(8)
	v_mfma_f32_32x32x16_bf16 v[160:175], v[128:131], v[2:5], 0
	v_mfma_f32_32x32x16_bf16 v[160:175], v[132:135], v[6:9], v[160:175]
	v_mfma_f32_32x32x16_bf16 v[160:175], v[136:139], v[10:13], v[160:175]
	v_mfma_f32_32x32x16_bf16 v[160:175], v[140:143], v[14:17], v[160:175]
.Lidx_p42:
	v_cmp_le_i32_e32 vcc, 0x520, v59
	v_max_f32_e32 v204, 0, v176
	v_max_f32_e32 v208, 0, v177
	v_fma_f32 v201, v144, v204, 0
	v_max_f32_e32 v204, 0, v178
	v_fmac_f32_e32 v201, v145, v208
	v_max_f32_e32 v208, 0, v179
	v_fmac_f32_e32 v201, v146, v204
	v_max_f32_e32 v204, 0, v180
	v_fmac_f32_e32 v201, v147, v208
	v_max_f32_e32 v208, 0, v181
	v_fmac_f32_e32 v201, v148, v204
	v_max_f32_e32 v204, 0, v182
	v_fmac_f32_e32 v201, v149, v208
	v_max_f32_e32 v208, 0, v183
	v_fmac_f32_e32 v201, v150, v204
	v_max_f32_e32 v204, 0, v184
	v_fmac_f32_e32 v201, v151, v208
	v_max_f32_e32 v208, 0, v185
	v_fmac_f32_e32 v201, v152, v204
	v_max_f32_e32 v204, 0, v186
	v_fmac_f32_e32 v201, v153, v208
	v_max_f32_e32 v208, 0, v187
	v_fmac_f32_e32 v201, v154, v204
	v_max_f32_e32 v204, 0, v188
	v_fmac_f32_e32 v201, v155, v208
	v_max_f32_e32 v208, 0, v189
	v_fmac_f32_e32 v201, v156, v204
	v_max_f32_e32 v204, 0, v190
	v_fmac_f32_e32 v201, v157, v208
	v_max_f32_e32 v208, 0, v191
	v_fmac_f32_e32 v201, v158, v204
	v_fmac_f32_e32 v201, v159, v208
	v_cndmask_b32_e32 v201, v61, v201, vcc
	v_ashrrev_i32_e32 v207, 31, v201
	v_or_b32_e32 v207, 0x80000000, v207
	v_xor_b32_e32 v105, v201, v207
	s_cmp_le_u32 s15, 42
	s_cbranch_scc1 .Lidx_search
	s_cmp_le_u32 s15, 43
	s_cbranch_scc1 .Lidx_p43
	global_load_dwordx4 v[2:5], v57, s[20:21]
	global_load_dwordx4 v[6:9], v57, s[20:21] offset:1024
	global_load_dwordx4 v[10:13], v57, s[20:21] offset:2048
	global_load_dwordx4 v[14:17], v57, s[20:21] offset:3072
	s_add_u32 s20, s20, 0x1000
	s_addc_u32 s21, s21, 0
	s_waitcnt vmcnt(8)
	v_mfma_f32_32x32x16_bf16 v[176:191], v[128:131], v[18:21], 0
	v_mfma_f32_32x32x16_bf16 v[176:191], v[132:135], v[22:25], v[176:191]
	v_mfma_f32_32x32x16_bf16 v[176:191], v[136:139], v[26:29], v[176:191]
	v_mfma_f32_32x32x16_bf16 v[176:191], v[140:143], v[30:33], v[176:191]
.Lidx_p43:
	v_cmp_le_i32_e32 vcc, 0x540, v59
	v_max_f32_e32 v204, 0, v160
	v_max_f32_e32 v208, 0, v161
	v_fma_f32 v201, v144, v204, 0
	v_max_f32_e32 v204, 0, v162
	v_fmac_f32_e32 v201, v145, v208
	v_max_f32_e32 v208, 0, v163
	v_fmac_f32_e32 v201, v146, v204
	v_max_f32_e32 v204, 0, v164
	v_fmac_f32_e32 v201, v147, v208
	v_max_f32_e32 v208, 0, v165
	v_fmac_f32_e32 v201, v148, v204
	v_max_f32_e32 v204, 0, v166
	v_fmac_f32_e32 v201, v149, v208
	v_max_f32_e32 v208, 0, v167
	v_fmac_f32_e32 v201, v150, v204
	v_max_f32_e32 v204, 0, v168
	v_fmac_f32_e32 v201, v151, v208
	v_max_f32_e32 v208, 0, v169
	v_fmac_f32_e32 v201, v152, v204
	v_max_f32_e32 v204, 0, v170
	v_fmac_f32_e32 v201, v153, v208
	v_max_f32_e32 v208, 0, v171
	v_fmac_f32_e32 v201, v154, v204
	v_max_f32_e32 v204, 0, v172
	v_fmac_f32_e32 v201, v155, v208
	v_max_f32_e32 v208, 0, v173
	v_fmac_f32_e32 v201, v156, v204
	v_max_f32_e32 v204, 0, v174
	v_fmac_f32_e32 v201, v157, v208
	v_max_f32_e32 v208, 0, v175
	v_fmac_f32_e32 v201, v158, v204
	v_fmac_f32_e32 v201, v159, v208
	v_cndmask_b32_e32 v201, v61, v201, vcc
	v_ashrrev_i32_e32 v207, 31, v201
	v_or_b32_e32 v207, 0x80000000, v207
	v_xor_b32_e32 v106, v201, v207
	s_cmp_le_u32 s15, 43
	s_cbranch_scc1 .Lidx_search
	s_cmp_le_u32 s15, 44
	s_cbranch_scc1 .Lidx_p44
	global_load_dwordx4 v[18:21], v57, s[20:21]
	global_load_dwordx4 v[22:25], v57, s[20:21] offset:1024
	global_load_dwordx4 v[26:29], v57, s[20:21] offset:2048
	global_load_dwordx4 v[30:33], v57, s[20:21] offset:3072
	s_add_u32 s20, s20, 0x1000
	s_addc_u32 s21, s21, 0
	s_waitcnt vmcnt(8)
	v_mfma_f32_32x32x16_bf16 v[160:175], v[128:131], v[34:37], 0
	v_mfma_f32_32x32x16_bf16 v[160:175], v[132:135], v[38:41], v[160:175]
	v_mfma_f32_32x32x16_bf16 v[160:175], v[136:139], v[42:45], v[160:175]
	v_mfma_f32_32x32x16_bf16 v[160:175], v[140:143], v[46:49], v[160:175]
.Lidx_p44:
	v_cmp_le_i32_e32 vcc, 0x560, v59
	v_max_f32_e32 v204, 0, v176
	v_max_f32_e32 v208, 0, v177
	v_fma_f32 v201, v144, v204, 0
	v_max_f32_e32 v204, 0, v178
	v_fmac_f32_e32 v201, v145, v208
	v_max_f32_e32 v208, 0, v179
	v_fmac_f32_e32 v201, v146, v204
	v_max_f32_e32 v204, 0, v180
	v_fmac_f32_e32 v201, v147, v208
	v_max_f32_e32 v208, 0, v181
	v_fmac_f32_e32 v201, v148, v204
	v_max_f32_e32 v204, 0, v182
	v_fmac_f32_e32 v201, v149, v208
	v_max_f32_e32 v208, 0, v183
	v_fmac_f32_e32 v201, v150, v204
	v_max_f32_e32 v204, 0, v184
	v_fmac_f32_e32 v201, v151, v208
	v_max_f32_e32 v208, 0, v185
	v_fmac_f32_e32 v201, v152, v204
	v_max_f32_e32 v204, 0, v186
	v_fmac_f32_e32 v201, v153, v208
	v_max_f32_e32 v208, 0, v187
	v_fmac_f32_e32 v201, v154, v204
	v_max_f32_e32 v204, 0, v188
	v_fmac_f32_e32 v201, v155, v208
	v_max_f32_e32 v208, 0, v189
	v_fmac_f32_e32 v201, v156, v204
	v_max_f32_e32 v204, 0, v190
	v_fmac_f32_e32 v201, v157, v208
	v_max_f32_e32 v208, 0, v191
	v_fmac_f32_e32 v201, v158, v204
	v_fmac_f32_e32 v201, v159, v208
	v_cndmask_b32_e32 v201, v61, v201, vcc
	v_ashrrev_i32_e32 v207, 31, v201
	v_or_b32_e32 v207, 0x80000000, v207
	v_xor_b32_e32 v107, v201, v207
	s_cmp_le_u32 s15, 44
	s_cbranch_scc1 .Lidx_search
	s_cmp_le_u32 s15, 45
	s_cbranch_scc1 .Lidx_p45
	global_load_dwordx4 v[34:37], v57, s[20:21]
	global_load_dwordx4 v[38:41], v57, s[20:21] offset:1024
	global_load_dwordx4 v[42:45], v57, s[20:21] offset:2048
	global_load_dwordx4 v[46:49], v57, s[20:21] offset:3072
	s_add_u32 s20, s20, 0x1000
	s_addc_u32 s21, s21, 0
	s_waitcnt vmcnt(8)
	v_mfma_f32_32x32x16_bf16 v[176:191], v[128:131], v[2:5], 0
	v_mfma_f32_32x32x16_bf16 v[176:191], v[132:135], v[6:9], v[176:191]
	v_mfma_f32_32x32x16_bf16 v[176:191], v[136:139], v[10:13], v[176:191]
	v_mfma_f32_32x32x16_bf16 v[176:191], v[140:143], v[14:17], v[176:191]
.Lidx_p45:
	v_cmp_le_i32_e32 vcc, 0x580, v59
	v_max_f32_e32 v204, 0, v160
	v_max_f32_e32 v208, 0, v161
	v_fma_f32 v201, v144, v204, 0
	v_max_f32_e32 v204, 0, v162
	v_fmac_f32_e32 v201, v145, v208
	v_max_f32_e32 v208, 0, v163
	v_fmac_f32_e32 v201, v146, v204
	v_max_f32_e32 v204, 0, v164
	v_fmac_f32_e32 v201, v147, v208
	v_max_f32_e32 v208, 0, v165
	v_fmac_f32_e32 v201, v148, v204
	v_max_f32_e32 v204, 0, v166
	v_fmac_f32_e32 v201, v149, v208
	v_max_f32_e32 v208, 0, v167
	v_fmac_f32_e32 v201, v150, v204
	v_max_f32_e32 v204, 0, v168
	v_fmac_f32_e32 v201, v151, v208
	v_max_f32_e32 v208, 0, v169
	v_fmac_f32_e32 v201, v152, v204
	v_max_f32_e32 v204, 0, v170
	v_fmac_f32_e32 v201, v153, v208
	v_max_f32_e32 v208, 0, v171
	v_fmac_f32_e32 v201, v154, v204
	v_max_f32_e32 v204, 0, v172
	v_fmac_f32_e32 v201, v155, v208
	v_max_f32_e32 v208, 0, v173
	v_fmac_f32_e32 v201, v156, v204
	v_max_f32_e32 v204, 0, v174
	v_fmac_f32_e32 v201, v157, v208
	v_max_f32_e32 v208, 0, v175
	v_fmac_f32_e32 v201, v158, v204
	v_fmac_f32_e32 v201, v159, v208
	v_cndmask_b32_e32 v201, v61, v201, vcc
	v_ashrrev_i32_e32 v207, 31, v201
	v_or_b32_e32 v207, 0x80000000, v207
	v_xor_b32_e32 v108, v201, v207
	s_cmp_le_u32 s15, 45
	s_cbranch_scc1 .Lidx_search
	s_cmp_le_u32 s15, 46
	s_cbranch_scc1 .Lidx_p46
	global_load_dwordx4 v[2:5], v57, s[20:21]
	global_load_dwordx4 v[6:9], v57, s[20:21] offset:1024
	global_load_dwordx4 v[10:13], v57, s[20:21] offset:2048
	global_load_dwordx4 v[14:17], v57, s[20:21] offset:3072
	s_add_u32 s20, s20, 0x1000
	s_addc_u32 s21, s21, 0
	s_waitcnt vmcnt(8)
	v_mfma_f32_32x32x16_bf16 v[160:175], v[128:131], v[18:21], 0
	v_mfma_f32_32x32x16_bf16 v[160:175], v[132:135], v[22:25], v[160:175]
	v_mfma_f32_32x32x16_bf16 v[160:175], v[136:139], v[26:29], v[160:175]
	v_mfma_f32_32x32x16_bf16 v[160:175], v[140:143], v[30:33], v[160:175]
.Lidx_p46:
	v_cmp_le_i32_e32 vcc, 0x5a0, v59
	v_max_f32_e32 v204, 0, v176
	v_max_f32_e32 v208, 0, v177
	v_fma_f32 v201, v144, v204, 0
	v_max_f32_e32 v204, 0, v178
	v_fmac_f32_e32 v201, v145, v208
	v_max_f32_e32 v208, 0, v179
	v_fmac_f32_e32 v201, v146, v204
	v_max_f32_e32 v204, 0, v180
	v_fmac_f32_e32 v201, v147, v208
	v_max_f32_e32 v208, 0, v181
	v_fmac_f32_e32 v201, v148, v204
	v_max_f32_e32 v204, 0, v182
	v_fmac_f32_e32 v201, v149, v208
	v_max_f32_e32 v208, 0, v183
	v_fmac_f32_e32 v201, v150, v204
	v_max_f32_e32 v204, 0, v184
	v_fmac_f32_e32 v201, v151, v208
	v_max_f32_e32 v208, 0, v185
	v_fmac_f32_e32 v201, v152, v204
	v_max_f32_e32 v204, 0, v186
	v_fmac_f32_e32 v201, v153, v208
	v_max_f32_e32 v208, 0, v187
	v_fmac_f32_e32 v201, v154, v204
	v_max_f32_e32 v204, 0, v188
	v_fmac_f32_e32 v201, v155, v208
	v_max_f32_e32 v208, 0, v189
	v_fmac_f32_e32 v201, v156, v204
	v_max_f32_e32 v204, 0, v190
	v_fmac_f32_e32 v201, v157, v208
	v_max_f32_e32 v208, 0, v191
	v_fmac_f32_e32 v201, v158, v204
	v_fmac_f32_e32 v201, v159, v208
	v_cndmask_b32_e32 v201, v61, v201, vcc
	v_ashrrev_i32_e32 v207, 31, v201
	v_or_b32_e32 v207, 0x80000000, v207
	v_xor_b32_e32 v109, v201, v207
	s_cmp_le_u32 s15, 46
	s_cbranch_scc1 .Lidx_search
	s_cmp_le_u32 s15, 47
	s_cbranch_scc1 .Lidx_p47
	global_load_dwordx4 v[18:21], v57, s[20:21]
	global_load_dwordx4 v[22:25], v57, s[20:21] offset:1024
	global_load_dwordx4 v[26:29], v57, s[20:21] offset:2048
	global_load_dwordx4 v[30:33], v57, s[20:21] offset:3072
	s_add_u32 s20, s20, 0x1000
	s_addc_u32 s21, s21, 0
	s_waitcnt vmcnt(8)
	v_mfma_f32_32x32x16_bf16 v[176:191], v[128:131], v[34:37], 0
	v_mfma_f32_32x32x16_bf16 v[176:191], v[132:135], v[38:41], v[176:191]
	v_mfma_f32_32x32x16_bf16 v[176:191], v[136:139], v[42:45], v[176:191]
	v_mfma_f32_32x32x16_bf16 v[176:191], v[140:143], v[46:49], v[176:191]
.Lidx_p47:
	v_cmp_le_i32_e32 vcc, 0x5c0, v59
	v_max_f32_e32 v204, 0, v160
	v_max_f32_e32 v208, 0, v161
	v_fma_f32 v201, v144, v204, 0
	v_max_f32_e32 v204, 0, v162
	v_fmac_f32_e32 v201, v145, v208
	v_max_f32_e32 v208, 0, v163
	v_fmac_f32_e32 v201, v146, v204
	v_max_f32_e32 v204, 0, v164
	v_fmac_f32_e32 v201, v147, v208
	v_max_f32_e32 v208, 0, v165
	v_fmac_f32_e32 v201, v148, v204
	v_max_f32_e32 v204, 0, v166
	v_fmac_f32_e32 v201, v149, v208
	v_max_f32_e32 v208, 0, v167
	v_fmac_f32_e32 v201, v150, v204
	v_max_f32_e32 v204, 0, v168
	v_fmac_f32_e32 v201, v151, v208
	v_max_f32_e32 v208, 0, v169
	v_fmac_f32_e32 v201, v152, v204
	v_max_f32_e32 v204, 0, v170
	v_fmac_f32_e32 v201, v153, v208
	v_max_f32_e32 v208, 0, v171
	v_fmac_f32_e32 v201, v154, v204
	v_max_f32_e32 v204, 0, v172
	v_fmac_f32_e32 v201, v155, v208
	v_max_f32_e32 v208, 0, v173
	v_fmac_f32_e32 v201, v156, v204
	v_max_f32_e32 v204, 0, v174
	v_fmac_f32_e32 v201, v157, v208
	v_max_f32_e32 v208, 0, v175
	v_fmac_f32_e32 v201, v158, v204
	v_fmac_f32_e32 v201, v159, v208
	v_cndmask_b32_e32 v201, v61, v201, vcc
	v_ashrrev_i32_e32 v207, 31, v201
	v_or_b32_e32 v207, 0x80000000, v207
	v_xor_b32_e32 v110, v201, v207
	s_cmp_le_u32 s15, 47
	s_cbranch_scc1 .Lidx_search
	s_cmp_le_u32 s15, 48
	s_cbranch_scc1 .Lidx_p48
	global_load_dwordx4 v[34:37], v57, s[20:21]
	global_load_dwordx4 v[38:41], v57, s[20:21] offset:1024
	global_load_dwordx4 v[42:45], v57, s[20:21] offset:2048
	global_load_dwordx4 v[46:49], v57, s[20:21] offset:3072
	s_add_u32 s20, s20, 0x1000
	s_addc_u32 s21, s21, 0
	s_waitcnt vmcnt(8)
	v_mfma_f32_32x32x16_bf16 v[160:175], v[128:131], v[2:5], 0
	v_mfma_f32_32x32x16_bf16 v[160:175], v[132:135], v[6:9], v[160:175]
	v_mfma_f32_32x32x16_bf16 v[160:175], v[136:139], v[10:13], v[160:175]
	v_mfma_f32_32x32x16_bf16 v[160:175], v[140:143], v[14:17], v[160:175]
.Lidx_p48:
	v_cmp_le_i32_e32 vcc, 0x5e0, v59
	v_max_f32_e32 v204, 0, v176
	v_max_f32_e32 v208, 0, v177
	v_fma_f32 v201, v144, v204, 0
	v_max_f32_e32 v204, 0, v178
	v_fmac_f32_e32 v201, v145, v208
	v_max_f32_e32 v208, 0, v179
	v_fmac_f32_e32 v201, v146, v204
	v_max_f32_e32 v204, 0, v180
	v_fmac_f32_e32 v201, v147, v208
	v_max_f32_e32 v208, 0, v181
	v_fmac_f32_e32 v201, v148, v204
	v_max_f32_e32 v204, 0, v182
	v_fmac_f32_e32 v201, v149, v208
	v_max_f32_e32 v208, 0, v183
	v_fmac_f32_e32 v201, v150, v204
	v_max_f32_e32 v204, 0, v184
	v_fmac_f32_e32 v201, v151, v208
	v_max_f32_e32 v208, 0, v185
	v_fmac_f32_e32 v201, v152, v204
	v_max_f32_e32 v204, 0, v186
	v_fmac_f32_e32 v201, v153, v208
	v_max_f32_e32 v208, 0, v187
	v_fmac_f32_e32 v201, v154, v204
	v_max_f32_e32 v204, 0, v188
	v_fmac_f32_e32 v201, v155, v208
	v_max_f32_e32 v208, 0, v189
	v_fmac_f32_e32 v201, v156, v204
	v_max_f32_e32 v204, 0, v190
	v_fmac_f32_e32 v201, v157, v208
	v_max_f32_e32 v208, 0, v191
	v_fmac_f32_e32 v201, v158, v204
	v_fmac_f32_e32 v201, v159, v208
	v_cndmask_b32_e32 v201, v61, v201, vcc
	v_ashrrev_i32_e32 v207, 31, v201
	v_or_b32_e32 v207, 0x80000000, v207
	v_xor_b32_e32 v111, v201, v207
	s_cmp_le_u32 s15, 48
	s_cbranch_scc1 .Lidx_search
	s_cmp_le_u32 s15, 49
	s_cbranch_scc1 .Lidx_p49
	global_load_dwordx4 v[2:5], v57, s[20:21]
	global_load_dwordx4 v[6:9], v57, s[20:21] offset:1024
	global_load_dwordx4 v[10:13], v57, s[20:21] offset:2048
	global_load_dwordx4 v[14:17], v57, s[20:21] offset:3072
	s_add_u32 s20, s20, 0x1000
	s_addc_u32 s21, s21, 0
	s_waitcnt vmcnt(8)
	v_mfma_f32_32x32x16_bf16 v[176:191], v[128:131], v[18:21], 0
	v_mfma_f32_32x32x16_bf16 v[176:191], v[132:135], v[22:25], v[176:191]
	v_mfma_f32_32x32x16_bf16 v[176:191], v[136:139], v[26:29], v[176:191]
	v_mfma_f32_32x32x16_bf16 v[176:191], v[140:143], v[30:33], v[176:191]
.Lidx_p49:
	v_cmp_le_i32_e32 vcc, 0x600, v59
	v_max_f32_e32 v204, 0, v160
	v_max_f32_e32 v208, 0, v161
	v_fma_f32 v201, v144, v204, 0
	v_max_f32_e32 v204, 0, v162
	v_fmac_f32_e32 v201, v145, v208
	v_max_f32_e32 v208, 0, v163
	v_fmac_f32_e32 v201, v146, v204
	v_max_f32_e32 v204, 0, v164
	v_fmac_f32_e32 v201, v147, v208
	v_max_f32_e32 v208, 0, v165
	v_fmac_f32_e32 v201, v148, v204
	v_max_f32_e32 v204, 0, v166
	v_fmac_f32_e32 v201, v149, v208
	v_max_f32_e32 v208, 0, v167
	v_fmac_f32_e32 v201, v150, v204
	v_max_f32_e32 v204, 0, v168
	v_fmac_f32_e32 v201, v151, v208
	v_max_f32_e32 v208, 0, v169
	v_fmac_f32_e32 v201, v152, v204
	v_max_f32_e32 v204, 0, v170
	v_fmac_f32_e32 v201, v153, v208
	v_max_f32_e32 v208, 0, v171
	v_fmac_f32_e32 v201, v154, v204
	v_max_f32_e32 v204, 0, v172
	v_fmac_f32_e32 v201, v155, v208
	v_max_f32_e32 v208, 0, v173
	v_fmac_f32_e32 v201, v156, v204
	v_max_f32_e32 v204, 0, v174
	v_fmac_f32_e32 v201, v157, v208
	v_max_f32_e32 v208, 0, v175
	v_fmac_f32_e32 v201, v158, v204
	v_fmac_f32_e32 v201, v159, v208
	v_cndmask_b32_e32 v201, v61, v201, vcc
	v_ashrrev_i32_e32 v207, 31, v201
	v_or_b32_e32 v207, 0x80000000, v207
	v_xor_b32_e32 v112, v201, v207
	s_cmp_le_u32 s15, 49
	s_cbranch_scc1 .Lidx_search
	s_cmp_le_u32 s15, 50
	s_cbranch_scc1 .Lidx_p50
	global_load_dwordx4 v[18:21], v57, s[20:21]
	global_load_dwordx4 v[22:25], v57, s[20:21] offset:1024
	global_load_dwordx4 v[26:29], v57, s[20:21] offset:2048
	global_load_dwordx4 v[30:33], v57, s[20:21] offset:3072
	s_add_u32 s20, s20, 0x1000
	s_addc_u32 s21, s21, 0
	s_waitcnt vmcnt(8)
	v_mfma_f32_32x32x16_bf16 v[160:175], v[128:131], v[34:37], 0
	v_mfma_f32_32x32x16_bf16 v[160:175], v[132:135], v[38:41], v[160:175]
	v_mfma_f32_32x32x16_bf16 v[160:175], v[136:139], v[42:45], v[160:175]
	v_mfma_f32_32x32x16_bf16 v[160:175], v[140:143], v[46:49], v[160:175]
.Lidx_p50:
	v_cmp_le_i32_e32 vcc, 0x620, v59
	v_max_f32_e32 v204, 0, v176
	v_max_f32_e32 v208, 0, v177
	v_fma_f32 v201, v144, v204, 0
	v_max_f32_e32 v204, 0, v178
	v_fmac_f32_e32 v201, v145, v208
	v_max_f32_e32 v208, 0, v179
	v_fmac_f32_e32 v201, v146, v204
	v_max_f32_e32 v204, 0, v180
	v_fmac_f32_e32 v201, v147, v208
	v_max_f32_e32 v208, 0, v181
	v_fmac_f32_e32 v201, v148, v204
	v_max_f32_e32 v204, 0, v182
	v_fmac_f32_e32 v201, v149, v208
	v_max_f32_e32 v208, 0, v183
	v_fmac_f32_e32 v201, v150, v204
	v_max_f32_e32 v204, 0, v184
	v_fmac_f32_e32 v201, v151, v208
	v_max_f32_e32 v208, 0, v185
	v_fmac_f32_e32 v201, v152, v204
	v_max_f32_e32 v204, 0, v186
	v_fmac_f32_e32 v201, v153, v208
	v_max_f32_e32 v208, 0, v187
	v_fmac_f32_e32 v201, v154, v204
	v_max_f32_e32 v204, 0, v188
	v_fmac_f32_e32 v201, v155, v208
	v_max_f32_e32 v208, 0, v189
	v_fmac_f32_e32 v201, v156, v204
	v_max_f32_e32 v204, 0, v190
	v_fmac_f32_e32 v201, v157, v208
	v_max_f32_e32 v208, 0, v191
	v_fmac_f32_e32 v201, v158, v204
	v_fmac_f32_e32 v201, v159, v208
	v_cndmask_b32_e32 v201, v61, v201, vcc
	v_ashrrev_i32_e32 v207, 31, v201
	v_or_b32_e32 v207, 0x80000000, v207
	v_xor_b32_e32 v113, v201, v207
	s_cmp_le_u32 s15, 50
	s_cbranch_scc1 .Lidx_search
	s_cmp_le_u32 s15, 51
	s_cbranch_scc1 .Lidx_p51
	global_load_dwordx4 v[34:37], v57, s[20:21]
	global_load_dwordx4 v[38:41], v57, s[20:21] offset:1024
	global_load_dwordx4 v[42:45], v57, s[20:21] offset:2048
	global_load_dwordx4 v[46:49], v57, s[20:21] offset:3072
	s_add_u32 s20, s20, 0x1000
	s_addc_u32 s21, s21, 0
	s_waitcnt vmcnt(8)
	v_mfma_f32_32x32x16_bf16 v[176:191], v[128:131], v[2:5], 0
	v_mfma_f32_32x32x16_bf16 v[176:191], v[132:135], v[6:9], v[176:191]
	v_mfma_f32_32x32x16_bf16 v[176:191], v[136:139], v[10:13], v[176:191]
	v_mfma_f32_32x32x16_bf16 v[176:191], v[140:143], v[14:17], v[176:191]
.Lidx_p51:
	v_cmp_le_i32_e32 vcc, 0x640, v59
	v_max_f32_e32 v204, 0, v160
	v_max_f32_e32 v208, 0, v161
	v_fma_f32 v201, v144, v204, 0
	v_max_f32_e32 v204, 0, v162
	v_fmac_f32_e32 v201, v145, v208
	v_max_f32_e32 v208, 0, v163
	v_fmac_f32_e32 v201, v146, v204
	v_max_f32_e32 v204, 0, v164
	v_fmac_f32_e32 v201, v147, v208
	v_max_f32_e32 v208, 0, v165
	v_fmac_f32_e32 v201, v148, v204
	v_max_f32_e32 v204, 0, v166
	v_fmac_f32_e32 v201, v149, v208
	v_max_f32_e32 v208, 0, v167
	v_fmac_f32_e32 v201, v150, v204
	v_max_f32_e32 v204, 0, v168
	v_fmac_f32_e32 v201, v151, v208
	v_max_f32_e32 v208, 0, v169
	v_fmac_f32_e32 v201, v152, v204
	v_max_f32_e32 v204, 0, v170
	v_fmac_f32_e32 v201, v153, v208
	v_max_f32_e32 v208, 0, v171
	v_fmac_f32_e32 v201, v154, v204
	v_max_f32_e32 v204, 0, v172
	v_fmac_f32_e32 v201, v155, v208
	v_max_f32_e32 v208, 0, v173
	v_fmac_f32_e32 v201, v156, v204
	v_max_f32_e32 v204, 0, v174
	v_fmac_f32_e32 v201, v157, v208
	v_max_f32_e32 v208, 0, v175
	v_fmac_f32_e32 v201, v158, v204
	v_fmac_f32_e32 v201, v159, v208
	v_cndmask_b32_e32 v201, v61, v201, vcc
	v_ashrrev_i32_e32 v207, 31, v201
	v_or_b32_e32 v207, 0x80000000, v207
	v_xor_b32_e32 v114, v201, v207
	s_cmp_le_u32 s15, 51
	s_cbranch_scc1 .Lidx_search
	s_cmp_le_u32 s15, 52
	s_cbranch_scc1 .Lidx_p52
	global_load_dwordx4 v[2:5], v57, s[20:21]
	global_load_dwordx4 v[6:9], v57, s[20:21] offset:1024
	global_load_dwordx4 v[10:13], v57, s[20:21] offset:2048
	global_load_dwordx4 v[14:17], v57, s[20:21] offset:3072
	s_add_u32 s20, s20, 0x1000
	s_addc_u32 s21, s21, 0
	s_waitcnt vmcnt(8)
	v_mfma_f32_32x32x16_bf16 v[160:175], v[128:131], v[18:21], 0
	v_mfma_f32_32x32x16_bf16 v[160:175], v[132:135], v[22:25], v[160:175]
	v_mfma_f32_32x32x16_bf16 v[160:175], v[136:139], v[26:29], v[160:175]
	v_mfma_f32_32x32x16_bf16 v[160:175], v[140:143], v[30:33], v[160:175]
.Lidx_p52:
	v_cmp_le_i32_e32 vcc, 0x660, v59
	v_max_f32_e32 v204, 0, v176
	v_max_f32_e32 v208, 0, v177
	v_fma_f32 v201, v144, v204, 0
	v_max_f32_e32 v204, 0, v178
	v_fmac_f32_e32 v201, v145, v208
	v_max_f32_e32 v208, 0, v179
	v_fmac_f32_e32 v201, v146, v204
	v_max_f32_e32 v204, 0, v180
	v_fmac_f32_e32 v201, v147, v208
	v_max_f32_e32 v208, 0, v181
	v_fmac_f32_e32 v201, v148, v204
	v_max_f32_e32 v204, 0, v182
	v_fmac_f32_e32 v201, v149, v208
	v_max_f32_e32 v208, 0, v183
	v_fmac_f32_e32 v201, v150, v204
	v_max_f32_e32 v204, 0, v184
	v_fmac_f32_e32 v201, v151, v208
	v_max_f32_e32 v208, 0, v185
	v_fmac_f32_e32 v201, v152, v204
	v_max_f32_e32 v204, 0, v186
	v_fmac_f32_e32 v201, v153, v208
	v_max_f32_e32 v208, 0, v187
	v_fmac_f32_e32 v201, v154, v204
	v_max_f32_e32 v204, 0, v188
	v_fmac_f32_e32 v201, v155, v208
	v_max_f32_e32 v208, 0, v189
	v_fmac_f32_e32 v201, v156, v204
	v_max_f32_e32 v204, 0, v190
	v_fmac_f32_e32 v201, v157, v208
	v_max_f32_e32 v208, 0, v191
	v_fmac_f32_e32 v201, v158, v204
	v_fmac_f32_e32 v201, v159, v208
	v_cndmask_b32_e32 v201, v61, v201, vcc
	v_ashrrev_i32_e32 v207, 31, v201
	v_or_b32_e32 v207, 0x80000000, v207
	v_xor_b32_e32 v115, v201, v207
	s_cmp_le_u32 s15, 52
	s_cbranch_scc1 .Lidx_search
	s_cmp_le_u32 s15, 53
	s_cbranch_scc1 .Lidx_p53
	global_load_dwordx4 v[18:21], v57, s[20:21]
	global_load_dwordx4 v[22:25], v57, s[20:21] offset:1024
	global_load_dwordx4 v[26:29], v57, s[20:21] offset:2048
	global_load_dwordx4 v[30:33], v57, s[20:21] offset:3072
	s_add_u32 s20, s20, 0x1000
	s_addc_u32 s21, s21, 0
	s_waitcnt vmcnt(8)
	v_mfma_f32_32x32x16_bf16 v[176:191], v[128:131], v[34:37], 0
	v_mfma_f32_32x32x16_bf16 v[176:191], v[132:135], v[38:41], v[176:191]
	v_mfma_f32_32x32x16_bf16 v[176:191], v[136:139], v[42:45], v[176:191]
	v_mfma_f32_32x32x16_bf16 v[176:191], v[140:143], v[46:49], v[176:191]
.Lidx_p53:
	v_cmp_le_i32_e32 vcc, 0x680, v59
	v_max_f32_e32 v204, 0, v160
	v_max_f32_e32 v208, 0, v161
	v_fma_f32 v201, v144, v204, 0
	v_max_f32_e32 v204, 0, v162
	v_fmac_f32_e32 v201, v145, v208
	v_max_f32_e32 v208, 0, v163
	v_fmac_f32_e32 v201, v146, v204
	v_max_f32_e32 v204, 0, v164
	v_fmac_f32_e32 v201, v147, v208
	v_max_f32_e32 v208, 0, v165
	v_fmac_f32_e32 v201, v148, v204
	v_max_f32_e32 v204, 0, v166
	v_fmac_f32_e32 v201, v149, v208
	v_max_f32_e32 v208, 0, v167
	v_fmac_f32_e32 v201, v150, v204
	v_max_f32_e32 v204, 0, v168
	v_fmac_f32_e32 v201, v151, v208
	v_max_f32_e32 v208, 0, v169
	v_fmac_f32_e32 v201, v152, v204
	v_max_f32_e32 v204, 0, v170
	v_fmac_f32_e32 v201, v153, v208
	v_max_f32_e32 v208, 0, v171
	v_fmac_f32_e32 v201, v154, v204
	v_max_f32_e32 v204, 0, v172
	v_fmac_f32_e32 v201, v155, v208
	v_max_f32_e32 v208, 0, v173
	v_fmac_f32_e32 v201, v156, v204
	v_max_f32_e32 v204, 0, v174
	v_fmac_f32_e32 v201, v157, v208
	v_max_f32_e32 v208, 0, v175
	v_fmac_f32_e32 v201, v158, v204
	v_fmac_f32_e32 v201, v159, v208
	v_cndmask_b32_e32 v201, v61, v201, vcc
	v_ashrrev_i32_e32 v207, 31, v201
	v_or_b32_e32 v207, 0x80000000, v207
	v_xor_b32_e32 v116, v201, v207
	s_cmp_le_u32 s15, 53
	s_cbranch_scc1 .Lidx_search
	s_cmp_le_u32 s15, 54
	s_cbranch_scc1 .Lidx_p54
	global_load_dwordx4 v[34:37], v57, s[20:21]
	global_load_dwordx4 v[38:41], v57, s[20:21] offset:1024
	global_load_dwordx4 v[42:45], v57, s[20:21] offset:2048
	global_load_dwordx4 v[46:49], v57, s[20:21] offset:3072
	s_add_u32 s20, s20, 0x1000
	s_addc_u32 s21, s21, 0
	s_waitcnt vmcnt(8)
	v_mfma_f32_32x32x16_bf16 v[160:175], v[128:131], v[2:5], 0
	v_mfma_f32_32x32x16_bf16 v[160:175], v[132:135], v[6:9], v[160:175]
	v_mfma_f32_32x32x16_bf16 v[160:175], v[136:139], v[10:13], v[160:175]
	v_mfma_f32_32x32x16_bf16 v[160:175], v[140:143], v[14:17], v[160:175]
.Lidx_p54:
	v_cmp_le_i32_e32 vcc, 0x6a0, v59
	v_max_f32_e32 v204, 0, v176
	v_max_f32_e32 v208, 0, v177
	v_fma_f32 v201, v144, v204, 0
	v_max_f32_e32 v204, 0, v178
	v_fmac_f32_e32 v201, v145, v208
	v_max_f32_e32 v208, 0, v179
	v_fmac_f32_e32 v201, v146, v204
	v_max_f32_e32 v204, 0, v180
	v_fmac_f32_e32 v201, v147, v208
	v_max_f32_e32 v208, 0, v181
	v_fmac_f32_e32 v201, v148, v204
	v_max_f32_e32 v204, 0, v182
	v_fmac_f32_e32 v201, v149, v208
	v_max_f32_e32 v208, 0, v183
	v_fmac_f32_e32 v201, v150, v204
	v_max_f32_e32 v204, 0, v184
	v_fmac_f32_e32 v201, v151, v208
	v_max_f32_e32 v208, 0, v185
	v_fmac_f32_e32 v201, v152, v204
	v_max_f32_e32 v204, 0, v186
	v_fmac_f32_e32 v201, v153, v208
	v_max_f32_e32 v208, 0, v187
	v_fmac_f32_e32 v201, v154, v204
	v_max_f32_e32 v204, 0, v188
	v_fmac_f32_e32 v201, v155, v208
	v_max_f32_e32 v208, 0, v189
	v_fmac_f32_e32 v201, v156, v204
	v_max_f32_e32 v204, 0, v190
	v_fmac_f32_e32 v201, v157, v208
	v_max_f32_e32 v208, 0, v191
	v_fmac_f32_e32 v201, v158, v204
	v_fmac_f32_e32 v201, v159, v208
	v_cndmask_b32_e32 v201, v61, v201, vcc
	v_ashrrev_i32_e32 v207, 31, v201
	v_or_b32_e32 v207, 0x80000000, v207
	v_xor_b32_e32 v117, v201, v207
	s_cmp_le_u32 s15, 54
	s_cbranch_scc1 .Lidx_search
	s_cmp_le_u32 s15, 55
	s_cbranch_scc1 .Lidx_p55
	global_load_dwordx4 v[2:5], v57, s[20:21]
	global_load_dwordx4 v[6:9], v57, s[20:21] offset:1024
	global_load_dwordx4 v[10:13], v57, s[20:21] offset:2048
	global_load_dwordx4 v[14:17], v57, s[20:21] offset:3072
	s_add_u32 s20, s20, 0x1000
	s_addc_u32 s21, s21, 0
	s_waitcnt vmcnt(8)
	v_mfma_f32_32x32x16_bf16 v[176:191], v[128:131], v[18:21], 0
	v_mfma_f32_32x32x16_bf16 v[176:191], v[132:135], v[22:25], v[176:191]
	v_mfma_f32_32x32x16_bf16 v[176:191], v[136:139], v[26:29], v[176:191]
	v_mfma_f32_32x32x16_bf16 v[176:191], v[140:143], v[30:33], v[176:191]
.Lidx_p55:
	v_cmp_le_i32_e32 vcc, 0x6c0, v59
	v_max_f32_e32 v204, 0, v160
	v_max_f32_e32 v208, 0, v161
	v_fma_f32 v201, v144, v204, 0
	v_max_f32_e32 v204, 0, v162
	v_fmac_f32_e32 v201, v145, v208
	v_max_f32_e32 v208, 0, v163
	v_fmac_f32_e32 v201, v146, v204
	v_max_f32_e32 v204, 0, v164
	v_fmac_f32_e32 v201, v147, v208
	v_max_f32_e32 v208, 0, v165
	v_fmac_f32_e32 v201, v148, v204
	v_max_f32_e32 v204, 0, v166
	v_fmac_f32_e32 v201, v149, v208
	v_max_f32_e32 v208, 0, v167
	v_fmac_f32_e32 v201, v150, v204
	v_max_f32_e32 v204, 0, v168
	v_fmac_f32_e32 v201, v151, v208
	v_max_f32_e32 v208, 0, v169
	v_fmac_f32_e32 v201, v152, v204
	v_max_f32_e32 v204, 0, v170
	v_fmac_f32_e32 v201, v153, v208
	v_max_f32_e32 v208, 0, v171
	v_fmac_f32_e32 v201, v154, v204
	v_max_f32_e32 v204, 0, v172
	v_fmac_f32_e32 v201, v155, v208
	v_max_f32_e32 v208, 0, v173
	v_fmac_f32_e32 v201, v156, v204
	v_max_f32_e32 v204, 0, v174
	v_fmac_f32_e32 v201, v157, v208
	v_max_f32_e32 v208, 0, v175
	v_fmac_f32_e32 v201, v158, v204
	v_fmac_f32_e32 v201, v159, v208
	v_cndmask_b32_e32 v201, v61, v201, vcc
	v_ashrrev_i32_e32 v207, 31, v201
	v_or_b32_e32 v207, 0x80000000, v207
	v_xor_b32_e32 v118, v201, v207
	s_cmp_le_u32 s15, 55
	s_cbranch_scc1 .Lidx_search
	s_cmp_le_u32 s15, 56
	s_cbranch_scc1 .Lidx_p56
	global_load_dwordx4 v[18:21], v57, s[20:21]
	global_load_dwordx4 v[22:25], v57, s[20:21] offset:1024
	global_load_dwordx4 v[26:29], v57, s[20:21] offset:2048
	global_load_dwordx4 v[30:33], v57, s[20:21] offset:3072
	s_add_u32 s20, s20, 0x1000
	s_addc_u32 s21, s21, 0
	s_waitcnt vmcnt(8)
	v_mfma_f32_32x32x16_bf16 v[160:175], v[128:131], v[34:37], 0
	v_mfma_f32_32x32x16_bf16 v[160:175], v[132:135], v[38:41], v[160:175]
	v_mfma_f32_32x32x16_bf16 v[160:175], v[136:139], v[42:45], v[160:175]
	v_mfma_f32_32x32x16_bf16 v[160:175], v[140:143], v[46:49], v[160:175]
.Lidx_p56:
	v_cmp_le_i32_e32 vcc, 0x6e0, v59
	v_max_f32_e32 v204, 0, v176
	v_max_f32_e32 v208, 0, v177
	v_fma_f32 v201, v144, v204, 0
	v_max_f32_e32 v204, 0, v178
	v_fmac_f32_e32 v201, v145, v208
	v_max_f32_e32 v208, 0, v179
	v_fmac_f32_e32 v201, v146, v204
	v_max_f32_e32 v204, 0, v180
	v_fmac_f32_e32 v201, v147, v208
	v_max_f32_e32 v208, 0, v181
	v_fmac_f32_e32 v201, v148, v204
	v_max_f32_e32 v204, 0, v182
	v_fmac_f32_e32 v201, v149, v208
	v_max_f32_e32 v208, 0, v183
	v_fmac_f32_e32 v201, v150, v204
	v_max_f32_e32 v204, 0, v184
	v_fmac_f32_e32 v201, v151, v208
	v_max_f32_e32 v208, 0, v185
	v_fmac_f32_e32 v201, v152, v204
	v_max_f32_e32 v204, 0, v186
	v_fmac_f32_e32 v201, v153, v208
	v_max_f32_e32 v208, 0, v187
	v_fmac_f32_e32 v201, v154, v204
	v_max_f32_e32 v204, 0, v188
	v_fmac_f32_e32 v201, v155, v208
	v_max_f32_e32 v208, 0, v189
	v_fmac_f32_e32 v201, v156, v204
	v_max_f32_e32 v204, 0, v190
	v_fmac_f32_e32 v201, v157, v208
	v_max_f32_e32 v208, 0, v191
	v_fmac_f32_e32 v201, v158, v204
	v_fmac_f32_e32 v201, v159, v208
	v_cndmask_b32_e32 v201, v61, v201, vcc
	v_ashrrev_i32_e32 v207, 31, v201
	v_or_b32_e32 v207, 0x80000000, v207
	v_xor_b32_e32 v119, v201, v207
	s_cmp_le_u32 s15, 56
	s_cbranch_scc1 .Lidx_search
	s_cmp_le_u32 s15, 57
	s_cbranch_scc1 .Lidx_p57
	global_load_dwordx4 v[34:37], v57, s[20:21]
	global_load_dwordx4 v[38:41], v57, s[20:21] offset:1024
	global_load_dwordx4 v[42:45], v57, s[20:21] offset:2048
	global_load_dwordx4 v[46:49], v57, s[20:21] offset:3072
	s_add_u32 s20, s20, 0x1000
	s_addc_u32 s21, s21, 0
	s_waitcnt vmcnt(8)
	v_mfma_f32_32x32x16_bf16 v[176:191], v[128:131], v[2:5], 0
	v_mfma_f32_32x32x16_bf16 v[176:191], v[132:135], v[6:9], v[176:191]
	v_mfma_f32_32x32x16_bf16 v[176:191], v[136:139], v[10:13], v[176:191]
	v_mfma_f32_32x32x16_bf16 v[176:191], v[140:143], v[14:17], v[176:191]
.Lidx_p57:
	v_cmp_le_i32_e32 vcc, 0x700, v59
	v_max_f32_e32 v204, 0, v160
	v_max_f32_e32 v208, 0, v161
	v_fma_f32 v201, v144, v204, 0
	v_max_f32_e32 v204, 0, v162
	v_fmac_f32_e32 v201, v145, v208
	v_max_f32_e32 v208, 0, v163
	v_fmac_f32_e32 v201, v146, v204
	v_max_f32_e32 v204, 0, v164
	v_fmac_f32_e32 v201, v147, v208
	v_max_f32_e32 v208, 0, v165
	v_fmac_f32_e32 v201, v148, v204
	v_max_f32_e32 v204, 0, v166
	v_fmac_f32_e32 v201, v149, v208
	v_max_f32_e32 v208, 0, v167
	v_fmac_f32_e32 v201, v150, v204
	v_max_f32_e32 v204, 0, v168
	v_fmac_f32_e32 v201, v151, v208
	v_max_f32_e32 v208, 0, v169
	v_fmac_f32_e32 v201, v152, v204
	v_max_f32_e32 v204, 0, v170
	v_fmac_f32_e32 v201, v153, v208
	v_max_f32_e32 v208, 0, v171
	v_fmac_f32_e32 v201, v154, v204
	v_max_f32_e32 v204, 0, v172
	v_fmac_f32_e32 v201, v155, v208
	v_max_f32_e32 v208, 0, v173
	v_fmac_f32_e32 v201, v156, v204
	v_max_f32_e32 v204, 0, v174
	v_fmac_f32_e32 v201, v157, v208
	v_max_f32_e32 v208, 0, v175
	v_fmac_f32_e32 v201, v158, v204
	v_fmac_f32_e32 v201, v159, v208
	v_cndmask_b32_e32 v201, v61, v201, vcc
	v_ashrrev_i32_e32 v207, 31, v201
	v_or_b32_e32 v207, 0x80000000, v207
	v_xor_b32_e32 v120, v201, v207
	s_cmp_le_u32 s15, 57
	s_cbranch_scc1 .Lidx_search
	s_cmp_le_u32 s15, 58
	s_cbranch_scc1 .Lidx_p58
	global_load_dwordx4 v[2:5], v57, s[20:21]
	global_load_dwordx4 v[6:9], v57, s[20:21] offset:1024
	global_load_dwordx4 v[10:13], v57, s[20:21] offset:2048
	global_load_dwordx4 v[14:17], v57, s[20:21] offset:3072
	s_add_u32 s20, s20, 0x1000
	s_addc_u32 s21, s21, 0
	s_waitcnt vmcnt(8)
	v_mfma_f32_32x32x16_bf16 v[160:175], v[128:131], v[18:21], 0
	v_mfma_f32_32x32x16_bf16 v[160:175], v[132:135], v[22:25], v[160:175]
	v_mfma_f32_32x32x16_bf16 v[160:175], v[136:139], v[26:29], v[160:175]
	v_mfma_f32_32x32x16_bf16 v[160:175], v[140:143], v[30:33], v[160:175]
.Lidx_p58:
	v_cmp_le_i32_e32 vcc, 0x720, v59
	v_max_f32_e32 v204, 0, v176
	v_max_f32_e32 v208, 0, v177
	v_fma_f32 v201, v144, v204, 0
	v_max_f32_e32 v204, 0, v178
	v_fmac_f32_e32 v201, v145, v208
	v_max_f32_e32 v208, 0, v179
	v_fmac_f32_e32 v201, v146, v204
	v_max_f32_e32 v204, 0, v180
	v_fmac_f32_e32 v201, v147, v208
	v_max_f32_e32 v208, 0, v181
	v_fmac_f32_e32 v201, v148, v204
	v_max_f32_e32 v204, 0, v182
	v_fmac_f32_e32 v201, v149, v208
	v_max_f32_e32 v208, 0, v183
	v_fmac_f32_e32 v201, v150, v204
	v_max_f32_e32 v204, 0, v184
	v_fmac_f32_e32 v201, v151, v208
	v_max_f32_e32 v208, 0, v185
	v_fmac_f32_e32 v201, v152, v204
	v_max_f32_e32 v204, 0, v186
	v_fmac_f32_e32 v201, v153, v208
	v_max_f32_e32 v208, 0, v187
	v_fmac_f32_e32 v201, v154, v204
	v_max_f32_e32 v204, 0, v188
	v_fmac_f32_e32 v201, v155, v208
	v_max_f32_e32 v208, 0, v189
	v_fmac_f32_e32 v201, v156, v204
	v_max_f32_e32 v204, 0, v190
	v_fmac_f32_e32 v201, v157, v208
	v_max_f32_e32 v208, 0, v191
	v_fmac_f32_e32 v201, v158, v204
	v_fmac_f32_e32 v201, v159, v208
	v_cndmask_b32_e32 v201, v61, v201, vcc
	v_ashrrev_i32_e32 v207, 31, v201
	v_or_b32_e32 v207, 0x80000000, v207
	v_xor_b32_e32 v121, v201, v207
	s_cmp_le_u32 s15, 58
	s_cbranch_scc1 .Lidx_search
	s_cmp_le_u32 s15, 59
	s_cbranch_scc1 .Lidx_p59
	global_load_dwordx4 v[18:21], v57, s[20:21]
	global_load_dwordx4 v[22:25], v57, s[20:21] offset:1024
	global_load_dwordx4 v[26:29], v57, s[20:21] offset:2048
	global_load_dwordx4 v[30:33], v57, s[20:21] offset:3072
	s_add_u32 s20, s20, 0x1000
	s_addc_u32 s21, s21, 0
	s_waitcnt vmcnt(8)
	v_mfma_f32_32x32x16_bf16 v[176:191], v[128:131], v[34:37], 0
	v_mfma_f32_32x32x16_bf16 v[176:191], v[132:135], v[38:41], v[176:191]
	v_mfma_f32_32x32x16_bf16 v[176:191], v[136:139], v[42:45], v[176:191]
	v_mfma_f32_32x32x16_bf16 v[176:191], v[140:143], v[46:49], v[176:191]
.Lidx_p59:
	v_cmp_le_i32_e32 vcc, 0x740, v59
	v_max_f32_e32 v204, 0, v160
	v_max_f32_e32 v208, 0, v161
	v_fma_f32 v201, v144, v204, 0
	v_max_f32_e32 v204, 0, v162
	v_fmac_f32_e32 v201, v145, v208
	v_max_f32_e32 v208, 0, v163
	v_fmac_f32_e32 v201, v146, v204
	v_max_f32_e32 v204, 0, v164
	v_fmac_f32_e32 v201, v147, v208
	v_max_f32_e32 v208, 0, v165
	v_fmac_f32_e32 v201, v148, v204
	v_max_f32_e32 v204, 0, v166
	v_fmac_f32_e32 v201, v149, v208
	v_max_f32_e32 v208, 0, v167
	v_fmac_f32_e32 v201, v150, v204
	v_max_f32_e32 v204, 0, v168
	v_fmac_f32_e32 v201, v151, v208
	v_max_f32_e32 v208, 0, v169
	v_fmac_f32_e32 v201, v152, v204
	v_max_f32_e32 v204, 0, v170
	v_fmac_f32_e32 v201, v153, v208
	v_max_f32_e32 v208, 0, v171
	v_fmac_f32_e32 v201, v154, v204
	v_max_f32_e32 v204, 0, v172
	v_fmac_f32_e32 v201, v155, v208
	v_max_f32_e32 v208, 0, v173
	v_fmac_f32_e32 v201, v156, v204
	v_max_f32_e32 v204, 0, v174
	v_fmac_f32_e32 v201, v157, v208
	v_max_f32_e32 v208, 0, v175
	v_fmac_f32_e32 v201, v158, v204
	v_fmac_f32_e32 v201, v159, v208
	v_cndmask_b32_e32 v201, v61, v201, vcc
	v_ashrrev_i32_e32 v207, 31, v201
	v_or_b32_e32 v207, 0x80000000, v207
	v_xor_b32_e32 v122, v201, v207
	s_cmp_le_u32 s15, 59
	s_cbranch_scc1 .Lidx_search
	s_cmp_le_u32 s15, 60
	s_cbranch_scc1 .Lidx_p60
	global_load_dwordx4 v[34:37], v57, s[20:21]
	global_load_dwordx4 v[38:41], v57, s[20:21] offset:1024
	global_load_dwordx4 v[42:45], v57, s[20:21] offset:2048
	global_load_dwordx4 v[46:49], v57, s[20:21] offset:3072
	s_add_u32 s20, s20, 0x1000
	s_addc_u32 s21, s21, 0
	s_waitcnt vmcnt(8)
	v_mfma_f32_32x32x16_bf16 v[160:175], v[128:131], v[2:5], 0
	v_mfma_f32_32x32x16_bf16 v[160:175], v[132:135], v[6:9], v[160:175]
	v_mfma_f32_32x32x16_bf16 v[160:175], v[136:139], v[10:13], v[160:175]
	v_mfma_f32_32x32x16_bf16 v[160:175], v[140:143], v[14:17], v[160:175]
.Lidx_p60:
	v_cmp_le_i32_e32 vcc, 0x760, v59
	v_max_f32_e32 v204, 0, v176
	v_max_f32_e32 v208, 0, v177
	v_fma_f32 v201, v144, v204, 0
	v_max_f32_e32 v204, 0, v178
	v_fmac_f32_e32 v201, v145, v208
	v_max_f32_e32 v208, 0, v179
	v_fmac_f32_e32 v201, v146, v204
	v_max_f32_e32 v204, 0, v180
	v_fmac_f32_e32 v201, v147, v208
	v_max_f32_e32 v208, 0, v181
	v_fmac_f32_e32 v201, v148, v204
	v_max_f32_e32 v204, 0, v182
	v_fmac_f32_e32 v201, v149, v208
	v_max_f32_e32 v208, 0, v183
	v_fmac_f32_e32 v201, v150, v204
	v_max_f32_e32 v204, 0, v184
	v_fmac_f32_e32 v201, v151, v208
	v_max_f32_e32 v208, 0, v185
	v_fmac_f32_e32 v201, v152, v204
	v_max_f32_e32 v204, 0, v186
	v_fmac_f32_e32 v201, v153, v208
	v_max_f32_e32 v208, 0, v187
	v_fmac_f32_e32 v201, v154, v204
	v_max_f32_e32 v204, 0, v188
	v_fmac_f32_e32 v201, v155, v208
	v_max_f32_e32 v208, 0, v189
	v_fmac_f32_e32 v201, v156, v204
	v_max_f32_e32 v204, 0, v190
	v_fmac_f32_e32 v201, v157, v208
	v_max_f32_e32 v208, 0, v191
	v_fmac_f32_e32 v201, v158, v204
	v_fmac_f32_e32 v201, v159, v208
	v_cndmask_b32_e32 v201, v61, v201, vcc
	v_ashrrev_i32_e32 v207, 31, v201
	v_or_b32_e32 v207, 0x80000000, v207
	v_xor_b32_e32 v123, v201, v207
	s_cmp_le_u32 s15, 60
	s_cbranch_scc1 .Lidx_search
	s_cmp_le_u32 s15, 61
	s_cbranch_scc1 .Lidx_p61
	global_load_dwordx4 v[2:5], v57, s[20:21]
	global_load_dwordx4 v[6:9], v57, s[20:21] offset:1024
	global_load_dwordx4 v[10:13], v57, s[20:21] offset:2048
	global_load_dwordx4 v[14:17], v57, s[20:21] offset:3072
	s_add_u32 s20, s20, 0x1000
	s_addc_u32 s21, s21, 0
	s_waitcnt vmcnt(8)
	v_mfma_f32_32x32x16_bf16 v[176:191], v[128:131], v[18:21], 0
	v_mfma_f32_32x32x16_bf16 v[176:191], v[132:135], v[22:25], v[176:191]
	v_mfma_f32_32x32x16_bf16 v[176:191], v[136:139], v[26:29], v[176:191]
	v_mfma_f32_32x32x16_bf16 v[176:191], v[140:143], v[30:33], v[176:191]
.Lidx_p61:
	v_cmp_le_i32_e32 vcc, 0x780, v59
	v_max_f32_e32 v204, 0, v160
	v_max_f32_e32 v208, 0, v161
	v_fma_f32 v201, v144, v204, 0
	v_max_f32_e32 v204, 0, v162
	v_fmac_f32_e32 v201, v145, v208
	v_max_f32_e32 v208, 0, v163
	v_fmac_f32_e32 v201, v146, v204
	v_max_f32_e32 v204, 0, v164
	v_fmac_f32_e32 v201, v147, v208
	v_max_f32_e32 v208, 0, v165
	v_fmac_f32_e32 v201, v148, v204
	v_max_f32_e32 v204, 0, v166
	v_fmac_f32_e32 v201, v149, v208
	v_max_f32_e32 v208, 0, v167
	v_fmac_f32_e32 v201, v150, v204
	v_max_f32_e32 v204, 0, v168
	v_fmac_f32_e32 v201, v151, v208
	v_max_f32_e32 v208, 0, v169
	v_fmac_f32_e32 v201, v152, v204
	v_max_f32_e32 v204, 0, v170
	v_fmac_f32_e32 v201, v153, v208
	v_max_f32_e32 v208, 0, v171
	v_fmac_f32_e32 v201, v154, v204
	v_max_f32_e32 v204, 0, v172
	v_fmac_f32_e32 v201, v155, v208
	v_max_f32_e32 v208, 0, v173
	v_fmac_f32_e32 v201, v156, v204
	v_max_f32_e32 v204, 0, v174
	v_fmac_f32_e32 v201, v157, v208
	v_max_f32_e32 v208, 0, v175
	v_fmac_f32_e32 v201, v158, v204
	v_fmac_f32_e32 v201, v159, v208
	v_cndmask_b32_e32 v201, v61, v201, vcc
	v_ashrrev_i32_e32 v207, 31, v201
	v_or_b32_e32 v207, 0x80000000, v207
	v_xor_b32_e32 v124, v201, v207
	s_cmp_le_u32 s15, 61
	s_cbranch_scc1 .Lidx_search
	s_cmp_le_u32 s15, 62
	s_cbranch_scc1 .Lidx_p62
	s_waitcnt vmcnt(4)
	v_mfma_f32_32x32x16_bf16 v[160:175], v[128:131], v[34:37], 0
	v_mfma_f32_32x32x16_bf16 v[160:175], v[132:135], v[38:41], v[160:175]
	v_mfma_f32_32x32x16_bf16 v[160:175], v[136:139], v[42:45], v[160:175]
	v_mfma_f32_32x32x16_bf16 v[160:175], v[140:143], v[46:49], v[160:175]
.Lidx_p62:
	v_cmp_le_i32_e32 vcc, 0x7a0, v59
	v_max_f32_e32 v204, 0, v176
	v_max_f32_e32 v208, 0, v177
	v_fma_f32 v201, v144, v204, 0
	v_max_f32_e32 v204, 0, v178
	v_fmac_f32_e32 v201, v145, v208
	v_max_f32_e32 v208, 0, v179
	v_fmac_f32_e32 v201, v146, v204
	v_max_f32_e32 v204, 0, v180
	v_fmac_f32_e32 v201, v147, v208
	v_max_f32_e32 v208, 0, v181
	v_fmac_f32_e32 v201, v148, v204
	v_max_f32_e32 v204, 0, v182
	v_fmac_f32_e32 v201, v149, v208
	v_max_f32_e32 v208, 0, v183
	v_fmac_f32_e32 v201, v150, v204
	v_max_f32_e32 v204, 0, v184
	v_fmac_f32_e32 v201, v151, v208
	v_max_f32_e32 v208, 0, v185
	v_fmac_f32_e32 v201, v152, v204
	v_max_f32_e32 v204, 0, v186
	v_fmac_f32_e32 v201, v153, v208
	v_max_f32_e32 v208, 0, v187
	v_fmac_f32_e32 v201, v154, v204
	v_max_f32_e32 v204, 0, v188
	v_fmac_f32_e32 v201, v155, v208
	v_max_f32_e32 v208, 0, v189
	v_fmac_f32_e32 v201, v156, v204
	v_max_f32_e32 v204, 0, v190
	v_fmac_f32_e32 v201, v157, v208
	v_max_f32_e32 v208, 0, v191
	v_fmac_f32_e32 v201, v158, v204
	v_fmac_f32_e32 v201, v159, v208
	v_cndmask_b32_e32 v201, v61, v201, vcc
	v_ashrrev_i32_e32 v207, 31, v201
	v_or_b32_e32 v207, 0x80000000, v207
	v_xor_b32_e32 v125, v201, v207
	s_cmp_le_u32 s15, 62
	s_cbranch_scc1 .Lidx_search
	s_cmp_le_u32 s15, 63
	s_cbranch_scc1 .Lidx_p63
	s_waitcnt vmcnt(0)
	v_mfma_f32_32x32x16_bf16 v[176:191], v[128:131], v[2:5], 0
	v_mfma_f32_32x32x16_bf16 v[176:191], v[132:135], v[6:9], v[176:191]
	v_mfma_f32_32x32x16_bf16 v[176:191], v[136:139], v[10:13], v[176:191]
	v_mfma_f32_32x32x16_bf16 v[176:191], v[140:143], v[14:17], v[176:191]
.Lidx_p63:
	v_cmp_le_i32_e32 vcc, 0x7c0, v59
	v_max_f32_e32 v204, 0, v160
	v_max_f32_e32 v208, 0, v161
	v_fma_f32 v201, v144, v204, 0
	v_max_f32_e32 v204, 0, v162
	v_fmac_f32_e32 v201, v145, v208
	v_max_f32_e32 v208, 0, v163
	v_fmac_f32_e32 v201, v146, v204
	v_max_f32_e32 v204, 0, v164
	v_fmac_f32_e32 v201, v147, v208
	v_max_f32_e32 v208, 0, v165
	v_fmac_f32_e32 v201, v148, v204
	v_max_f32_e32 v204, 0, v166
	v_fmac_f32_e32 v201, v149, v208
	v_max_f32_e32 v208, 0, v167
	v_fmac_f32_e32 v201, v150, v204
	v_max_f32_e32 v204, 0, v168
	v_fmac_f32_e32 v201, v151, v208
	v_max_f32_e32 v208, 0, v169
	v_fmac_f32_e32 v201, v152, v204
	v_max_f32_e32 v204, 0, v170
	v_fmac_f32_e32 v201, v153, v208
	v_max_f32_e32 v208, 0, v171
	v_fmac_f32_e32 v201, v154, v204
	v_max_f32_e32 v204, 0, v172
	v_fmac_f32_e32 v201, v155, v208
	v_max_f32_e32 v208, 0, v173
	v_fmac_f32_e32 v201, v156, v204
	v_max_f32_e32 v204, 0, v174
	v_fmac_f32_e32 v201, v157, v208
	v_max_f32_e32 v208, 0, v175
	v_fmac_f32_e32 v201, v158, v204
	v_fmac_f32_e32 v201, v159, v208
	v_cndmask_b32_e32 v201, v61, v201, vcc
	v_ashrrev_i32_e32 v207, 31, v201
	v_or_b32_e32 v207, 0x80000000, v207
	v_xor_b32_e32 v126, v201, v207
	s_cmp_le_u32 s15, 63
	s_cbranch_scc1 .Lidx_search
	s_nop 15
	v_cmp_le_i32_e32 vcc, 0x7e0, v59
	v_max_f32_e32 v204, 0, v176
	v_max_f32_e32 v208, 0, v177
	v_fma_f32 v201, v144, v204, 0
	v_max_f32_e32 v204, 0, v178
	v_fmac_f32_e32 v201, v145, v208
	v_max_f32_e32 v208, 0, v179
	v_fmac_f32_e32 v201, v146, v204
	v_max_f32_e32 v204, 0, v180
	v_fmac_f32_e32 v201, v147, v208
	v_max_f32_e32 v208, 0, v181
	v_fmac_f32_e32 v201, v148, v204
	v_max_f32_e32 v204, 0, v182
	v_fmac_f32_e32 v201, v149, v208
	v_max_f32_e32 v208, 0, v183
	v_fmac_f32_e32 v201, v150, v204
	v_max_f32_e32 v204, 0, v184
	v_fmac_f32_e32 v201, v151, v208
	v_max_f32_e32 v208, 0, v185
	v_fmac_f32_e32 v201, v152, v204
	v_max_f32_e32 v204, 0, v186
	v_fmac_f32_e32 v201, v153, v208
	v_max_f32_e32 v208, 0, v187
	v_fmac_f32_e32 v201, v154, v204
	v_max_f32_e32 v204, 0, v188
	v_fmac_f32_e32 v201, v155, v208
	v_max_f32_e32 v208, 0, v189
	v_fmac_f32_e32 v201, v156, v204
	v_max_f32_e32 v204, 0, v190
	v_fmac_f32_e32 v201, v157, v208
	v_max_f32_e32 v208, 0, v191
	v_fmac_f32_e32 v201, v158, v204
	v_fmac_f32_e32 v201, v159, v208
	v_cndmask_b32_e32 v201, v61, v201, vcc
	v_ashrrev_i32_e32 v207, 31, v201
	v_or_b32_e32 v207, 0x80000000, v207
	v_xor_b32_e32 v127, v201, v207
.Lidx_search:
	s_waitcnt vmcnt(0)
	v_mov_b32_e32 v62, 0
	s_mov_b32 s24, 0x80000000
.Lidx_step:
	v_or_b32_e32 v63, s24, v62
	v_mov_b32_e32 v200, 0
	v_cmp_ge_u32_e64 s[34:35], v64, v63
	v_cmp_ge_u32_e64 s[36:37], v65, v63
	v_cmp_ge_u32_e64 s[38:39], v66, v63
	v_addc_co_u32_e64 v200, vcc, 0, v200, s[34:35]
	v_cmp_ge_u32_e64 s[40:41], v67, v63
	v_addc_co_u32_e64 v200, vcc, 0, v200, s[36:37]
	v_cmp_ge_u32_e64 s[34:35], v68, v63
	v_addc_co_u32_e64 v200, vcc, 0, v200, s[38:39]
	v_cmp_ge_u32_e64 s[36:37], v69, v63
	v_addc_co_u32_e64 v200, vcc, 0, v200, s[40:41]
	v_cmp_ge_u32_e64 s[38:39], v70, v63
	v_addc_co_u32_e64 v200, vcc, 0, v200, s[34:35]
	v_cmp_ge_u32_e64 s[40:41], v71, v63
	v_addc_co_u32_e64 v200, vcc, 0, v200, s[36:37]
	v_addc_co_u32_e64 v200, vcc, 0, v200, s[38:39]
	v_addc_co_u32_e64 v200, vcc, 0, v200, s[40:41]
	s_cmp_le_u32 s16, 1
	s_cbranch_scc1 .Lidx_red
	v_cmp_ge_u32_e64 s[34:35], v72, v63
	v_cmp_ge_u32_e64 s[36:37], v73, v63
	v_cmp_ge_u32_e64 s[38:39], v74, v63
	v_addc_co_u32_e64 v200, vcc, 0, v200, s[34:35]
	v_cmp_ge_u32_e64 s[40:41], v75, v63
	v_addc_co_u32_e64 v200, vcc, 0, v200, s[36:37]
	v_cmp_ge_u32_e64 s[34:35], v76, v63
	v_addc_co_u32_e64 v200, vcc, 0, v200, s[38:39]
	v_cmp_ge_u32_e64 s[36:37], v77, v63
	v_addc_co_u32_e64 v200, vcc, 0, v200, s[40:41]
	v_cmp_ge_u32_e64 s[38:39], v78, v63
	v_addc_co_u32_e64 v200, vcc, 0, v200, s[34:35]
	v_cmp_ge_u32_e64 s[40:41], v79, v63
	v_addc_co_u32_e64 v200, vcc, 0, v200, s[36:37]
	v_addc_co_u32_e64 v200, vcc, 0, v200, s[38:39]
	v_addc_co_u32_e64 v200, vcc, 0, v200, s[40:41]
	s_cmp_le_u32 s16, 2
	s_cbranch_scc1 .Lidx_red
	v_cmp_ge_u32_e64 s[34:35], v80, v63
	v_cmp_ge_u32_e64 s[36:37], v81, v63
	v_cmp_ge_u32_e64 s[38:39], v82, v63
	v_addc_co_u32_e64 v200, vcc, 0, v200, s[34:35]
	v_cmp_ge_u32_e64 s[40:41], v83, v63
	v_addc_co_u32_e64 v200, vcc, 0, v200, s[36:37]
	v_cmp_ge_u32_e64 s[34:35], v84, v63
	v_addc_co_u32_e64 v200, vcc, 0, v200, s[38:39]
	v_cmp_ge_u32_e64 s[36:37], v85, v63
	v_addc_co_u32_e64 v200, vcc, 0, v200, s[40:41]
	v_cmp_ge_u32_e64 s[38:39], v86, v63
	v_addc_co_u32_e64 v200, vcc, 0, v200, s[34:35]
	v_cmp_ge_u32_e64 s[40:41], v87, v63
	v_addc_co_u32_e64 v200, vcc, 0, v200, s[36:37]
	v_addc_co_u32_e64 v200, vcc, 0, v200, s[38:39]
	v_addc_co_u32_e64 v200, vcc, 0, v200, s[40:41]
	s_cmp_le_u32 s16, 3
	s_cbranch_scc1 .Lidx_red
	v_cmp_ge_u32_e64 s[34:35], v88, v63
	v_cmp_ge_u32_e64 s[36:37], v89, v63
	v_cmp_ge_u32_e64 s[38:39], v90, v63
	v_addc_co_u32_e64 v200, vcc, 0, v200, s[34:35]
	v_cmp_ge_u32_e64 s[40:41], v91, v63
	v_addc_co_u32_e64 v200, vcc, 0, v200, s[36:37]
	v_cmp_ge_u32_e64 s[34:35], v92, v63
	v_addc_co_u32_e64 v200, vcc, 0, v200, s[38:39]
	v_cmp_ge_u32_e64 s[36:37], v93, v63
	v_addc_co_u32_e64 v200, vcc, 0, v200, s[40:41]
	v_cmp_ge_u32_e64 s[38:39], v94, v63
	v_addc_co_u32_e64 v200, vcc, 0, v200, s[34:35]
	v_cmp_ge_u32_e64 s[40:41], v95, v63
	v_addc_co_u32_e64 v200, vcc, 0, v200, s[36:37]
	v_addc_co_u32_e64 v200, vcc, 0, v200, s[38:39]
	v_addc_co_u32_e64 v200, vcc, 0, v200, s[40:41]
	s_cmp_le_u32 s16, 4
	s_cbranch_scc1 .Lidx_red
	v_cmp_ge_u32_e64 s[34:35], v96, v63
	v_cmp_ge_u32_e64 s[36:37], v97, v63
	v_cmp_ge_u32_e64 s[38:39], v98, v63
	v_addc_co_u32_e64 v200, vcc, 0, v200, s[34:35]
	v_cmp_ge_u32_e64 s[40:41], v99, v63
	v_addc_co_u32_e64 v200, vcc, 0, v200, s[36:37]
	v_cmp_ge_u32_e64 s[34:35], v100, v63
	v_addc_co_u32_e64 v200, vcc, 0, v200, s[38:39]
	v_cmp_ge_u32_e64 s[36:37], v101, v63
	v_addc_co_u32_e64 v200, vcc, 0, v200, s[40:41]
	v_cmp_ge_u32_e64 s[38:39], v102, v63
	v_addc_co_u32_e64 v200, vcc, 0, v200, s[34:35]
	v_cmp_ge_u32_e64 s[40:41], v103, v63
	v_addc_co_u32_e64 v200, vcc, 0, v200, s[36:37]
	v_addc_co_u32_e64 v200, vcc, 0, v200, s[38:39]
	v_addc_co_u32_e64 v200, vcc, 0, v200, s[40:41]
	s_cmp_le_u32 s16, 5
	s_cbranch_scc1 .Lidx_red
	v_cmp_ge_u32_e64 s[34:35], v104, v63
	v_cmp_ge_u32_e64 s[36:37], v105, v63
	v_cmp_ge_u32_e64 s[38:39], v106, v63
	v_addc_co_u32_e64 v200, vcc, 0, v200, s[34:35]
	v_cmp_ge_u32_e64 s[40:41], v107, v63
	v_addc_co_u32_e64 v200, vcc, 0, v200, s[36:37]
	v_cmp_ge_u32_e64 s[34:35], v108, v63
	v_addc_co_u32_e64 v200, vcc, 0, v200, s[38:39]
	v_cmp_ge_u32_e64 s[36:37], v109, v63
	v_addc_co_u32_e64 v200, vcc, 0, v200, s[40:41]
	v_cmp_ge_u32_e64 s[38:39], v110, v63
	v_addc_co_u32_e64 v200, vcc, 0, v200, s[34:35]
	v_cmp_ge_u32_e64 s[40:41], v111, v63
	v_addc_co_u32_e64 v200, vcc, 0, v200, s[36:37]
	v_addc_co_u32_e64 v200, vcc, 0, v200, s[38:39]
	v_addc_co_u32_e64 v200, vcc, 0, v200, s[40:41]
	s_cmp_le_u32 s16, 6
	s_cbranch_scc1 .Lidx_red
	v_cmp_ge_u32_e64 s[34:35], v112, v63
	v_cmp_ge_u32_e64 s[36:37], v113, v63
	v_cmp_ge_u32_e64 s[38:39], v114, v63
	v_addc_co_u32_e64 v200, vcc, 0, v200, s[34:35]
	v_cmp_ge_u32_e64 s[40:41], v115, v63
	v_addc_co_u32_e64 v200, vcc, 0, v200, s[36:37]
	v_cmp_ge_u32_e64 s[34:35], v116, v63
	v_addc_co_u32_e64 v200, vcc, 0, v200, s[38:39]
	v_cmp_ge_u32_e64 s[36:37], v117, v63
	v_addc_co_u32_e64 v200, vcc, 0, v200, s[40:41]
	v_cmp_ge_u32_e64 s[38:39], v118, v63
	v_addc_co_u32_e64 v200, vcc, 0, v200, s[34:35]
	v_cmp_ge_u32_e64 s[40:41], v119, v63
	v_addc_co_u32_e64 v200, vcc, 0, v200, s[36:37]
	v_addc_co_u32_e64 v200, vcc, 0, v200, s[38:39]
	v_addc_co_u32_e64 v200, vcc, 0, v200, s[40:41]
	s_cmp_le_u32 s16, 7
	s_cbranch_scc1 .Lidx_red
	v_cmp_ge_u32_e64 s[34:35], v120, v63
	v_cmp_ge_u32_e64 s[36:37], v121, v63
	v_cmp_ge_u32_e64 s[38:39], v122, v63
	v_addc_co_u32_e64 v200, vcc, 0, v200, s[34:35]
	v_cmp_ge_u32_e64 s[40:41], v123, v63
	v_addc_co_u32_e64 v200, vcc, 0, v200, s[36:37]
	v_cmp_ge_u32_e64 s[34:35], v124, v63
	v_addc_co_u32_e64 v200, vcc, 0, v200, s[38:39]
	v_cmp_ge_u32_e64 s[36:37], v125, v63
	v_addc_co_u32_e64 v200, vcc, 0, v200, s[40:41]
	v_cmp_ge_u32_e64 s[38:39], v126, v63
	v_addc_co_u32_e64 v200, vcc, 0, v200, s[34:35]
	v_cmp_ge_u32_e64 s[40:41], v127, v63
	v_addc_co_u32_e64 v200, vcc, 0, v200, s[36:37]
	v_addc_co_u32_e64 v200, vcc, 0, v200, s[38:39]
	v_addc_co_u32_e64 v200, vcc, 0, v200, s[40:41]
.Lidx_red:
	s_nop 1
	v_add_u32_dpp v200, v200, v200 quad_perm:[1,0,3,2] row_mask:0xf bank_mask:0xf
	s_nop 1
	v_add_u32_dpp v200, v200, v200 quad_perm:[2,3,0,1] row_mask:0xf bank_mask:0xf
	s_nop 1
	v_add_u32_dpp v200, v200, v200 row_half_mirror row_mask:0xf bank_mask:0xf
	s_nop 1
	v_add_u32_dpp v200, v200, v200 row_mirror row_mask:0xf bank_mask:0xf
	s_nop 1
	v_readlane_b32 s25, v200, 0
	v_readlane_b32 s26, v200, 16
	v_readlane_b32 s27, v200, 32
	v_readlane_b32 s28, v200, 48
	s_add_i32 s25, s25, s26
	s_add_i32 s27, s27, s28
	s_cmp_ge_u32 s25, 0x100
	s_cselect_b32 s42, -1, 0
	s_cmp_ge_u32 s27, 0x100
	s_cselect_b32 s43, -1, 0
	v_cndmask_b32_e64 v62, v62, v63, s[42:43]
	s_lshr_b32 s24, s24, 1
	s_cmp_lg_u32 s24, 0
	s_cbranch_scc1 .Lidx_step
	v_max_u32_e32 v62, 0x800000, v62
	s_nop 1
	v_cmp_ge_u32_e64 s[34:35], v64, v62
	v_cmp_ge_u32_e64 s[36:37], v65, v62
	s_nop 1
	v_writelane_b32 v205, s34, 0
	v_writelane_b32 v206, s35, 0
	v_cmp_ge_u32_e64 s[38:39], v66, v62
	v_writelane_b32 v205, s36, 1
	v_writelane_b32 v206, s37, 1
	v_cmp_ge_u32_e64 s[34:35], v67, v62
	v_writelane_b32 v205, s38, 2
	v_writelane_b32 v206, s39, 2
	v_cmp_ge_u32_e64 s[36:37], v68, v62
	v_writelane_b32 v205, s34, 3
	v_writelane_b32 v206, s35, 3
	v_cmp_ge_u32_e64 s[38:39], v69, v62
	v_writelane_b32 v205, s36, 4
	v_writelane_b32 v206, s37, 4
	v_cmp_ge_u32_e64 s[34:35], v70, v62
	v_writelane_b32 v205, s38, 5
	v_writelane_b32 v206, s39, 5
	v_cmp_ge_u32_e64 s[36:37], v71, v62
	v_writelane_b32 v205, s34, 6
	v_writelane_b32 v206, s35, 6
	v_cmp_ge_u32_e64 s[38:39], v72, v62
	v_writelane_b32 v205, s36, 7
	v_writelane_b32 v206, s37, 7
	v_cmp_ge_u32_e64 s[34:35], v73, v62
	v_writelane_b32 v205, s38, 8
	v_writelane_b32 v206, s39, 8
	v_cmp_ge_u32_e64 s[36:37], v74, v62
	v_writelane_b32 v205, s34, 9
	v_writelane_b32 v206, s35, 9
	v_cmp_ge_u32_e64 s[38:39], v75, v62
	v_writelane_b32 v205, s36, 10
	v_writelane_b32 v206, s37, 10
	v_cmp_ge_u32_e64 s[34:35], v76, v62
	v_writelane_b32 v205, s38, 11
	v_writelane_b32 v206, s39, 11
	v_cmp_ge_u32_e64 s[36:37], v77, v62
	v_writelane_b32 v205, s34, 12
	v_writelane_b32 v206, s35, 12
	v_cmp_ge_u32_e64 s[38:39], v78, v62
	v_writelane_b32 v205, s36, 13
	v_writelane_b32 v206, s37, 13
	v_cmp_ge_u32_e64 s[34:35], v79, v62
	v_writelane_b32 v205, s38, 14
	v_writelane_b32 v206, s39, 14
	v_cmp_ge_u32_e64 s[36:37], v80, v62
	v_writelane_b32 v205, s34, 15
	v_writelane_b32 v206, s35, 15
	v_cmp_ge_u32_e64 s[38:39], v81, v62
	v_writelane_b32 v205, s36, 16
	v_writelane_b32 v206, s37, 16
	v_cmp_ge_u32_e64 s[34:35], v82, v62
	v_writelane_b32 v205, s38, 17
	v_writelane_b32 v206, s39, 17
	v_cmp_ge_u32_e64 s[36:37], v83, v62
	v_writelane_b32 v205, s34, 18
	v_writelane_b32 v206, s35, 18
	v_cmp_ge_u32_e64 s[38:39], v84, v62
	v_writelane_b32 v205, s36, 19
	v_writelane_b32 v206, s37, 19
	v_cmp_ge_u32_e64 s[34:35], v85, v62
	v_writelane_b32 v205, s38, 20
	v_writelane_b32 v206, s39, 20
	v_cmp_ge_u32_e64 s[36:37], v86, v62
	v_writelane_b32 v205, s34, 21
	v_writelane_b32 v206, s35, 21
	v_cmp_ge_u32_e64 s[38:39], v87, v62
	v_writelane_b32 v205, s36, 22
	v_writelane_b32 v206, s37, 22
	v_cmp_ge_u32_e64 s[34:35], v88, v62
	v_writelane_b32 v205, s38, 23
	v_writelane_b32 v206, s39, 23
	v_cmp_ge_u32_e64 s[36:37], v89, v62
	v_writelane_b32 v205, s34, 24
	v_writelane_b32 v206, s35, 24
	v_cmp_ge_u32_e64 s[38:39], v90, v62
	v_writelane_b32 v205, s36, 25
	v_writelane_b32 v206, s37, 25
	v_cmp_ge_u32_e64 s[34:35], v91, v62
	v_writelane_b32 v205, s38, 26
	v_writelane_b32 v206, s39, 26
	v_cmp_ge_u32_e64 s[36:37], v92, v62
	v_writelane_b32 v205, s34, 27
	v_writelane_b32 v206, s35, 27
	v_cmp_ge_u32_e64 s[38:39], v93, v62
	v_writelane_b32 v205, s36, 28
	v_writelane_b32 v206, s37, 28
	v_cmp_ge_u32_e64 s[34:35], v94, v62
	v_writelane_b32 v205, s38, 29
	v_writelane_b32 v206, s39, 29
	v_cmp_ge_u32_e64 s[36:37], v95, v62
	v_writelane_b32 v205, s34, 30
	v_writelane_b32 v206, s35, 30
	v_cmp_ge_u32_e64 s[38:39], v96, v62
	v_writelane_b32 v205, s36, 31
	v_writelane_b32 v206, s37, 31
	v_cmp_ge_u32_e64 s[34:35], v97, v62
	v_writelane_b32 v205, s38, 32
	v_writelane_b32 v206, s39, 32
	v_cmp_ge_u32_e64 s[36:37], v98, v62
	v_writelane_b32 v205, s34, 33
	v_writelane_b32 v206, s35, 33
	v_cmp_ge_u32_e64 s[38:39], v99, v62
	v_writelane_b32 v205, s36, 34
	v_writelane_b32 v206, s37, 34
	v_cmp_ge_u32_e64 s[34:35], v100, v62
	v_writelane_b32 v205, s38, 35
	v_writelane_b32 v206, s39, 35
	v_cmp_ge_u32_e64 s[36:37], v101, v62
	v_writelane_b32 v205, s34, 36
	v_writelane_b32 v206, s35, 36
	v_cmp_ge_u32_e64 s[38:39], v102, v62
	v_writelane_b32 v205, s36, 37
	v_writelane_b32 v206, s37, 37
	v_cmp_ge_u32_e64 s[34:35], v103, v62
	v_writelane_b32 v205, s38, 38
	v_writelane_b32 v206, s39, 38
	v_cmp_ge_u32_e64 s[36:37], v104, v62
	v_writelane_b32 v205, s34, 39
	v_writelane_b32 v206, s35, 39
	v_cmp_ge_u32_e64 s[38:39], v105, v62
	v_writelane_b32 v205, s36, 40
	v_writelane_b32 v206, s37, 40
	v_cmp_ge_u32_e64 s[34:35], v106, v62
	v_writelane_b32 v205, s38, 41
	v_writelane_b32 v206, s39, 41
	v_cmp_ge_u32_e64 s[36:37], v107, v62
	v_writelane_b32 v205, s34, 42
	v_writelane_b32 v206, s35, 42
	v_cmp_ge_u32_e64 s[38:39], v108, v62
	v_writelane_b32 v205, s36, 43
	v_writelane_b32 v206, s37, 43
	v_cmp_ge_u32_e64 s[34:35], v109, v62
	v_writelane_b32 v205, s38, 44
	v_writelane_b32 v206, s39, 44
	v_cmp_ge_u32_e64 s[36:37], v110, v62
	v_writelane_b32 v205, s34, 45
	v_writelane_b32 v206, s35, 45
	v_cmp_ge_u32_e64 s[38:39], v111, v62
	v_writelane_b32 v205, s36, 46
	v_writelane_b32 v206, s37, 46
	v_cmp_ge_u32_e64 s[34:35], v112, v62
	v_writelane_b32 v205, s38, 47
	v_writelane_b32 v206, s39, 47
	v_cmp_ge_u32_e64 s[36:37], v113, v62
	v_writelane_b32 v205, s34, 48
	v_writelane_b32 v206, s35, 48
	v_cmp_ge_u32_e64 s[38:39], v114, v62
	v_writelane_b32 v205, s36, 49
	v_writelane_b32 v206, s37, 49
	v_cmp_ge_u32_e64 s[34:35], v115, v62
	v_writelane_b32 v205, s38, 50
	v_writelane_b32 v206, s39, 50
	v_cmp_ge_u32_e64 s[36:37], v116, v62
	v_writelane_b32 v205, s34, 51
	v_writelane_b32 v206, s35, 51
	v_cmp_ge_u32_e64 s[38:39], v117, v62
	v_writelane_b32 v205, s36, 52
	v_writelane_b32 v206, s37, 52
	v_cmp_ge_u32_e64 s[34:35], v118, v62
	v_writelane_b32 v205, s38, 53
	v_writelane_b32 v206, s39, 53
	v_cmp_ge_u32_e64 s[36:37], v119, v62
	v_writelane_b32 v205, s34, 54
	v_writelane_b32 v206, s35, 54
	v_cmp_ge_u32_e64 s[38:39], v120, v62
	v_writelane_b32 v205, s36, 55
	v_writelane_b32 v206, s37, 55
	v_cmp_ge_u32_e64 s[34:35], v121, v62
	v_writelane_b32 v205, s38, 56
	v_writelane_b32 v206, s39, 56
	v_cmp_ge_u32_e64 s[36:37], v122, v62
	v_writelane_b32 v205, s34, 57
	v_writelane_b32 v206, s35, 57
	v_cmp_ge_u32_e64 s[38:39], v123, v62
	v_writelane_b32 v205, s36, 58
	v_writelane_b32 v206, s37, 58
	v_cmp_ge_u32_e64 s[34:35], v124, v62
	v_writelane_b32 v205, s38, 59
	v_writelane_b32 v206, s39, 59
	v_cmp_ge_u32_e64 s[36:37], v125, v62
	v_writelane_b32 v205, s34, 60
	v_writelane_b32 v206, s35, 60
	v_cmp_ge_u32_e64 s[38:39], v126, v62
	v_writelane_b32 v205, s36, 61
	v_writelane_b32 v206, s37, 61
	v_cmp_ge_u32_e64 s[34:35], v127, v62
	v_writelane_b32 v205, s38, 62
	v_writelane_b32 v206, s39, 62
	v_writelane_b32 v205, s34, 63
	v_writelane_b32 v206, s35, 63
	s_nop 1
	global_store_dword v58, v205, s[22:23]
	global_store_dword v58, v206, s[22:23] offset:256
	v_readlane_b32 s17, v255, 40
	s_add_i32 s10, s10, 1
	s_add_i32 s81, s81, s17
	s_cmpk_gt_i32 s81, 0xfff
	s_cbranch_scc0 .Lidx_id
	s_branch .LBB0_937
